# combined micro-edits on top of conv-wait version: hyprep/pool load hoists, hyena order-0 filter load merge, post1 packed LayerNorm reductions
# speedup vs baseline: 1.0156x; 1.0107x over previous
; #define LAS __attribute__((address_space(3)))
; __device__ __forceinline__ void hyprep_unit(Ctx& C, int l, int uidx) {
;     ...
;     __syncthreads();
;     { u32x4 v[5];
; #pragma unroll
;         for (int i = 0; i < 5; ++i) { const int idx0 = C.tid + 512 * i, idx = idx0 < 66 * 32 ? idx0 : 66 * 32 - 1, r = idx >> 5, ch = idx & 31, t = t0 - 1 + r; const bool ok = t >= 0 && t < L;
;             const int tc = t < 0 ? 0 : (t < L ? t : L - 1);
;             v[i] = *(const u32x4*)(Z + (size_t)(rowbase + tc) * INW + 1280 + 256 * cb + 8 * ch); if (!ok) v[i] = (u32x4){0u, 0u, 0u, 0u}; }
; #pragma unroll
;         for (int i = 0; i < 5; ++i) { const int idx0 = C.tid + 512 * i, idx = idx0 < 66 * 32 ? idx0 : 66 * 32 - 1, r = idx >> 5, ch = idx & 31;
;             if (i < 4 || idx0 < 66 * 32) *(LAS u32x4*)(C.lds + r * RS + ch * 16) = v[i]; } }
;     __syncthreads();
;     const int c = C.tid & 255, hf = C.tid >> 8, ch = 256 * cb + c, comp = ch >> 9, cc = ch & 511;
;     const float w0 = INP(I_HCW)[(l * 3 + 0) * 1536 + ch], w1 = INP(I_HCW)[(l * 3 + 1) * 1536 + ch], w2 = INP(I_HCW)[(l * 3 + 2) * 1536 + ch], bias = INP(I_HCB)[l * 1536 + ch];
.LBB0_474:
	s_and_b32 s9, 0xffff, s8
	s_mul_i32 s9, s9, 0xaaab
	s_lshr_b32 s9, s9, 18
	s_mul_i32 s11, s9, 6
	s_lshl_b32 s14, s9, 6
	v_min_i32_e32 v2, 0x63f, v178
	s_sub_i32 s18, s8, s11
	s_load_dwordx2 s[44:45], s[56:57], 0x60
	v_and_b32_e32 v60, 0xff, v178
	v_lshl_or_b32 v60, s18, 8, v60
	v_and_b32_e32 v60, 0xffff, v60
	v_lshlrev_b32_e32 v60, 2, v60
	s_and_b32 s11, s14, 0xffc0
	v_add_u32_e32 v4, 0x200, v2
	s_add_i32 s11, s11, -1
	v_ashrrev_i32_e32 v26, 5, v4
	s_add_i32 s15, s12, -1
	v_add_u32_e32 v27, s11, v26
	v_min_i32_e32 v4, s15, v27
	v_cmp_lt_i32_e32 vcc, -1, v27
	v_mov_b64_e32 v[16:17], s[54:55]
	v_lshlrev_b32_e32 v2, 4, v2
	v_cndmask_b32_e32 v4, 0, v4, vcc
	v_add_u32_e32 v4, s10, v4
	v_mad_u64_u32 v[4:5], s[8:9], v4, s66, v[16:17]
	s_lshl_b32 s8, s18, 9
	s_and_b32 s38, s8, 0x1fe00
	v_lshl_add_u64 v[4:5], v[4:5], 0, s[38:39]
	v_and_b32_e32 v2, 0x1f0, v2
	v_min_i32_e32 v8, 0x43f, v178
	v_lshl_add_u64 v[4:5], v[4:5], 0, v[2:3]
	s_mov_b32 s19, 0x36000000
	v_add_u32_e32 v6, 0x400, v8
	v_add_co_u32_e32 v4, vcc, s19, v4
	v_ashrrev_i32_e32 v28, 5, v6
	s_nop 0
	v_addc_co_u32_e32 v5, vcc, 0, v5, vcc
	v_add_u32_e32 v29, s11, v28
	v_min_i32_e32 v6, s15, v29
	v_cmp_lt_i32_e32 vcc, -1, v29
	v_lshlrev_b32_e32 v8, 4, v8
	v_and_b32_e32 v20, 0x1f0, v8
	v_cndmask_b32_e32 v6, 0, v6, vcc
	v_add_u32_e32 v6, s10, v6
	v_mad_u64_u32 v[6:7], s[8:9], v6, s66, v[16:17]
	v_lshl_add_u64 v[6:7], v[6:7], 0, s[38:39]
	v_mov_b32_e32 v21, v3
	v_add_u32_e32 v58, 0x1000, v60
	v_add_u32_e32 v59, 0x3000, v60
	s_waitcnt lgkmcnt(0)
	global_load_dword v61, v60, s[44:45]
	global_load_dword v62, v58, s[44:45] offset:2048
	global_load_dword v63, v59, s[44:45]
	v_min_i32_e32 v14, 0x23f, v178
	v_lshl_add_u64 v[6:7], v[6:7], 0, v[20:21]
	v_add_u32_e32 v12, 0x600, v14
	v_add_co_u32_e32 v8, vcc, s19, v6
	v_ashrrev_i32_e32 v21, 5, v12
	s_nop 0
	v_addc_co_u32_e32 v9, vcc, 0, v7, vcc
	v_add_u32_e32 v30, s11, v21
	v_min_i32_e32 v12, s15, v30
	v_cmp_lt_i32_e32 vcc, -1, v30
	v_lshlrev_b32_e32 v14, 4, v14
	v_and_b32_e32 v22, 0x1f0, v14
	v_cndmask_b32_e32 v12, 0, v12, vcc
	v_add_u32_e32 v12, s10, v12
	v_mad_u64_u32 v[12:13], s[8:9], v12, s66, v[16:17]
	v_lshl_add_u64 v[12:13], v[12:13], 0, s[38:39]
	v_mov_b32_e32 v23, v3
	v_lshl_add_u64 v[12:13], v[12:13], 0, v[22:23]
	v_min_i32_e32 v18, 0x83f, v178
	v_add_co_u32_e32 v12, vcc, s19, v12
	v_ashrrev_i32_e32 v23, 5, v18
	s_nop 0
	v_addc_co_u32_e32 v13, vcc, 0, v13, vcc
	v_add_u32_e32 v31, s11, v23
	v_min_i32_e32 v19, s15, v31
	v_cmp_lt_i32_e32 vcc, -1, v31
	v_lshlrev_b32_e32 v18, 4, v18
	v_and_b32_e32 v24, 0x1f0, v18
	v_cndmask_b32_e32 v19, 0, v19, vcc
	v_add_u32_e32 v19, s10, v19
	v_mad_u64_u32 v[16:17], s[8:9], v19, s66, v[16:17]
	s_load_dwordx2 s[8:9], s[56:57], 0x68
	v_lshl_add_u64 v[16:17], v[16:17], 0, s[38:39]
	v_mov_b32_e32 v25, v3
	v_lshl_add_u64 v[16:17], v[16:17], 0, v[24:25]
	v_min_i32_e32 v52, 63, v178
	v_add_u32_e32 v53, 0x800, v52
	v_ashrrev_i32_e32 v53, 5, v53
	v_add_u32_e32 v56, s11, v53
	v_min_i32_e32 v53, s15, v56
	v_cmp_lt_i32_e32 vcc, -1, v56
	s_nop 1
	v_cndmask_b32_e32 v53, 0, v53, vcc
	v_add_u32_e32 v53, s10, v53
	v_mov_b64_e32 v[54:55], s[54:55]
	v_mad_u64_u32 v[54:55], vcc, v53, s66, v[54:55]
	v_lshlrev_b32_e32 v52, 4, v52
	v_lshl_add_u64 v[54:55], v[54:55], 0, s[38:39]
	v_and_b32_e32 v52, 0x1f0, v52
	v_mov_b32_e32 v53, v3
	v_lshl_add_u64 v[54:55], v[54:55], 0, v[52:53]
	v_add_co_u32_e32 v54, vcc, s19, v54
	s_nop 1
	v_addc_co_u32_e32 v55, vcc, 0, v55, vcc
	s_waitcnt lgkmcnt(0)
	global_load_dword v64, v60, s[8:9]
	s_barrier
	global_load_dwordx4 v[4:7], v[4:5], off offset:2560
	s_nop 0
	global_load_dwordx4 v[8:11], v[8:9], off offset:2560
	v_add_co_u32_e32 v16, vcc, s19, v16
	global_load_dwordx4 v[12:15], v[12:13], off offset:2560
	s_nop 0
	v_addc_co_u32_e32 v17, vcc, 0, v17, vcc
	global_load_dwordx4 v[16:19], v[16:17], off offset:2560
	global_load_dwordx4 v[66:69], v[54:55], off offset:2560
	v_cmp_gt_u32_e32 vcc, s12, v27
	v_mul_lo_u32 v23, v23, s36
	v_add3_u32 v23, 0, v23, v24
	s_mov_b32 s34, 0x36000000
	s_lshl_b32 s18, s18, 8
	s_waitcnt vmcnt(4)
	v_cndmask_b32_e32 v7, 0, v7, vcc
	v_cndmask_b32_e32 v6, 0, v6, vcc
	v_cndmask_b32_e32 v5, 0, v5, vcc
	v_cndmask_b32_e32 v4, 0, v4, vcc
	v_cmp_gt_u32_e32 vcc, s12, v29
	s_waitcnt vmcnt(3)
	s_nop 0
	v_cndmask_b32_e32 v11, 0, v11, vcc
	v_cndmask_b32_e32 v10, 0, v10, vcc
	v_cndmask_b32_e32 v9, 0, v9, vcc
	v_cndmask_b32_e32 v8, 0, v8, vcc
	v_cmp_gt_u32_e32 vcc, s12, v30
	s_waitcnt vmcnt(2)
	s_nop 0
	v_cndmask_b32_e32 v15, 0, v15, vcc
	v_cndmask_b32_e32 v14, 0, v14, vcc
	v_cndmask_b32_e32 v13, 0, v13, vcc
	v_cndmask_b32_e32 v12, 0, v12, vcc
	v_cmp_gt_u32_e32 vcc, s12, v31
	s_waitcnt vmcnt(1)
	s_nop 0
	v_cndmask_b32_e32 v19, 0, v19, vcc
	v_cndmask_b32_e32 v18, 0, v18, vcc
	v_cndmask_b32_e32 v17, 0, v17, vcc
	v_cndmask_b32_e32 v16, 0, v16, vcc
	ds_write_b128 v23, v[16:19]
	v_mul_lo_u32 v16, v26, s36
	v_add3_u32 v2, 0, v16, v2
	ds_write_b128 v2, v[4:7]
	v_mul_lo_u32 v2, v28, s36
	v_add3_u32 v2, 0, v2, v20
	ds_write_b128 v2, v[8:11]
	v_mul_lo_u32 v2, v21, s36
	v_add3_u32 v2, 0, v2, v22
	v_cmp_gt_i32_e32 vcc, 64, v178
	ds_write_b128 v2, v[12:15]
	s_and_saveexec_b64 s[8:9], vcc
	s_cbranch_execz .LBB0_476
	v_add_u32_e32 v2, 0x800, v178
	v_cmp_gt_u32_e32 vcc, s12, v56
	v_ashrrev_i32_e32 v2, 5, v2
	v_lshlrev_b32_e32 v8, 4, v178
	v_mul_lo_u32 v2, v2, s36
	v_and_b32_e32 v8, 0x1f0, v8
	v_add3_u32 v2, 0, v2, v8
	s_waitcnt vmcnt(0)
	v_cndmask_b32_e32 v69, 0, v69, vcc
	v_cndmask_b32_e32 v68, 0, v68, vcc
	v_cndmask_b32_e32 v67, 0, v67, vcc
	v_cndmask_b32_e32 v66, 0, v66, vcc
	ds_write_b128 v2, v[66:69]
; #define LAS __attribute__((address_space(3)))
; __device__ __forceinline__ unsigned pk2(float lo, float hi) { f32x2 v = {lo, hi}; bf16x2_t b = __builtin_convertvector(v, bf16x2_t); return __builtin_bit_cast(unsigned, b); }
; __device__ __forceinline__ float bf1(bf16 v) { return __uint_as_float(((unsigned)v) << 16); }
; __device__ __forceinline__ void hyprep_unit(Ctx& C, int l, int uidx) {
;     ...
;     const int c = C.tid & 255, hf = C.tid >> 8, ch = 256 * cb + c, comp = ch >> 9, cc = ch & 511;
;     const float w0 = INP(I_HCW)[(l * 3 + 0) * 1536 + ch], w1 = INP(I_HCW)[(l * 3 + 1) * 1536 + ch], w2 = INP(I_HCW)[(l * 3 + 2) * 1536 + ch], bias = INP(I_HCB)[l * 1536 + ch];
;     bf16* dst = T + ((size_t)(comp * 512 + cc) * 4 + seq) * L + t0 + 32 * hf;
;     float zm = bf1(*(const LAS bf16*)(C.lds + (32 * hf) * RS + c * 2)), zc = bf1(*(const LAS bf16*)(C.lds + (32 * hf + 1) * RS + c * 2));
; #pragma unroll
;     for (int k = 0; k < 4; ++k) { float o[8];
; #pragma unroll
;         for (int e = 0; e < 8; ++e) { const float zn = bf1(*(const LAS bf16*)(C.lds + (32 * hf + 8 * k + e + 2) * RS + c * 2)); o[e] = bias + w0 * zm + w1 * zc + w2 * zn; zm = zc; zc = zn; }
;         u32x4 w; w.x = pk2(o[0], o[1]); w.y = pk2(o[2], o[3]); w.z = pk2(o[4], o[5]); w.w = pk2(o[6], o[7]); *(u32x4*)(dst + 8 * k) = w; }
.LBB0_476:
	s_or_b64 exec, exec, s[8:9]
	s_waitcnt vmcnt(0) lgkmcnt(0)
	s_barrier
	s_add_u32 s6, s54, s6
	s_addc_u32 s7, s55, s7
	s_and_b32 s15, 0xffff, s18
	v_or_b32_sdwa v2, v178, s15 dst_sel:DWORD dst_unused:UNUSED_PAD src0_sel:BYTE_0 src1_sel:DWORD
	v_lshlrev_b32_e32 v2, 2, v2
	v_mov_b32_e32 v8, v61
	v_mov_b32_e32 v10, v64
	v_mov_b32_e32 v12, v62
	v_mov_b32_e32 v14, v63
	v_ashrrev_i32_e32 v9, 3, v178
	v_and_b32_e32 v4, 0xffffffe0, v9
	v_add_u32_e32 v2, s13, v2
	v_lshlrev_b32_sdwa v11, v169, v178 dst_sel:DWORD dst_unused:UNUSED_PAD src0_sel:DWORD src1_sel:BYTE_0
	s_and_b32 s8, 0xffff, s14
	v_mul_lo_u32 v6, v4, s36
	v_mul_u32_u24_e32 v2, s12, v2
	s_lshl_b32 s38, s8, 1
	v_add3_u32 v13, 0, v6, v11
	v_lshl_add_u64 v[6:7], v[2:3], 1, s[6:7]
	v_ashrrev_i32_e32 v5, 31, v4
	ds_read_u16 v15, v13 offset:4752
	ds_read_u16 v38, v13 offset:7392
	ds_read_u16 v39, v13 offset:7920
	ds_read_u16 v40, v13 offset:6336
	ds_read_u16 v41, v13 offset:6864
	ds_read_u16 v42, v13 offset:5280
	ds_read_u16 v43, v13 offset:5808
	ds_read_u16 v18, v13 offset:4224
	ds_read_u16 v19, v13 offset:3168
	ds_read_u16 v21, v13 offset:3696
	ds_read_u16 v22, v13 offset:2112
	ds_read_u16 v23, v13 offset:2640
	ds_read_u16 v24, v13 offset:1056
	ds_read_u16 v25, v13 offset:1584
	ds_read_u16 v26, v13
	ds_read_u16 v27, v13 offset:528
	ds_read_u16 v44, v13 offset:8976
	ds_read_u16 v45, v13 offset:11616
	ds_read_u16 v46, v13 offset:12144
	ds_read_u16 v47, v13 offset:10560
	ds_read_u16 v48, v13 offset:11088
	ds_read_u16 v49, v13 offset:9504
	ds_read_u16 v50, v13 offset:10032
	ds_read_u16 v51, v13 offset:8448
	v_lshl_add_u64 v[6:7], v[6:7], 0, s[38:39]
	v_lshl_add_u64 v[16:17], v[4:5], 1, v[6:7]
	s_waitcnt lgkmcnt(14)
	v_lshlrev_b32_e32 v4, 16, v19
	v_lshlrev_b32_e32 v20, 16, v18
	v_lshlrev_b32_e32 v5, 16, v21
	s_waitcnt lgkmcnt(12)
	v_lshlrev_b32_e32 v7, 16, v23
	v_lshlrev_b32_e32 v6, 16, v22
	s_waitcnt lgkmcnt(10)
	v_lshlrev_b32_e32 v19, 16, v25
	v_lshlrev_b32_e32 v18, 16, v24
	s_waitcnt lgkmcnt(8)
	v_lshlrev_b32_e32 v23, 16, v27
	v_lshlrev_b32_e32 v22, 16, v26
	v_mov_b32_e32 v24, v5
	v_mov_b32_e32 v25, v20
	v_pk_mov_b32 v[26:27], v[22:23], v[18:19] op_sel:[1,0]
	v_pk_mov_b32 v[28:29], v[18:19], v[6:7] op_sel:[1,0]
	v_lshlrev_b32_e32 v21, 16, v15
	v_pk_mov_b32 v[30:31], v[6:7], v[4:5] op_sel:[1,0]
	s_mov_b64 s[6:7], 0
	s_waitcnt vmcnt(2)
	v_pk_fma_f32 v[22:23], v[8:9], v[22:23], v[10:11] op_sel_hi:[0,1,0]
	v_pk_fma_f32 v[32:33], v[8:9], v[18:19], v[10:11] op_sel_hi:[0,1,0]
	v_pk_fma_f32 v[36:37], v[8:9], v[4:5], v[10:11] op_sel_hi:[0,1,0]
	v_pk_fma_f32 v[34:35], v[8:9], v[6:7], v[10:11] op_sel_hi:[0,1,0]
	s_waitcnt vmcnt(1)
	v_pk_fma_f32 v[22:23], v[12:13], v[26:27], v[22:23] op_sel_hi:[0,1,1]
	v_pk_fma_f32 v[26:27], v[12:13], v[28:29], v[32:33] op_sel_hi:[0,1,1]
	v_pk_fma_f32 v[24:25], v[12:13], v[24:25], v[36:37] op_sel_hi:[0,1,1]
	v_pk_fma_f32 v[28:29], v[12:13], v[30:31], v[34:35] op_sel_hi:[0,1,1]
	s_waitcnt vmcnt(0)
	v_pk_fma_f32 v[6:7], v[14:15], v[6:7], v[26:27] op_sel_hi:[0,1,1]
	v_pk_fma_f32 v[24:25], v[14:15], v[20:21], v[24:25] op_sel_hi:[0,1,1]
	v_pk_fma_f32 v[18:19], v[14:15], v[18:19], v[22:23] op_sel_hi:[0,1,1]
	v_pk_fma_f32 v[22:23], v[14:15], v[4:5], v[28:29] op_sel_hi:[0,1,1]
	v_cvt_pk_bf16_f32 v5, v6, v7
	v_cvt_pk_bf16_f32 v7, v24, v25
	v_lshlrev_b32_e32 v25, 16, v43
	v_lshlrev_b32_e32 v24, 16, v42
	v_cvt_pk_bf16_f32 v4, v18, v19
	v_cvt_pk_bf16_f32 v6, v22, v23
	v_pk_fma_f32 v[26:27], v[8:9], v[20:21], v[10:11] op_sel_hi:[0,1,0]
	v_pk_mov_b32 v[20:21], v[20:21], v[24:25] op_sel:[1,0]
	global_store_dwordx4 v[16:17], v[4:7], off
	v_pk_fma_f32 v[20:21], v[12:13], v[20:21], v[26:27] op_sel_hi:[0,1,1]
	v_pk_fma_f32 v[26:27], v[14:15], v[24:25], v[20:21] op_sel_hi:[0,1,1]
	v_lshlrev_b32_e32 v7, 16, v41
	v_lshlrev_b32_e32 v6, 16, v40
	v_pk_fma_f32 v[20:21], v[8:9], v[24:25], v[10:11] op_sel_hi:[0,1,0]
	v_pk_mov_b32 v[24:25], v[24:25], v[6:7] op_sel:[1,0]
	v_lshlrev_b32_e32 v4, 16, v38
	v_lshlrev_b32_e32 v5, 16, v39
	v_pk_fma_f32 v[20:21], v[12:13], v[24:25], v[20:21] op_sel_hi:[0,1,1]
	v_pk_fma_f32 v[24:25], v[14:15], v[6:7], v[20:21] op_sel_hi:[0,1,1]
	v_pk_fma_f32 v[20:21], v[8:9], v[6:7], v[10:11] op_sel_hi:[0,1,0]
	v_pk_mov_b32 v[6:7], v[6:7], v[4:5] op_sel:[1,0]
	s_waitcnt lgkmcnt(0)
	v_lshlrev_b32_e32 v18, 16, v51
	v_pk_fma_f32 v[6:7], v[12:13], v[6:7], v[20:21] op_sel_hi:[0,1,1]
	v_mov_b32_e32 v22, v5
	v_mov_b32_e32 v23, v18
	v_pk_fma_f32 v[6:7], v[14:15], v[4:5], v[6:7] op_sel_hi:[0,1,1]
	v_pk_fma_f32 v[4:5], v[8:9], v[4:5], v[10:11] op_sel_hi:[0,1,0]
	v_lshlrev_b32_e32 v19, 16, v44
	v_pk_fma_f32 v[4:5], v[12:13], v[22:23], v[4:5] op_sel_hi:[0,1,1]
	v_pk_fma_f32 v[20:21], v[14:15], v[18:19], v[4:5] op_sel_hi:[0,1,1]
	ds_read_u16 v2, v13 offset:13200
	ds_read_u16 v15, v13 offset:15840
	ds_read_u16 v28, v13 offset:16368
	ds_read_u16 v29, v13 offset:14784
	ds_read_u16 v30, v13 offset:15312
	ds_read_u16 v31, v13 offset:13728
	ds_read_u16 v32, v13 offset:14256
	ds_read_u16 v22, v13 offset:12672
	v_cvt_pk_bf16_f32 v5, v24, v25
	v_lshlrev_b32_e32 v25, 16, v50
	v_lshlrev_b32_e32 v24, 16, v49
	v_cvt_pk_bf16_f32 v4, v26, v27
	v_pk_fma_f32 v[26:27], v[8:9], v[18:19], v[10:11] op_sel_hi:[0,1,0]
	v_pk_mov_b32 v[18:19], v[18:19], v[24:25] op_sel:[1,0]
	v_cvt_pk_bf16_f32 v6, v6, v7
	v_cvt_pk_bf16_f32 v7, v20, v21
	s_waitcnt lgkmcnt(0)
; #define LAS __attribute__((address_space(3)))
; __device__ __forceinline__ unsigned pk2(float lo, float hi) { f32x2 v = {lo, hi}; bf16x2_t b = __builtin_convertvector(v, bf16x2_t); return __builtin_bit_cast(unsigned, b); }
; __device__ __forceinline__ float bf1(bf16 v) { return __uint_as_float(((unsigned)v) << 16); }
; __device__ __forceinline__ void hyprep_unit(Ctx& C, int l, int uidx) {
;     ...
;     for (int k = 0; k < 4; ++k) { float o[8];
; #pragma unroll
;         for (int e = 0; e < 8; ++e) { const float zn = bf1(*(const LAS bf16*)(C.lds + (32 * hf + 8 * k + e + 2) * RS + c * 2)); o[e] = bias + w0 * zm + w1 * zc + w2 * zn; zm = zc; zc = zn; }
;         u32x4 w; w.x = pk2(o[0], o[1]); w.y = pk2(o[2], o[3]); w.z = pk2(o[4], o[5]); w.w = pk2(o[6], o[7]); *(u32x4*)(dst + 8 * k) = w; }
	v_lshlrev_b32_e32 v20, 16, v22
	v_lshlrev_b32_e32 v23, 16, v48
	v_lshlrev_b32_e32 v22, 16, v47
	v_pk_fma_f32 v[18:19], v[12:13], v[18:19], v[26:27] op_sel_hi:[0,1,1]
	v_pk_fma_f32 v[18:19], v[14:15], v[24:25], v[18:19] op_sel_hi:[0,1,1]
	v_pk_fma_f32 v[26:27], v[8:9], v[24:25], v[10:11] op_sel_hi:[0,1,0]
	v_pk_mov_b32 v[24:25], v[24:25], v[22:23] op_sel:[1,0]
	global_store_dwordx4 v[16:17], v[4:7], off offset:16
	v_lshlrev_b32_e32 v21, 16, v2
	v_pk_fma_f32 v[24:25], v[12:13], v[24:25], v[26:27] op_sel_hi:[0,1,1]
	v_lshlrev_b32_e32 v4, 16, v45
	v_lshlrev_b32_e32 v5, 16, v46
	v_or_b32_e32 v2, 31, v9
	v_pk_fma_f32 v[24:25], v[14:15], v[22:23], v[24:25] op_sel_hi:[0,1,1]
	v_pk_fma_f32 v[26:27], v[8:9], v[22:23], v[10:11] op_sel_hi:[0,1,0]
	v_pk_mov_b32 v[22:23], v[22:23], v[4:5] op_sel:[1,0]
	v_mul_lo_u32 v2, v2, s36
	v_pk_fma_f32 v[22:23], v[12:13], v[22:23], v[26:27] op_sel_hi:[0,1,1]
	v_add3_u32 v2, 0, v2, v11
	v_mov_b32_e32 v6, v5
	v_pk_fma_f32 v[22:23], v[14:15], v[4:5], v[22:23] op_sel_hi:[0,1,1]
	v_pk_fma_f32 v[4:5], v[8:9], v[4:5], v[10:11] op_sel_hi:[0,1,0]
	ds_read_u16 v9, v13 offset:16896
	ds_read_u16 v2, v2 offset:1056
	v_mov_b32_e32 v7, v20
	v_pk_fma_f32 v[4:5], v[12:13], v[6:7], v[4:5] op_sel_hi:[0,1,1]
	v_pk_fma_f32 v[26:27], v[14:15], v[20:21], v[4:5] op_sel_hi:[0,1,1]
	v_cvt_pk_bf16_f32 v5, v24, v25
	v_lshlrev_b32_e32 v25, 16, v32
	v_lshlrev_b32_e32 v24, 16, v31
	v_cvt_pk_bf16_f32 v7, v26, v27
	s_waitcnt lgkmcnt(1)
	v_pk_fma_f32 v[26:27], v[8:9], v[20:21], v[10:11] op_sel_hi:[0,1,0]
	v_pk_mov_b32 v[20:21], v[20:21], v[24:25] op_sel:[1,0]
	v_cvt_pk_bf16_f32 v6, v22, v23
	v_lshlrev_b32_e32 v23, 16, v30
	v_lshlrev_b32_e32 v22, 16, v29
	v_pk_fma_f32 v[20:21], v[12:13], v[20:21], v[26:27] op_sel_hi:[0,1,1]
	v_cvt_pk_bf16_f32 v4, v18, v19
	v_pk_fma_f32 v[20:21], v[14:15], v[24:25], v[20:21] op_sel_hi:[0,1,1]
	v_pk_fma_f32 v[26:27], v[8:9], v[24:25], v[10:11] op_sel_hi:[0,1,0]
	v_pk_mov_b32 v[24:25], v[24:25], v[22:23] op_sel:[1,0]
	global_store_dwordx4 v[16:17], v[4:7], off offset:32
	v_pk_fma_f32 v[24:25], v[12:13], v[24:25], v[26:27] op_sel_hi:[0,1,1]
	v_pk_fma_f32 v[24:25], v[14:15], v[22:23], v[24:25] op_sel_hi:[0,1,1]
	v_lshlrev_b32_e32 v4, 16, v15
	v_lshlrev_b32_e32 v5, 16, v28
	v_pk_fma_f32 v[26:27], v[8:9], v[22:23], v[10:11] op_sel_hi:[0,1,0]
	v_pk_mov_b32 v[22:23], v[22:23], v[4:5] op_sel:[1,0]
	v_lshlrev_b32_e32 v19, 16, v9
	v_pk_fma_f32 v[22:23], v[12:13], v[22:23], v[26:27] op_sel_hi:[0,1,1]
	v_mov_b32_e32 v18, v5
	v_pk_fma_f32 v[22:23], v[14:15], v[4:5], v[22:23] op_sel_hi:[0,1,1]
	v_pk_fma_f32 v[4:5], v[8:9], v[4:5], v[10:11] op_sel_hi:[0,1,0]
	s_waitcnt lgkmcnt(0)
	v_lshlrev_b32_e32 v7, 16, v2
	v_mov_b32_e32 v6, v19
	v_pk_fma_f32 v[4:5], v[12:13], v[18:19], v[4:5] op_sel_hi:[0,1,1]
	v_pk_fma_f32 v[8:9], v[14:15], v[6:7], v[4:5] op_sel_hi:[0,1,1]
	v_cvt_pk_bf16_f32 v4, v20, v21
	v_cvt_pk_bf16_f32 v5, v24, v25
	v_cvt_pk_bf16_f32 v6, v22, v23
	v_cvt_pk_bf16_f32 v7, v8, v9
	global_store_dwordx4 v[16:17], v[4:7], off offset:48
; #define LAS __attribute__((address_space(3)))
; #define MFMA32(a, b, c) __builtin_amdgcn_mfma_f32_32x32x16_bf16((a), (b), (c), 0, 0, 0)
; __device__ __forceinline__ void pool_unit(Ctx& C, int l, int blk) {
;     ...
;     __syncthreads();
;     { u32x4 v[6];
; #pragma unroll
;         for (int i = 0; i < 6; ++i) { const int idx = C.tid + 512 * i, r = idx >> 6, ch = idx & 63, t = t0 - 8 + r; const bool ok = t >= 0 && t < L; const int tc = t < 0 ? 0 : (t < L ? t : L - 1);
;             v[i] = *(const u32x4*)(Z + (size_t)(s0 + tc) * INW + 8 * ch); if (!ok) v[i] = (u32x4){0u, 0u, 0u, 0u}; }
; #pragma unroll
;         for (int i = 0; i < 6; ++i) { const int idx = C.tid + 512 * i, r = idx >> 6, ch = idx & 63; *(LAS u32x4*)(C.lds + r * RS + ch * 16) = v[i]; } }
;     __syncthreads();
;     ...
;     const bf16* wt = WSP(bf16, WS_POOLWT) + (size_t)((l * 4 + gi) * 128 + 64 * oh + r32) * 128 + 8 * h;
; #pragma unroll
;     for (int s = 0; s < 8; ++s) {
;         const bf16x8 Bf = *(const LAS bf16x8*)(C.lds + DT_OFF + r32 * RS + (128 * gi + 16 * s + 8 * h) * 2);
; #pragma unroll
;         for (int rb = 0; rb < 2; ++rb) { const bf16x8 Af = *(const bf16x8*)(wt + (size_t)(32 * rb) * 128 + 16 * s); acc[rb] = MFMA32(Af, Bf, acc[rb]); }
.LBB0_477:
	s_and_b64 vcc, exec, s[6:7]
	s_cbranch_vccz .LBB0_485
	s_add_i32 s6, s43, 0xfffffdd0
	s_lshl_b32 s10, s6, 5
	s_cmpk_lt_u32 s6, 0x200
	s_movk_i32 s6, 0x100
	s_cselect_b32 s11, 0x1000, s6
	s_movk_i32 s6, 0x7f00
	s_cselect_b32 s6, 0x3000, s6
	s_and_b32 s12, s6, s10
	s_sub_i32 s13, s10, s12
	v_lshlrev_b32_e32 v2, 4, v178
	s_add_i32 s8, s13, -8
	v_and_b32_e32 v2, 0x3f0, v2
	v_ashrrev_i32_e32 v28, 6, v178
	v_add_u32_e32 v6, 0x200, v178
	s_add_i32 s9, s11, -1
	v_lshl_add_u64 v[4:5], s[54:55], 0, v[2:3]
	s_mov_b64 s[6:7], 0x36000000
	v_add_u32_e32 v29, s8, v28
	v_ashrrev_i32_e32 v30, 6, v6
	v_lshl_add_u64 v[24:25], v[4:5], 0, s[6:7]
	v_min_i32_e32 v4, s9, v29
	v_cmp_lt_i32_e32 vcc, -1, v29
	v_add_u32_e32 v31, s8, v30
	v_min_i32_e32 v6, s9, v31
	v_cndmask_b32_e32 v4, 0, v4, vcc
	v_cmp_lt_i32_e32 vcc, -1, v31
	v_add_u32_e32 v12, 0x400, v178
	v_ashrrev_i32_e32 v32, 6, v12
	v_cndmask_b32_e32 v6, 0, v6, vcc
	v_add_u32_e32 v14, 0x600, v178
	v_add_u32_e32 v4, s12, v4
	v_add_u32_e32 v6, s12, v6
	v_add_u32_e32 v33, s8, v32
	v_ashrrev_i32_e32 v34, 6, v14
	v_mad_u64_u32 v[4:5], s[6:7], v4, s66, v[24:25]
	v_mad_u64_u32 v[8:9], s[6:7], v6, s66, v[24:25]
	v_min_i32_e32 v12, s9, v33
	v_cmp_lt_i32_e32 vcc, -1, v33
	v_add_u32_e32 v35, s8, v34
	s_waitcnt lgkmcnt(0)
	s_barrier
	global_load_dwordx4 v[4:7], v[4:5], off
	s_nop 0
	global_load_dwordx4 v[8:11], v[8:9], off
	v_cndmask_b32_e32 v12, 0, v12, vcc
	v_min_i32_e32 v14, s9, v35
	v_cmp_lt_i32_e32 vcc, -1, v35
	v_add_u32_e32 v20, 0x800, v178
	v_ashrrev_i32_e32 v36, 6, v20
	v_cndmask_b32_e32 v14, 0, v14, vcc
	v_add_u32_e32 v12, s12, v12
	v_add_u32_e32 v14, s12, v14
	v_add_u32_e32 v37, s8, v36
	v_add_u32_e32 v26, 0xa00, v178
	v_mad_u64_u32 v[12:13], s[6:7], v12, s66, v[24:25]
	v_mad_u64_u32 v[16:17], s[6:7], v14, s66, v[24:25]
	v_min_i32_e32 v20, s9, v37
	v_cmp_lt_i32_e32 vcc, -1, v37
	v_ashrrev_i32_e32 v38, 6, v26
	global_load_dwordx4 v[12:15], v[12:13], off
	s_nop 0
	global_load_dwordx4 v[16:19], v[16:17], off
	v_cndmask_b32_e32 v20, 0, v20, vcc
	v_add_u32_e32 v39, s8, v38
	v_add_u32_e32 v20, s12, v20
	v_min_i32_e32 v26, s9, v39
	v_cmp_lt_i32_e32 vcc, -1, v39
	v_mad_u64_u32 v[20:21], s[6:7], v20, s66, v[24:25]
	s_nop 0
	v_cndmask_b32_e32 v26, 0, v26, vcc
	global_load_dwordx4 v[20:23], v[20:21], off
	v_add_u32_e32 v26, s12, v26
	v_mad_u64_u32 v[24:25], s[6:7], v26, s66, v[24:25]
	global_load_dwordx4 v[24:27], v[24:25], off
	v_cmp_gt_u32_e32 vcc, s11, v29
	v_mul_lo_u32 v28, v28, s71
	v_add3_u32 v28, 0, v28, v2
	s_mul_i32 s6, s43, 0x8200
	s_mov_b32 s14, 0
	s_waitcnt vmcnt(5)
	v_cndmask_b32_e32 v7, 0, v7, vcc
	v_cndmask_b32_e32 v6, 0, v6, vcc
	v_cndmask_b32_e32 v5, 0, v5, vcc
	v_cndmask_b32_e32 v4, 0, v4, vcc
	v_cmp_gt_u32_e32 vcc, s11, v31
	ds_write_b128 v28, v[4:7]
	v_mul_lo_u32 v4, v30, s71
	s_waitcnt vmcnt(4)
	v_cndmask_b32_e32 v11, 0, v11, vcc
	v_cndmask_b32_e32 v10, 0, v10, vcc
	v_cndmask_b32_e32 v9, 0, v9, vcc
	v_cndmask_b32_e32 v8, 0, v8, vcc
	v_add3_u32 v4, 0, v4, v2
	v_cmp_gt_u32_e32 vcc, s11, v33
	ds_write_b128 v4, v[8:11]
	v_mul_lo_u32 v4, v32, s71
	v_add3_u32 v4, 0, v4, v2
	s_waitcnt vmcnt(3)
	v_cndmask_b32_e32 v15, 0, v15, vcc
	v_cndmask_b32_e32 v14, 0, v14, vcc
	v_cndmask_b32_e32 v13, 0, v13, vcc
	v_cndmask_b32_e32 v12, 0, v12, vcc
	v_cmp_gt_u32_e32 vcc, s11, v35
	ds_write_b128 v4, v[12:15]
	v_mul_lo_u32 v4, v34, s71
	s_waitcnt vmcnt(2)
	v_cndmask_b32_e32 v19, 0, v19, vcc
	v_cndmask_b32_e32 v18, 0, v18, vcc
	v_cndmask_b32_e32 v17, 0, v17, vcc
	v_cndmask_b32_e32 v16, 0, v16, vcc
	v_add3_u32 v4, 0, v4, v2
	v_cmp_gt_u32_e32 vcc, s11, v37
	ds_write_b128 v4, v[16:19]
	v_mul_lo_u32 v4, v36, s71
	s_waitcnt vmcnt(1)
	v_cndmask_b32_e32 v23, 0, v23, vcc
	v_cndmask_b32_e32 v22, 0, v22, vcc
	v_cndmask_b32_e32 v21, 0, v21, vcc
	v_cndmask_b32_e32 v20, 0, v20, vcc
	v_add3_u32 v4, 0, v4, v2
	v_cmp_gt_u32_e32 vcc, s11, v39
	ds_write_b128 v4, v[20:23]
	v_mul_lo_u32 v4, v38, s71
	s_waitcnt vmcnt(0)
	v_cndmask_b32_e32 v27, 0, v27, vcc
	v_cndmask_b32_e32 v26, 0, v26, vcc
	v_cndmask_b32_e32 v25, 0, v25, vcc
	v_cndmask_b32_e32 v24, 0, v24, vcc
	v_add3_u32 v2, 0, v4, v2
	ds_write_b128 v2, v[24:27]
	v_lshrrev_b32_e32 v2, 4, v162
	v_lshlrev_b32_e64 v5, v2, 1
	v_ashrrev_i32_e32 v2, 4, v178
	v_lshlrev_b32_e32 v4, 4, v162
	v_and_b32_e32 v16, -4, v2
	v_add_u32_e32 v2, 0, v4
	v_subrev_u32_e32 v4, s6, v4
	v_readlane_b32 s6, v242, 9
	s_waitcnt lgkmcnt(0)
	s_barrier
	v_and_b32_e32 v128, 0xffffffdf, v178
	v_lshlrev_b32_e32 v128, 8, v128
	v_lshrrev_b32_e32 v129, 5, v162
	v_lshl_add_u32 v128, v129, 4, v128
	v_mov_b32_e32 v129, v3
	v_lshl_add_u64 v[128:129], s[54:55], 0, v[128:129]
	v_add_co_u32_e32 v130, vcc, 0x300000, v128
	s_nop 1
	v_addc_co_u32_e32 v131, vcc, 0, v129, vcc
	v_add_co_u32_e32 v132, vcc, 0x302000, v128
	s_nop 1
	v_addc_co_u32_e32 v133, vcc, 0, v129, vcc
	global_load_dwordx4 v[64:67], v[130:131], off
	global_load_dwordx4 v[68:71], v[132:133], off
	global_load_dwordx4 v[72:75], v[130:131], off offset:32
	global_load_dwordx4 v[76:79], v[132:133], off offset:32
	global_load_dwordx4 v[80:83], v[130:131], off offset:64
	global_load_dwordx4 v[84:87], v[132:133], off offset:64
	global_load_dwordx4 v[88:91], v[130:131], off offset:96
	global_load_dwordx4 v[92:95], v[132:133], off offset:96
	global_load_dwordx4 v[96:99], v[130:131], off offset:128
	global_load_dwordx4 v[100:103], v[132:133], off offset:128
	global_load_dwordx4 v[104:107], v[130:131], off offset:160
	global_load_dwordx4 v[108:111], v[132:133], off offset:160
	global_load_dwordx4 v[112:115], v[130:131], off offset:192
	global_load_dwordx4 v[116:119], v[132:133], off offset:192
	global_load_dwordx4 v[120:123], v[130:131], off offset:224
	global_load_dwordx4 v[124:127], v[132:133], off offset:224
	v_add_u32_e32 v4, s6, v4
	s_lshl_b32 s6, s43, 5
	s_addk_i32 s6, 0xba00
	v_add_u32_e32 v6, s6, v16
	v_subrev_u32_e32 v6, s12, v6
	v_sub_u32_e32 v17, v6, v5
	s_branch .LBB0_480

; #define LAS __attribute__((address_space(3)))
; __device__ __forceinline__ unsigned pk2(float lo, float hi) { f32x2 v = {lo, hi}; bf16x2_t b = __builtin_convertvector(v, bf16x2_t); return __builtin_bit_cast(unsigned, b); }
; #define MFMA32(a, b, c) __builtin_amdgcn_mfma_f32_32x32x16_bf16((a), (b), (c), 0, 0, 0)
; __device__ __forceinline__ void pool_unit(Ctx& C, int l, int blk) {
;     ...
;     const int gi = C.wave >> 1, oh = C.wave & 1, r32 = C.lane & 31, h = C.lane >> 5;
;     f32x16 acc[2];
; #pragma unroll
;     for (int a = 0; a < 2; ++a)
; #pragma unroll
;         for (int i = 0; i < 16; ++i) acc[a][i] = 0.f;
;     const bf16* wt = WSP(bf16, WS_POOLWT) + (size_t)((l * 4 + gi) * 128 + 64 * oh + r32) * 128 + 8 * h;
; #pragma unroll
;     for (int s = 0; s < 8; ++s) {
;         const bf16x8 Bf = *(const LAS bf16x8*)(C.lds + DT_OFF + r32 * RS + (128 * gi + 16 * s + 8 * h) * 2);
; #pragma unroll
;         for (int rb = 0; rb < 2; ++rb) { const bf16x8 Af = *(const bf16x8*)(wt + (size_t)(32 * rb) * 128 + 16 * s); acc[rb] = MFMA32(Af, Bf, acc[rb]); }
;     }
;     bf16* yp = WSP(bf16, WS_YCAT) + (size_t)(row0 + r32) * DM + 128 * gi + 64 * oh;
; #pragma unroll
;     for (int rb = 0; rb < 2; ++rb)
; #pragma unroll
;         for (int rg = 0; rg < 4; ++rg) { u32x2 w; w.x = pk2(acc[rb][4 * rg], acc[rb][4 * rg + 1]); w.y = pk2(acc[rb][4 * rg + 2], acc[rb][4 * rg + 3]); *(u32x2*)(yp + 32 * rb + 8 * rg + 4 * h) = w; }
.LBB0_484:
	v_and_b32_e32 v60, 31, v178
	s_and_b32 s6, s51, 0xffffffc0
	v_or_b32_e32 v4, s6, v60
	v_ashrrev_i32_e32 v5, 31, v4
	v_lshrrev_b32_e32 v2, 5, v162
	v_lshlrev_b64 v[4:5], 8, v[4:5]
	v_lshl_add_u64 v[4:5], s[54:55], 0, v[4:5]
	v_lshlrev_b32_e32 v6, 4, v2
	v_mov_b32_e32 v7, v3
	v_lshl_add_u64 v[12:13], v[4:5], 0, v[6:7]
	s_mov_b32 s6, 0x300000
	v_add_co_u32_e32 v4, vcc, s6, v12
	s_waitcnt lgkmcnt(0)
	s_nop 0
	v_addc_co_u32_e32 v5, vcc, 0, v13, vcc
	s_barrier
	s_waitcnt vmcnt(0)
	s_mov_b32 s6, 0x302000
	v_add_co_u32_e32 v56, vcc, s6, v12
	s_mov_b64 s[8:9], 0x300000
	s_nop 0
	v_addc_co_u32_e32 v57, vcc, 0, v13, vcc
	v_lshl_add_u64 v[58:59], v[12:13], 0, s[8:9]
	s_and_b32 s6, s51, 0xffffff80
	v_lshlrev_b32_e32 v2, 3, v2
	v_or_b32_e32 v15, s6, v2
	v_mul_u32_u24_e32 v14, 0x410, v60
	v_lshlrev_b32_e32 v15, 1, v15
	v_add3_u32 v61, 0, v14, v15
	ds_read_b128 v[12:15], v61 offset:49920
	ds_read_b128 v[40:43], v61 offset:49952
	s_and_b32 s11, s51, 64
	s_ashr_i32 s7, s6, 31
	s_lshl_b32 s38, s11, 1
	s_mov_b64 s[8:9], 0x3e000000
	s_waitcnt lgkmcnt(1)
	v_mfma_f32_32x32x16_bf16 v[20:35], v[64:67], v[12:15], 0
	v_mfma_f32_32x32x16_bf16 v[4:19], v[68:71], v[12:15], 0
	s_waitcnt lgkmcnt(0)
	v_mfma_f32_32x32x16_bf16 v[20:35], v[72:75], v[40:43], v[20:35]
	v_mfma_f32_32x32x16_bf16 v[4:19], v[76:79], v[40:43], v[4:19]
	ds_read_b128 v[44:47], v61 offset:49984
	ds_read_b128 v[52:55], v61 offset:50016
	s_waitcnt lgkmcnt(1)
	v_mfma_f32_32x32x16_bf16 v[20:35], v[80:83], v[44:47], v[20:35]
	v_mfma_f32_32x32x16_bf16 v[4:19], v[84:87], v[44:47], v[4:19]
	s_waitcnt lgkmcnt(0)
	v_mfma_f32_32x32x16_bf16 v[20:35], v[88:91], v[52:55], v[20:35]
	v_mfma_f32_32x32x16_bf16 v[4:19], v[92:95], v[52:55], v[4:19]
	ds_read_b128 v[48:51], v61 offset:50048
	ds_read_b128 v[52:55], v61 offset:50080
	s_waitcnt lgkmcnt(1)
	v_mfma_f32_32x32x16_bf16 v[20:35], v[96:99], v[48:51], v[20:35]
	v_mfma_f32_32x32x16_bf16 v[4:19], v[100:103], v[48:51], v[4:19]
	s_waitcnt lgkmcnt(0)
	v_mfma_f32_32x32x16_bf16 v[20:35], v[104:107], v[52:55], v[20:35]
	v_mfma_f32_32x32x16_bf16 v[4:19], v[108:111], v[52:55], v[4:19]
	ds_read_b128 v[48:51], v61 offset:50112
	ds_read_b128 v[52:55], v61 offset:50144
	s_waitcnt lgkmcnt(1)
	v_mfma_f32_32x32x16_bf16 v[20:35], v[112:115], v[48:51], v[20:35]
	v_mov_b32_e32 v57, v3
	v_mfma_f32_32x32x16_bf16 v[4:19], v[116:119], v[48:51], v[4:19]
	v_or_b32_e32 v44, s10, v60
	v_lshlrev_b32_e32 v56, 12, v44
	v_lshl_add_u64 v[44:45], s[54:55], 0, v[56:57]
	v_lshl_add_u64 v[44:45], s[6:7], 1, v[44:45]
	s_waitcnt lgkmcnt(0)
	v_mfma_f32_32x32x16_bf16 v[20:35], v[120:123], v[52:55], v[20:35]
	v_lshl_add_u64 v[36:37], v[44:45], 0, s[38:39]
	v_lshl_add_u64 v[36:37], v[36:37], 0, v[2:3]
	v_lshl_add_u64 v[38:39], v[36:37], 0, s[8:9]
	v_add_co_u32_e32 v36, vcc, s73, v36
	s_nop 7
	v_cvt_pk_bf16_f32 v20, v20, v21
	v_mfma_f32_32x32x16_bf16 v[4:19], v[124:127], v[52:55], v[4:19]
	v_addc_co_u32_e32 v37, vcc, 0, v37, vcc
	v_cvt_pk_bf16_f32 v21, v22, v23
	v_cvt_pk_bf16_f32 v22, v24, v25
	v_cvt_pk_bf16_f32 v23, v26, v27
	v_cvt_pk_bf16_f32 v24, v28, v29
	v_cvt_pk_bf16_f32 v25, v30, v31
	v_cvt_pk_bf16_f32 v26, v32, v33
	v_cvt_pk_bf16_f32 v27, v34, v35
	s_nop 3
	v_cvt_pk_bf16_f32 v4, v4, v5
	v_cvt_pk_bf16_f32 v5, v6, v7
	v_cvt_pk_bf16_f32 v6, v8, v9
	v_cvt_pk_bf16_f32 v7, v10, v11
	v_cvt_pk_bf16_f32 v8, v12, v13
	v_cvt_pk_bf16_f32 v9, v14, v15
	v_cvt_pk_bf16_f32 v10, v16, v17
	v_cvt_pk_bf16_f32 v11, v18, v19
	global_store_dwordx2 v[36:37], v[20:21], off
	global_store_dwordx2 v[38:39], v[22:23], off offset:16
	global_store_dwordx2 v[38:39], v[24:25], off offset:32
	global_store_dwordx2 v[38:39], v[26:27], off offset:48
	global_store_dwordx2 v[38:39], v[4:5], off offset:64
	global_store_dwordx2 v[38:39], v[6:7], off offset:80
	global_store_dwordx2 v[38:39], v[8:9], off offset:96
	global_store_dwordx2 v[38:39], v[10:11], off offset:112

; #define LAS __attribute__((address_space(3)))
;     ...
;         if (o == 0) { const bf16* src = T + (size_t)(2 * 512 + c) * 4 * L;
;             { constexpr int N1 = (4 * L / 8) / NT; u32x4 t1[N1];
; #pragma unroll
;               for (int i = 0; i < N1; ++i) t1[i] = *(const u32x4*)(src + 8 * (C.tid + NT * i));
; #pragma unroll
;               for (int i = 0; i < N1; ++i) { const int idx = C.tid + NT * i, b = idx / (L / 8), tc = idx % (L / 8); *(LAS u32x4*)(C.lds + b * SB + tc * 16) = t1[i]; } }
;             if (C.tid < 4) *(LAS u32x4*)(C.lds + Z_OFF + 16 * C.tid) = (u32x4){0u, 0u, 0u, 0u}; }
;         { const bf16* fsrc = (L == SL) ? WSP(bf16, WS_FILT) + (size_t)((l * 2 + o) * 512 + c) * (2 * L) : WSP(bf16, WS_FILTC) + (size_t)(o * 512 + c) * (2 * L);
;           constexpr int N2 = (L / 4) / NT; u32x4 t2[N2];
; #pragma unroll
;           for (int i = 0; i < N2; ++i) t2[i] = *(const u32x4*)(fsrc + 8 * (C.tid + NT * i));
; #pragma unroll
;           for (int i = 0; i < N2; ++i) *(LAS u32x4*)(C.lds + R_OFF + 16 * (C.tid + NT * i)) = t2[i]; }
;         __syncthreads();
;         for (int idx = C.tid; idx < 3 * (L / 2); idx += NT) { const int p = 1 + idx / (L / 2), w = idx % (L / 2); unsigned short e[4];
; #pragma unroll
;             for (int k = 0; k < 4; ++k) { const int n = 4 * w + p + k; e[k] = n < 2 * L ? *(const LAS bf16*)(C.lds + R_OFF + 2 * n) : (bf16)0; }
;             *(LAS u32x2*)(C.lds + R_OFF + p * CSZ + 8 + 64 * p + 8 * w) = (u32x2){(unsigned)e[0] | ((unsigned)e[1] << 16), (unsigned)e[2] | ((unsigned)e[3] << 16)}; }
.LBB0_913:
	s_xor_b64 s[48:49], s[10:11], -1
	s_and_b64 vcc, exec, s[48:49]
	s_waitcnt vmcnt(0) lgkmcnt(0)
	s_barrier
	s_cbranch_vccnz .LBB0_917
	global_load_dwordx4 v[2:5], v[168:169], off
	global_load_dwordx4 v[6:9], v[170:171], off
	global_load_dwordx4 v[10:13], v[172:173], off
	global_load_dwordx4 v[14:17], v[174:175], off
	s_add_i32 s34, s12, s42
	s_ashr_i32 s35, s34, 31
	s_lshl_b64 s[34:35], s[34:35], 14
	s_add_u32 s34, s19, s34
	s_addc_u32 s35, s24, s35
	v_lshl_add_u64 v[244:245], v[164:165], 1, s[34:35]
	v_lshl_add_u64 v[248:249], v[166:167], 1, s[34:35]
	global_load_dwordx4 v[244:247], v[244:245], off
	s_nop 0
	global_load_dwordx4 v[248:251], v[248:249], off
	s_waitcnt vmcnt(5)
	ds_write_b128 v225, v[2:5]
	s_waitcnt vmcnt(4)
	ds_write_b128 v226, v[6:9]
	s_waitcnt vmcnt(3)
	ds_write_b128 v227, v[10:13]
	s_waitcnt vmcnt(2)
	ds_write_b128 v228, v[14:17]
	s_and_saveexec_b64 s[10:11], s[8:9]
	v_add_u32_e32 v2, 0, v213
	ds_write_b128 v2, v[238:241] offset:32832
	s_or_b64 exec, exec, s[10:11]
	s_branch .Lhyf_l0_have
.LBB0_917:
	s_add_i32 s34, s12, s42
	s_ashr_i32 s35, s34, 31
	s_lshl_b64 s[34:35], s[34:35], 14
	s_add_u32 s34, s19, s34
	s_addc_u32 s35, s24, s35
	v_lshl_add_u64 v[244:245], v[164:165], 1, s[34:35]
	v_lshl_add_u64 v[248:249], v[166:167], 1, s[34:35]
	global_load_dwordx4 v[244:247], v[244:245], off
	s_nop 0
	global_load_dwordx4 v[248:251], v[248:249], off
.Lhyf_l0_have:
	s_add_i32 s10, s12, s42
	s_ashr_i32 s11, s10, 31
	v_add_u32_e32 v10, 0, v213
	s_waitcnt vmcnt(1)
	ds_write_b128 v10, v[244:247] offset:32896
	s_waitcnt vmcnt(0)
	ds_write_b128 v10, v[248:251] offset:41088
	s_waitcnt lgkmcnt(0)
	s_barrier
	s_and_saveexec_b64 s[12:13], s[6:7]
	s_cbranch_execz .LBB0_926
	v_lshlrev_b32_e32 v2, 3, v212
	v_add_u32_e32 v3, 0x8000, v2
	ds_read_b64 v[4:5], v2 offset:32896
	ds_read_b64 v[6:7], v2 offset:32904
	ds_read_b64 v[8:9], v2 offset:36992
	ds_read_b64 v[10:11], v2 offset:37000
	ds_read_b64 v[12:13], v2 offset:41088
	ds_read_b64 v[14:15], v2 offset:41096
	ds_read_b64 v[16:17], v2 offset:45184
	ds_read_b64 v[18:19], v2 offset:45192
	v_cmp_ne_u32_e32 vcc, 0x1ff, v212
	s_waitcnt lgkmcnt(0)
	v_cndmask_b32_e32 v18, 0, v18, vcc
	v_cndmask_b32_e32 v19, 0, v19, vcc
	v_alignbit_b32 v20, v5, v4, 16
	v_alignbit_b32 v21, v6, v5, 16
	v_mov_b32_e32 v22, v5
	v_mov_b32_e32 v23, v6
	v_mov_b32_e32 v24, v21
	v_alignbit_b32 v25, v7, v6, 16
	ds_write_b64 v2, v[20:21] offset:49352
	ds_write_b64 v3, v[22:23] offset:33032
	ds_write_b64 v3, v[24:25] offset:49480
	s_nop 0
	v_alignbit_b32 v20, v9, v8, 16
	v_alignbit_b32 v21, v10, v9, 16
	v_mov_b32_e32 v22, v9
	v_mov_b32_e32 v23, v10
	v_mov_b32_e32 v24, v21
	v_alignbit_b32 v25, v11, v10, 16
	ds_write_b64 v2, v[20:21] offset:53448
	ds_write_b64 v3, v[22:23] offset:37128
	ds_write_b64 v3, v[24:25] offset:53576
	s_nop 0
	v_alignbit_b32 v20, v13, v12, 16
	v_alignbit_b32 v21, v14, v13, 16
	v_mov_b32_e32 v22, v13
	v_mov_b32_e32 v23, v14
	v_mov_b32_e32 v24, v21
	v_alignbit_b32 v25, v15, v14, 16
	ds_write_b64 v2, v[20:21] offset:57544
	ds_write_b64 v3, v[22:23] offset:41224
	ds_write_b64 v3, v[24:25] offset:57672
	s_nop 0
	v_alignbit_b32 v20, v17, v16, 16
	v_alignbit_b32 v21, v18, v17, 16
	v_mov_b32_e32 v22, v17
	v_mov_b32_e32 v23, v18
	v_mov_b32_e32 v24, v21
	v_alignbit_b32 v25, v19, v18, 16
	ds_write_b64 v2, v[20:21] offset:61640
	ds_write_b64 v3, v[22:23] offset:45320
	ds_write_b64 v3, v[24:25] offset:61768
	s_nop 0

; __device__ __forceinline__ float wave_sum(float v) { return xor32_sum(xor16_sum(row16_sum(v))); }
; __device__ __forceinline__ void cvt8(const u32x4 r, float (&f)[8]) { f[0] = bflo(r.x); f[1] = bfhi(r.x); f[2] = bflo(r.y); f[3] = bfhi(r.y); f[4] = bflo(r.z); f[5] = bfhi(r.z); f[6] = bflo(r.w); f[7] = bfhi(r.w); }
; __device__ __forceinline__ void row_ln(float (&v)[32]) {
;     float s = 0.f;
; #pragma unroll
;     for (int i = 0; i < 32; ++i) s += v[i];
;     const float mean = wave_sum(s) * (1.0f / DM); float q = 0.f;
; #pragma unroll
;     for (int i = 0; i < 32; ++i) { v[i] -= mean; q += v[i] * v[i]; }
;     const float rstd = 1.0f / sqrtf(wave_sum(q) * (1.0f / DM) + LN_EPS);
; __device__ __forceinline__ void ph_post1(Ctx& C, int l, int nrows, bool dry = false) {
;     ...
;             if (l == 0) row_load(src_x0(C, row), C.lane, v); else row_load_bf16(WSP(bf16, WS_X) + (size_t)row * DM, C.lane, v);
;             row_load_lds(PAR, C.lane, g1);
;             { const bf16* yo = WSP(bf16, WS_YO) + (size_t)row * DM;
; #pragma unroll
;               for (int j = 0; j < 4; ++j) { float t8[8]; cvt8(*(const u32x4*)(yo + 512 * j + 8 * C.lane), t8);
; #pragma unroll
;                   for (int e = 0; e < 8; ++e) y[8 * j + e] = t8[e]; } }
; #pragma unroll
;             for (int i = 0; i < 32; ++i) v[i] = ALPHA * v[i] + g1[i] * y[i];
;             row_ln(v); row_affine_lds(v, PAR + 2048, PAR + 4096, C.lane, 0.f);
.Lp1a_nopf:
	s_lshl_b64 s[38:39], s[8:9], 11
	v_pk_add_f32 v[74:75], v[74:75], 0 op_sel_hi:[1,0]
	s_waitcnt lgkmcnt(8)
	v_pk_add_f32 v[2:3], v[2:3], 0 op_sel_hi:[1,0]
	v_pk_add_f32 v[46:47], v[46:47], 0 op_sel_hi:[1,0]
	v_pk_add_f32 v[44:45], v[44:45], 0 op_sel_hi:[1,0]
	v_pk_add_f32 v[42:43], v[42:43], 0 op_sel_hi:[1,0]
	v_pk_add_f32 v[48:49], v[48:49], 0 op_sel_hi:[1,0]
	v_pk_add_f32 v[40:41], v[40:41], 0 op_sel_hi:[1,0]
	v_pk_add_f32 v[38:39], v[38:39], 0 op_sel_hi:[1,0]
	v_lshlrev_b32_e32 v178, 16, v85
	v_and_b32_e32 v179, 0xffff0000, v85
	v_lshlrev_b32_e32 v182, 16, v82
	v_and_b32_e32 v183, 0xffff0000, v82
	v_lshlrev_b32_e32 v180, 16, v84
	v_and_b32_e32 v181, 0xffff0000, v84
	v_lshlrev_b32_e32 v84, 16, v83
	v_and_b32_e32 v85, 0xffff0000, v83
	v_lshlrev_b32_e32 v82, 16, v105
	v_and_b32_e32 v83, 0xffff0000, v105
	v_lshlrev_b32_e32 v184, 16, v104
	v_and_b32_e32 v185, 0xffff0000, v104
	v_lshlrev_b32_e32 v104, 16, v103
	v_and_b32_e32 v105, 0xffff0000, v103
	v_lshlrev_b32_e32 v186, 16, v102
	v_and_b32_e32 v187, 0xffff0000, v102
	v_pk_mul_f32 v[102:103], v[128:129], v[178:179]
	v_pk_mul_f32 v[122:123], v[122:123], v[182:183]
	v_pk_fma_f32 v[102:103], v[108:109], s[26:27], v[102:103] op_sel_hi:[1,0,1]
	v_pk_fma_f32 v[108:109], v[110:111], s[26:27], v[122:123] op_sel_hi:[1,0,1]
	v_pk_mul_f32 v[84:85], v[124:125], v[84:85]
	v_pk_fma_f32 v[84:85], v[112:113], s[26:27], v[84:85] op_sel_hi:[1,0,1]
	v_pk_mul_f32 v[126:127], v[126:127], v[180:181]
	v_pk_fma_f32 v[106:107], v[106:107], s[26:27], v[126:127] op_sel_hi:[1,0,1]
	v_pk_add_f32 v[248:249], v[108:109], v[84:85]
	v_pk_add_f32 v[248:249], v[248:249], v[106:107]
	v_pk_mul_f32 v[124:125], v[134:135], v[184:185]
	v_pk_mul_f32 v[128:129], v[130:131], v[186:187]
	v_pk_fma_f32 v[112:113], v[114:115], s[26:27], v[124:125] op_sel_hi:[1,0,1]
	v_pk_fma_f32 v[114:115], v[118:119], s[26:27], v[128:129] op_sel_hi:[1,0,1]
	v_pk_add_f32 v[248:249], v[248:249], v[102:103]
	v_pk_mul_f32 v[104:105], v[132:133], v[104:105]
	v_pk_fma_f32 v[104:105], v[120:121], s[26:27], v[104:105] op_sel_hi:[1,0,1]
	v_pk_add_f32 v[248:249], v[248:249], v[114:115]
	v_pk_add_f32 v[248:249], v[248:249], v[104:105]
	v_pk_mul_f32 v[82:83], v[136:137], v[82:83]
	v_pk_fma_f32 v[110:111], v[116:117], s[26:27], v[82:83] op_sel_hi:[1,0,1]
	v_pk_add_f32 v[248:249], v[248:249], v[112:113]
	v_lshlrev_b32_e32 v124, 16, v150
	v_and_b32_e32 v125, 0xffff0000, v150
	v_pk_mul_f32 v[124:125], v[138:139], v[124:125]
	v_pk_add_f32 v[248:249], v[248:249], v[110:111]
	v_lshlrev_b32_e32 v122, 16, v151
	v_and_b32_e32 v123, 0xffff0000, v151
	v_pk_fma_f32 v[124:125], v[154:155], s[26:27], v[124:125] op_sel_hi:[1,0,1]
	v_pk_mul_f32 v[122:123], v[140:141], v[122:123]
	v_lshlrev_b32_e32 v120, 16, v152
	v_and_b32_e32 v121, 0xffff0000, v152
	v_pk_fma_f32 v[122:123], v[156:157], s[26:27], v[122:123] op_sel_hi:[1,0,1]
	v_pk_add_f32 v[248:249], v[248:249], v[124:125]
	v_pk_mul_f32 v[120:121], v[142:143], v[120:121]
	v_lshlrev_b32_e32 v118, 16, v153
	v_and_b32_e32 v119, 0xffff0000, v153
	v_pk_fma_f32 v[120:121], v[158:159], s[26:27], v[120:121] op_sel_hi:[1,0,1]
	v_pk_add_f32 v[248:249], v[248:249], v[122:123]
	v_pk_mul_f32 v[118:119], v[144:145], v[118:119]
	v_lshlrev_b32_e32 v130, 16, v165
	v_and_b32_e32 v131, 0xffff0000, v165
	v_pk_fma_f32 v[118:119], v[160:161], s[26:27], v[118:119] op_sel_hi:[1,0,1]
	v_pk_add_f32 v[248:249], v[248:249], v[120:121]
	v_pk_mul_f32 v[52:53], v[52:53], v[130:131]
	v_lshlrev_b32_e32 v130, 16, v164
	v_and_b32_e32 v131, 0xffff0000, v164
	v_pk_mul_f32 v[50:51], v[50:51], v[130:131]
	v_pk_add_f32 v[248:249], v[248:249], v[118:119]
	v_pk_fma_f32 v[50:51], v[170:171], s[26:27], v[50:51] op_sel_hi:[1,0,1]
	v_lshlrev_b32_e32 v128, 16, v166
	v_and_b32_e32 v129, 0xffff0000, v166
	v_pk_fma_f32 v[52:53], v[172:173], s[26:27], v[52:53] op_sel_hi:[1,0,1]
	v_pk_add_f32 v[248:249], v[248:249], v[50:51]
	v_pk_mul_f32 v[128:129], v[146:147], v[128:129]
	v_lshlrev_b32_e32 v126, 16, v167
	v_and_b32_e32 v127, 0xffff0000, v167
	v_pk_fma_f32 v[128:129], v[174:175], s[26:27], v[128:129] op_sel_hi:[1,0,1]
	v_pk_add_f32 v[248:249], v[248:249], v[52:53]
	v_pk_mul_f32 v[126:127], v[148:149], v[126:127]
	v_pk_fma_f32 v[126:127], v[176:177], s[26:27], v[126:127] op_sel_hi:[1,0,1]
	v_pk_add_f32 v[248:249], v[248:249], v[128:129]
	v_pk_add_f32 v[248:249], v[248:249], v[126:127]
	v_add_f32_e32 v69, v248, v249
	v_pk_add_f32 v[82:83], v[162:163], 0 op_sel_hi:[1,0]
	v_pk_add_f32 v[116:117], v[168:169], 0 op_sel_hi:[1,0]
	v_add_f32_dpp v69, v69, v69 quad_perm:[1,0,3,2] row_mask:0xf bank_mask:0xf bound_ctrl:1
	s_nop 1
	v_add_f32_dpp v69, v69, v69 quad_perm:[2,3,0,1] row_mask:0xf bank_mask:0xf bound_ctrl:1
	s_nop 1
	v_add_f32_dpp v69, v69, v69 row_half_mirror row_mask:0xf bank_mask:0xf bound_ctrl:1
	s_nop 1
	v_add_f32_dpp v69, v69, v69 row_mirror row_mask:0xf bank_mask:0xf bound_ctrl:1
	v_mov_b32_e32 v130, v69
	s_nop 1
	v_permlane16_swap_b32_e32 v69, v130
	v_add_f32_e32 v69, v69, v130
	v_mov_b32_e32 v130, v69
	s_nop 1
	v_permlane32_swap_b32_e32 v69, v130
	v_add_f32_e32 v69, v69, v130
	v_mul_f32_e32 v130, 0x3a000000, v69
	v_pk_add_f32 v[108:109], v[108:109], v[130:131] op_sel_hi:[1,0] neg_lo:[0,1] neg_hi:[0,1]
	v_pk_add_f32 v[84:85], v[84:85], v[130:131] op_sel_hi:[1,0] neg_lo:[0,1] neg_hi:[0,1]
	v_pk_mul_f32 v[248:249], v[108:109], v[108:109]
	v_pk_fma_f32 v[248:249], v[84:85], v[84:85], v[248:249]
	v_pk_add_f32 v[106:107], v[106:107], v[130:131] op_sel_hi:[1,0] neg_lo:[0,1] neg_hi:[0,1]
	v_pk_fma_f32 v[248:249], v[106:107], v[106:107], v[248:249]
	v_pk_add_f32 v[102:103], v[102:103], v[130:131] op_sel_hi:[1,0] neg_lo:[0,1] neg_hi:[0,1]
; __device__ __forceinline__ float wave_sum(float v) { return xor32_sum(xor16_sum(row16_sum(v))); }
; __device__ __forceinline__ void row_ln(float (&v)[32]) {
;     float s = 0.f;
; #pragma unroll
;     for (int i = 0; i < 32; ++i) s += v[i];
;     const float mean = wave_sum(s) * (1.0f / DM); float q = 0.f;
; #pragma unroll
;     for (int i = 0; i < 32; ++i) { v[i] -= mean; q += v[i] * v[i]; }
;     const float rstd = 1.0f / sqrtf(wave_sum(q) * (1.0f / DM) + LN_EPS);
; #pragma unroll
;     for (int i = 0; i < 32; ++i) v[i] *= rstd;
; }
; __device__ __forceinline__ void ph_post1(Ctx& C, int l, int nrows, bool dry = false) {
;     ...
;             for (int i = 0; i < 32; ++i) v[i] = ALPHA * v[i] + g1[i] * y[i];
;             row_ln(v); row_affine_lds(v, PAR + 2048, PAR + 4096, C.lane, 0.f);
	v_pk_fma_f32 v[248:249], v[102:103], v[102:103], v[248:249]
	v_pk_add_f32 v[114:115], v[114:115], v[130:131] op_sel_hi:[1,0] neg_lo:[0,1] neg_hi:[0,1]
	v_pk_fma_f32 v[248:249], v[114:115], v[114:115], v[248:249]
	v_pk_add_f32 v[104:105], v[104:105], v[130:131] op_sel_hi:[1,0] neg_lo:[0,1] neg_hi:[0,1]
	v_pk_fma_f32 v[248:249], v[104:105], v[104:105], v[248:249]
	v_pk_add_f32 v[112:113], v[112:113], v[130:131] op_sel_hi:[1,0] neg_lo:[0,1] neg_hi:[0,1]
	v_pk_fma_f32 v[248:249], v[112:113], v[112:113], v[248:249]
	v_pk_add_f32 v[110:111], v[110:111], v[130:131] op_sel_hi:[1,0] neg_lo:[0,1] neg_hi:[0,1]
	v_pk_fma_f32 v[248:249], v[110:111], v[110:111], v[248:249]
	v_pk_add_f32 v[124:125], v[124:125], v[130:131] op_sel_hi:[1,0] neg_lo:[0,1] neg_hi:[0,1]
	v_pk_fma_f32 v[248:249], v[124:125], v[124:125], v[248:249]
	v_pk_add_f32 v[122:123], v[122:123], v[130:131] op_sel_hi:[1,0] neg_lo:[0,1] neg_hi:[0,1]
	v_pk_fma_f32 v[248:249], v[122:123], v[122:123], v[248:249]
	v_pk_add_f32 v[120:121], v[120:121], v[130:131] op_sel_hi:[1,0] neg_lo:[0,1] neg_hi:[0,1]
	v_pk_fma_f32 v[248:249], v[120:121], v[120:121], v[248:249]
	v_pk_add_f32 v[118:119], v[118:119], v[130:131] op_sel_hi:[1,0] neg_lo:[0,1] neg_hi:[0,1]
	v_pk_fma_f32 v[248:249], v[118:119], v[118:119], v[248:249]
	v_pk_add_f32 v[50:51], v[50:51], v[130:131] op_sel_hi:[1,0] neg_lo:[0,1] neg_hi:[0,1]
	v_pk_fma_f32 v[248:249], v[50:51], v[50:51], v[248:249]
	v_pk_add_f32 v[52:53], v[52:53], v[130:131] op_sel_hi:[1,0] neg_lo:[0,1] neg_hi:[0,1]
	v_pk_fma_f32 v[248:249], v[52:53], v[52:53], v[248:249]
	v_pk_add_f32 v[128:129], v[128:129], v[130:131] op_sel_hi:[1,0] neg_lo:[0,1] neg_hi:[0,1]
	v_pk_fma_f32 v[248:249], v[128:129], v[128:129], v[248:249]
	v_pk_add_f32 v[126:127], v[126:127], v[130:131] op_sel_hi:[1,0] neg_lo:[0,1] neg_hi:[0,1]
	v_pk_fma_f32 v[248:249], v[126:127], v[126:127], v[248:249]
	v_add_f32_e32 v69, v248, v249
	s_nop 1
	v_add_f32_dpp v69, v69, v69 quad_perm:[1,0,3,2] row_mask:0xf bank_mask:0xf bound_ctrl:1
	s_nop 1
	v_add_f32_dpp v69, v69, v69 quad_perm:[2,3,0,1] row_mask:0xf bank_mask:0xf bound_ctrl:1
	s_nop 1
	v_add_f32_dpp v69, v69, v69 row_half_mirror row_mask:0xf bank_mask:0xf bound_ctrl:1
	s_nop 1
	v_add_f32_dpp v69, v69, v69 row_mirror row_mask:0xf bank_mask:0xf bound_ctrl:1
	v_mov_b32_e32 v130, v69
	s_nop 1
	v_permlane16_swap_b32_e32 v69, v130
	v_add_f32_e32 v69, v69, v130
	v_mov_b32_e32 v130, v69
	s_nop 1
	v_permlane32_swap_b32_e32 v69, v130
	v_add_f32_e32 v69, v69, v130
	v_fmamk_f32 v69, v69, 0x3a000000, v97
	v_mul_f32_e32 v130, 0x4f800000, v69
	v_cmp_gt_f32_e32 vcc, s34, v69
	s_nop 1
	v_cndmask_b32_e32 v69, v69, v130, vcc
	v_sqrt_f32_e32 v130, v69
	s_nop 0
	v_add_u32_e32 v131, -1, v130
	v_fma_f32 v132, -v131, v130, v69
	v_cmp_ge_f32_e64 s[8:9], 0, v132
	v_add_u32_e32 v132, 1, v130
	s_nop 0
	v_cndmask_b32_e64 v131, v130, v131, s[8:9]
	v_fma_f32 v130, -v132, v130, v69
	v_cmp_lt_f32_e64 s[8:9], 0, v130
	s_nop 1
	v_cndmask_b32_e64 v130, v131, v132, s[8:9]
	v_mul_f32_e32 v131, 0x37800000, v130
	v_cndmask_b32_e32 v130, v130, v131, vcc
	v_cmp_class_f32_e32 vcc, v69, v98
	s_nop 1
	v_cndmask_b32_e32 v69, v130, v69, vcc
	v_div_scale_f32 v130, s[8:9], v69, v69, 1.0
	v_rcp_f32_e32 v131, v130
	s_nop 0
	v_fma_f32 v132, -v130, v131, 1.0
	v_fmac_f32_e32 v131, v132, v131
	v_div_scale_f32 v132, vcc, 1.0, v69, 1.0
	v_mul_f32_e32 v133, v132, v131
	v_fma_f32 v134, -v130, v133, v132
	v_fmac_f32_e32 v133, v134, v131
	v_fma_f32 v130, -v130, v133, v132
	v_div_fmas_f32 v130, v130, v131, v133
	v_div_fixup_f32 v130, v130, v69, 1.0
	v_pk_mul_f32 v[108:109], v[108:109], v[130:131] op_sel_hi:[1,0]
	v_pk_mul_f32 v[84:85], v[84:85], v[130:131] op_sel_hi:[1,0]
	v_pk_mul_f32 v[106:107], v[106:107], v[130:131] op_sel_hi:[1,0]
	v_pk_mul_f32 v[102:103], v[102:103], v[130:131] op_sel_hi:[1,0]
	v_pk_mul_f32 v[128:129], v[128:129], v[130:131] op_sel_hi:[1,0]
	v_pk_mul_f32 v[114:115], v[114:115], v[130:131] op_sel_hi:[1,0]
	v_pk_mul_f32 v[104:105], v[104:105], v[130:131] op_sel_hi:[1,0]
	v_pk_mul_f32 v[112:113], v[112:113], v[130:131] op_sel_hi:[1,0]
	v_pk_mul_f32 v[110:111], v[110:111], v[130:131] op_sel_hi:[1,0]
	v_pk_mul_f32 v[126:127], v[126:127], v[130:131] op_sel_hi:[1,0]
	s_waitcnt lgkmcnt(7)
	v_pk_fma_f32 v[108:109], v[74:75], v[108:109], v[34:35]
	v_pk_fma_f32 v[84:85], v[72:73], v[84:85], v[36:37]
	s_waitcnt lgkmcnt(6)
	v_pk_fma_f32 v[106:107], v[70:71], v[106:107], v[30:31]
	v_pk_fma_f32 v[102:103], v[76:77], v[102:103], v[32:33]
	s_waitcnt lgkmcnt(0)
; __device__ __forceinline__ unsigned pk2(float lo, float hi) { f32x2 v = {lo, hi}; bf16x2_t b = __builtin_convertvector(v, bf16x2_t); return __builtin_bit_cast(unsigned, b); }
; __device__ __forceinline__ unsigned pk4_fp8(float a, float b, float c, float d) { int p = 0; p = __builtin_amdgcn_cvt_pk_fp8_f32(a, b, p, false); p = __builtin_amdgcn_cvt_pk_fp8_f32(c, d, p, true); return (unsigned)p; }
; __device__ __forceinline__ float wave_sum(float v) { return xor32_sum(xor16_sum(row16_sum(v))); }
; __device__ __forceinline__ void row_store(float* p, int lane, const float (&v)[32]) {
; #pragma unroll
;     for (int j = 0; j < 4; ++j) { *(f32x4*)(p + 512 * j + 8 * lane) = (f32x4){v[8 * j], v[8 * j + 1], v[8 * j + 2], v[8 * j + 3]}; *(f32x4*)(p + 512 * j + 8 * lane + 4) = (f32x4){v[8 * j + 4], v[8 * j + 5], v[8 * j + 6], v[8 * j + 7]}; }
; }
; __device__ __forceinline__ void row_store_bf16(bf16* p, int lane, const float (&v)[32]) {
; #pragma unroll
;     for (int j = 0; j < 4; ++j) { u32x4 w; w.x = pk2(v[8 * j], v[8 * j + 1]); w.y = pk2(v[8 * j + 2], v[8 * j + 3]); w.z = pk2(v[8 * j + 4], v[8 * j + 5]); w.w = pk2(v[8 * j + 6], v[8 * j + 7]); *(u32x4*)(p + 512 * j + 8 * lane) = w; }
; }
; __device__ __forceinline__ void row_store_fp8(unsigned char* p, int lane, const float (&v)[32]) {
; #pragma unroll
;     for (int j = 0; j < 4; ++j) { u32x2 w; w.x = pk4_fp8(v[8 * j], v[8 * j + 1], v[8 * j + 2], v[8 * j + 3]); w.y = pk4_fp8(v[8 * j + 4], v[8 * j + 5], v[8 * j + 6], v[8 * j + 7]); *(u32x2*)(p + 512 * j + 8 * lane) = w; }
; }
; __device__ __forceinline__ void row_ln(float (&v)[32]) {
;     float s = 0.f;
; #pragma unroll
;     for (int i = 0; i < 32; ++i) s += v[i];
;     const float mean = wave_sum(s) * (1.0f / DM); float q = 0.f;
; #pragma unroll
;     for (int i = 0; i < 32; ++i) { v[i] -= mean; q += v[i] * v[i]; }
;     const float rstd = 1.0f / sqrtf(wave_sum(q) * (1.0f / DM) + LN_EPS);
; #pragma unroll
;     for (int i = 0; i < 32; ++i) v[i] *= rstd;
; }
; __device__ __forceinline__ void ph_post1(Ctx& C, int l, int nrows, bool dry = false) {
;     ...
;             row_ln(v); row_affine_lds(v, PAR + 2048, PAR + 4096, C.lane, 0.f);
;             row_store_bf16(WSP(bf16, WS_X) + (size_t)row * DM, C.lane, v);
;             row_ln(v); row_affine_lds(v, PAR + 6144, PAR + 8192, C.lane, 1.0f);
	v_pk_fma_f32 v[128:129], v[128:129], v[2:3], v[6:7]
	v_pk_add_f32 v[2:3], v[4:5], 0 op_sel_hi:[1,0]
	v_pk_mul_f32 v[124:125], v[124:125], v[130:131] op_sel_hi:[1,0]
	v_pk_mul_f32 v[122:123], v[122:123], v[130:131] op_sel_hi:[1,0]
	v_pk_mul_f32 v[120:121], v[120:121], v[130:131] op_sel_hi:[1,0]
	v_pk_mul_f32 v[118:119], v[118:119], v[130:131] op_sel_hi:[1,0]
	v_pk_fma_f32 v[82:83], v[82:83], v[114:115], v[26:27]
	v_pk_fma_f32 v[104:105], v[80:81], v[104:105], v[28:29]
	v_pk_fma_f32 v[112:113], v[78:79], v[112:113], v[22:23]
	v_pk_fma_f32 v[110:111], v[116:117], v[110:111], v[24:25]
	v_pk_fma_f32 v[126:127], v[126:127], v[2:3], v[8:9]
	v_lshl_add_u64 v[6:7], v[60:61], 0, s[42:43]
	v_cvt_pk_bf16_f32 v2, v108, v109
	v_cvt_pk_bf16_f32 v3, v84, v85
	v_cvt_pk_bf16_f32 v4, v106, v107
	v_cvt_pk_bf16_f32 v5, v102, v103
	v_pk_mul_f32 v[50:51], v[50:51], v[130:131] op_sel_hi:[1,0]
	v_pk_mul_f32 v[52:53], v[52:53], v[130:131] op_sel_hi:[1,0]
	v_pk_fma_f32 v[114:115], v[42:43], v[124:125], v[18:19]
	v_pk_fma_f32 v[116:117], v[44:45], v[122:123], v[20:21]
	v_pk_fma_f32 v[120:121], v[46:47], v[120:121], v[14:15]
	v_pk_fma_f32 v[118:119], v[48:49], v[118:119], v[16:17]
	global_store_dwordx4 v[6:7], v[2:5], off
	v_pk_fma_f32 v[122:123], v[50:51], v[38:39], v[10:11]
	v_pk_fma_f32 v[124:125], v[52:53], v[40:41], v[12:13]
	v_cvt_pk_bf16_f32 v2, v82, v83
	v_cvt_pk_bf16_f32 v3, v104, v105
	v_cvt_pk_bf16_f32 v4, v112, v113
	v_cvt_pk_bf16_f32 v5, v110, v111
	global_store_dwordx4 v[6:7], v[2:5], off offset:1024
	s_nop 1
	v_cvt_pk_bf16_f32 v2, v114, v115
	v_cvt_pk_bf16_f32 v3, v116, v117
	v_cvt_pk_bf16_f32 v4, v120, v121
	v_cvt_pk_bf16_f32 v5, v118, v119
	global_store_dwordx4 v[6:7], v[2:5], off offset:2048
	s_nop 1
	v_cvt_pk_bf16_f32 v2, v122, v123
	v_cvt_pk_bf16_f32 v3, v124, v125
	v_cvt_pk_bf16_f32 v4, v128, v129
	v_cvt_pk_bf16_f32 v5, v126, v127
	global_store_dwordx4 v[6:7], v[2:5], off offset:3072
	s_nop 1
	v_pk_add_f32 v[248:249], v[108:109], v[84:85]
	v_pk_add_f32 v[248:249], v[248:249], v[106:107]
	v_pk_add_f32 v[248:249], v[248:249], v[102:103]
	v_pk_add_f32 v[248:249], v[248:249], v[82:83]
	v_pk_add_f32 v[248:249], v[248:249], v[104:105]
	v_pk_add_f32 v[248:249], v[248:249], v[112:113]
	v_pk_add_f32 v[248:249], v[248:249], v[110:111]
	v_pk_add_f32 v[248:249], v[248:249], v[114:115]
	v_pk_add_f32 v[248:249], v[248:249], v[116:117]
	v_pk_add_f32 v[248:249], v[248:249], v[120:121]
	v_pk_add_f32 v[248:249], v[248:249], v[118:119]
	v_pk_add_f32 v[248:249], v[248:249], v[122:123]
	v_pk_add_f32 v[248:249], v[248:249], v[124:125]
	v_pk_add_f32 v[248:249], v[248:249], v[128:129]
	v_pk_add_f32 v[248:249], v[248:249], v[126:127]
	v_add_f32_e32 v2, v248, v249
	s_nop 1
	v_add_f32_dpp v2, v2, v2 quad_perm:[1,0,3,2] row_mask:0xf bank_mask:0xf bound_ctrl:1
	s_nop 1
	v_add_f32_dpp v2, v2, v2 quad_perm:[2,3,0,1] row_mask:0xf bank_mask:0xf bound_ctrl:1
	s_nop 1
	v_add_f32_dpp v2, v2, v2 row_half_mirror row_mask:0xf bank_mask:0xf bound_ctrl:1
	s_nop 1
	v_add_f32_dpp v2, v2, v2 row_mirror row_mask:0xf bank_mask:0xf bound_ctrl:1
	v_mov_b32_e32 v3, v2
	s_nop 1
	v_permlane16_swap_b32_e32 v2, v3
	v_add_f32_e32 v2, v2, v3
	v_mov_b32_e32 v3, v2
	s_nop 1
	v_permlane32_swap_b32_e32 v2, v3
	v_add_f32_e32 v2, v2, v3
	v_mul_f32_e32 v130, 0x3a000000, v2
	v_pk_add_f32 v[108:109], v[108:109], v[130:131] op_sel_hi:[1,0] neg_lo:[0,1] neg_hi:[0,1]
	v_pk_add_f32 v[84:85], v[84:85], v[130:131] op_sel_hi:[1,0] neg_lo:[0,1] neg_hi:[0,1]
	v_pk_mul_f32 v[248:249], v[108:109], v[108:109]
	v_pk_fma_f32 v[248:249], v[84:85], v[84:85], v[248:249]
	v_pk_add_f32 v[106:107], v[106:107], v[130:131] op_sel_hi:[1,0] neg_lo:[0,1] neg_hi:[0,1]
	v_pk_fma_f32 v[248:249], v[106:107], v[106:107], v[248:249]
	v_pk_add_f32 v[102:103], v[102:103], v[130:131] op_sel_hi:[1,0] neg_lo:[0,1] neg_hi:[0,1]
	v_pk_fma_f32 v[248:249], v[102:103], v[102:103], v[248:249]
	v_pk_add_f32 v[82:83], v[82:83], v[130:131] op_sel_hi:[1,0] neg_lo:[0,1] neg_hi:[0,1]
	v_pk_fma_f32 v[248:249], v[82:83], v[82:83], v[248:249]
	v_pk_add_f32 v[104:105], v[104:105], v[130:131] op_sel_hi:[1,0] neg_lo:[0,1] neg_hi:[0,1]
	v_pk_fma_f32 v[248:249], v[104:105], v[104:105], v[248:249]
	v_pk_add_f32 v[112:113], v[112:113], v[130:131] op_sel_hi:[1,0] neg_lo:[0,1] neg_hi:[0,1]
	v_pk_fma_f32 v[248:249], v[112:113], v[112:113], v[248:249]
	v_pk_add_f32 v[110:111], v[110:111], v[130:131] op_sel_hi:[1,0] neg_lo:[0,1] neg_hi:[0,1]
	v_pk_fma_f32 v[248:249], v[110:111], v[110:111], v[248:249]
	v_pk_add_f32 v[114:115], v[114:115], v[130:131] op_sel_hi:[1,0] neg_lo:[0,1] neg_hi:[0,1]
	v_pk_fma_f32 v[248:249], v[114:115], v[114:115], v[248:249]
	v_pk_add_f32 v[116:117], v[116:117], v[130:131] op_sel_hi:[1,0] neg_lo:[0,1] neg_hi:[0,1]
	v_pk_fma_f32 v[248:249], v[116:117], v[116:117], v[248:249]
	v_pk_add_f32 v[120:121], v[120:121], v[130:131] op_sel_hi:[1,0] neg_lo:[0,1] neg_hi:[0,1]
	v_pk_fma_f32 v[248:249], v[120:121], v[120:121], v[248:249]
	v_pk_add_f32 v[118:119], v[118:119], v[130:131] op_sel_hi:[1,0] neg_lo:[0,1] neg_hi:[0,1]
	v_pk_fma_f32 v[248:249], v[118:119], v[118:119], v[248:249]
	v_pk_add_f32 v[122:123], v[122:123], v[130:131] op_sel_hi:[1,0] neg_lo:[0,1] neg_hi:[0,1]
	v_pk_fma_f32 v[248:249], v[122:123], v[122:123], v[248:249]
	v_pk_add_f32 v[124:125], v[124:125], v[130:131] op_sel_hi:[1,0] neg_lo:[0,1] neg_hi:[0,1]
	v_pk_fma_f32 v[248:249], v[124:125], v[124:125], v[248:249]
	v_pk_add_f32 v[128:129], v[128:129], v[130:131] op_sel_hi:[1,0] neg_lo:[0,1] neg_hi:[0,1]
	v_pk_fma_f32 v[248:249], v[128:129], v[128:129], v[248:249]
	v_pk_add_f32 v[126:127], v[126:127], v[130:131] op_sel_hi:[1,0] neg_lo:[0,1] neg_hi:[0,1]
	v_pk_fma_f32 v[248:249], v[126:127], v[126:127], v[248:249]
	v_add_f32_e32 v69, v248, v249
	ds_read_b128 v[2:5], v99
	ds_read_b128 v[6:9], v99 offset:16
	ds_read_b128 v[10:13], v99 offset:2048
	ds_read_b128 v[14:17], v99 offset:2064
	ds_read_b128 v[18:21], v99 offset:4096
	ds_read_b128 v[22:25], v99 offset:4112
	ds_read_b128 v[26:29], v99 offset:6144
	ds_read_b128 v[30:33], v99 offset:6160
	ds_read_b128 v[34:37], v100
	ds_read_b128 v[38:41], v100 offset:16
	ds_read_b128 v[42:45], v100 offset:2048
	ds_read_b128 v[46:49], v100 offset:2064
	ds_read_b128 v[50:53], v100 offset:4096
	ds_read_b128 v[70:73], v100 offset:4112
	ds_read_b128 v[74:77], v100 offset:6144
	ds_read_b128 v[78:81], v100 offset:6160
	v_add_f32_dpp v69, v69, v69 quad_perm:[1,0,3,2] row_mask:0xf bank_mask:0xf bound_ctrl:1
	s_waitcnt lgkmcnt(14)
; #define LAS __attribute__((address_space(3)))
; __device__ __forceinline__ void ph_post1(Ctx& C, int l, int nrows, bool dry = false) {
;     ...
;             row_ln(v); row_affine_lds(v, PAR + 6144, PAR + 8192, C.lane, 1.0f);
;             row_store_fp8(WSP(unsigned char, WS_HB8) + (size_t)row * DM, C.lane, v);
; #pragma unroll
;             for (int j = 0; j < 4; ++j) { *(LAS f32x4*)(H2 + C.wave * DM + 512 * j + 8 * C.lane) = (f32x4){v[8 * j], v[8 * j + 1], v[8 * j + 2], v[8 * j + 3]};
;                 *(LAS f32x4*)(H2 + C.wave * DM + 512 * j + 8 * C.lane + 4) = (f32x4){v[8 * j + 4], v[8 * j + 5], v[8 * j + 6], v[8 * j + 7]}; }
;         }
;         __syncthreads();
	v_pk_add_f32 v[2:3], v[2:3], 1.0 op_sel_hi:[1,0]
	v_pk_add_f32 v[4:5], v[4:5], 1.0 op_sel_hi:[1,0]
	v_add_f32_dpp v69, v69, v69 quad_perm:[2,3,0,1] row_mask:0xf bank_mask:0xf bound_ctrl:1
	v_pk_add_f32 v[6:7], v[6:7], 1.0 op_sel_hi:[1,0]
	s_waitcnt lgkmcnt(13)
	v_pk_add_f32 v[10:11], v[10:11], 1.0 op_sel_hi:[1,0]
	v_add_f32_dpp v69, v69, v69 row_half_mirror row_mask:0xf bank_mask:0xf bound_ctrl:1
	s_waitcnt lgkmcnt(12)
	v_pk_add_f32 v[14:15], v[14:15], 1.0 op_sel_hi:[1,0]
	v_pk_add_f32 v[8:9], v[8:9], 1.0 op_sel_hi:[1,0]
	v_add_f32_dpp v69, v69, v69 row_mirror row_mask:0xf bank_mask:0xf bound_ctrl:1
	v_mov_b32_e32 v130, v69
	s_nop 1
	v_permlane16_swap_b32_e32 v69, v130
	v_add_f32_e32 v69, v69, v130
	v_mov_b32_e32 v130, v69
	s_nop 1
	v_permlane32_swap_b32_e32 v69, v130
	v_add_f32_e32 v69, v69, v130
	v_fmamk_f32 v69, v69, 0x3a000000, v97
	v_mul_f32_e32 v130, 0x4f800000, v69
	v_cmp_gt_f32_e32 vcc, s34, v69
	s_waitcnt lgkmcnt(11)
	v_pk_add_f32 v[18:19], v[18:19], 1.0 op_sel_hi:[1,0]
	s_waitcnt lgkmcnt(10)
	v_pk_add_f32 v[22:23], v[22:23], 1.0 op_sel_hi:[1,0]
	v_cndmask_b32_e32 v69, v69, v130, vcc
	v_sqrt_f32_e32 v130, v69
	s_waitcnt lgkmcnt(9)
	v_pk_add_f32 v[26:27], v[26:27], 1.0 op_sel_hi:[1,0]
	s_waitcnt lgkmcnt(8)
	v_pk_add_f32 v[30:31], v[30:31], 1.0 op_sel_hi:[1,0]
	v_pk_add_f32 v[12:13], v[12:13], 1.0 op_sel_hi:[1,0]
	v_add_u32_e32 v131, -1, v130
	v_fma_f32 v132, -v131, v130, v69
	v_cmp_ge_f32_e64 s[8:9], 0, v132
	v_add_u32_e32 v132, 1, v130
	v_pk_add_f32 v[16:17], v[16:17], 1.0 op_sel_hi:[1,0]
	v_cndmask_b32_e64 v131, v130, v131, s[8:9]
	v_fma_f32 v130, -v132, v130, v69
	v_cmp_lt_f32_e64 s[8:9], 0, v130
	v_pk_add_f32 v[20:21], v[20:21], 1.0 op_sel_hi:[1,0]
	v_pk_add_f32 v[24:25], v[24:25], 1.0 op_sel_hi:[1,0]
	v_cndmask_b32_e64 v130, v131, v132, s[8:9]
	v_mul_f32_e32 v131, 0x37800000, v130
	v_cndmask_b32_e32 v130, v130, v131, vcc
	v_cmp_class_f32_e32 vcc, v69, v98
	v_pk_add_f32 v[28:29], v[28:29], 1.0 op_sel_hi:[1,0]
	v_pk_add_f32 v[32:33], v[32:33], 1.0 op_sel_hi:[1,0]
	v_cndmask_b32_e32 v69, v130, v69, vcc
	v_div_scale_f32 v130, s[8:9], v69, v69, 1.0
	v_rcp_f32_e32 v131, v130
	s_mov_b32 s8, -4
	v_fma_f32 v132, -v130, v131, 1.0
	v_fmac_f32_e32 v131, v132, v131
	v_div_scale_f32 v132, vcc, 1.0, v69, 1.0
	v_mul_f32_e32 v133, v132, v131
	v_fma_f32 v134, -v130, v133, v132
	v_fmac_f32_e32 v133, v134, v131
	v_fma_f32 v130, -v130, v133, v132
	v_div_fmas_f32 v130, v130, v131, v133
	v_div_fixup_f32 v130, v130, v69, 1.0
	v_pk_mul_f32 v[108:109], v[108:109], v[130:131] op_sel_hi:[1,0]
	v_pk_mul_f32 v[84:85], v[84:85], v[130:131] op_sel_hi:[1,0]
	v_pk_mul_f32 v[106:107], v[106:107], v[130:131] op_sel_hi:[1,0]
	v_pk_mul_f32 v[82:83], v[82:83], v[130:131] op_sel_hi:[1,0]
	v_pk_mul_f32 v[112:113], v[112:113], v[130:131] op_sel_hi:[1,0]
	s_waitcnt lgkmcnt(7)
	v_pk_fma_f32 v[2:3], v[2:3], v[108:109], v[34:35]
	v_pk_fma_f32 v[4:5], v[4:5], v[84:85], v[36:37]
	s_waitcnt lgkmcnt(6)
	v_pk_fma_f32 v[6:7], v[6:7], v[106:107], v[38:39]
	v_mov_b32_e32 v36, 0
	v_mov_b32_e32 v37, 0
	v_pk_mul_f32 v[102:103], v[102:103], v[130:131] op_sel_hi:[1,0]
	v_pk_mul_f32 v[114:115], v[114:115], v[130:131] op_sel_hi:[1,0]
	v_pk_mul_f32 v[120:121], v[120:121], v[130:131] op_sel_hi:[1,0]
	s_waitcnt lgkmcnt(5)
	v_pk_fma_f32 v[10:11], v[10:11], v[82:83], v[42:43]
	s_waitcnt lgkmcnt(4)
	v_pk_fma_f32 v[14:15], v[14:15], v[112:113], v[46:47]
	v_cvt_pk_fp8_f32 v36, v2, v3
	v_cvt_pk_fp8_f32 v37, v6, v7
	v_mov_b32_e32 v38, 0
	v_mov_b32_e32 v39, 0
	v_pk_mul_f32 v[122:123], v[122:123], v[130:131] op_sel_hi:[1,0]
	v_pk_mul_f32 v[128:129], v[128:129], v[130:131] op_sel_hi:[1,0]
	v_pk_fma_f32 v[8:9], v[8:9], v[102:103], v[40:41]
	s_waitcnt lgkmcnt(3)
	v_pk_fma_f32 v[18:19], v[18:19], v[114:115], v[50:51]
	s_waitcnt lgkmcnt(2)
	v_pk_fma_f32 v[22:23], v[120:121], v[22:23], v[70:71]
	v_cvt_pk_fp8_f32 v38, v10, v11
	v_cvt_pk_fp8_f32 v39, v14, v15
	v_mov_b32_e32 v40, 0
	v_mov_b32_e32 v41, 0
	s_waitcnt lgkmcnt(1)
	v_pk_fma_f32 v[26:27], v[122:123], v[26:27], v[74:75]
	s_waitcnt lgkmcnt(0)
	v_pk_fma_f32 v[30:31], v[128:129], v[30:31], v[78:79]
	v_cvt_pk_fp8_f32 v40, v18, v19
	v_cvt_pk_fp8_f32 v41, v22, v23
	v_mov_b32_e32 v42, 0
	v_mov_b32_e32 v43, 0
	v_pk_mul_f32 v[104:105], v[104:105], v[130:131] op_sel_hi:[1,0]
	v_pk_mul_f32 v[110:111], v[110:111], v[130:131] op_sel_hi:[1,0]
	v_cvt_pk_fp8_f32 v42, v26, v27
	v_cvt_pk_fp8_f32 v43, v30, v31
	v_pk_mul_f32 v[116:117], v[116:117], v[130:131] op_sel_hi:[1,0]
	v_pk_mul_f32 v[118:119], v[118:119], v[130:131] op_sel_hi:[1,0]
	v_pk_fma_f32 v[12:13], v[12:13], v[104:105], v[44:45]
	v_pk_fma_f32 v[16:17], v[16:17], v[110:111], v[48:49]
	v_cvt_pk_fp8_f32 v36, v4, v5 op_sel:[0,0,1]
	v_cvt_pk_fp8_f32 v37, v8, v9 op_sel:[0,0,1]
	v_pk_mul_f32 v[124:125], v[124:125], v[130:131] op_sel_hi:[1,0]
	v_pk_mul_f32 v[126:127], v[126:127], v[130:131] op_sel_hi:[1,0]
	v_pk_fma_f32 v[20:21], v[20:21], v[116:117], v[52:53]
	v_pk_fma_f32 v[24:25], v[118:119], v[24:25], v[72:73]
	v_cvt_pk_fp8_f32 v38, v12, v13 op_sel:[0,0,1]
	v_cvt_pk_fp8_f32 v39, v16, v17 op_sel:[0,0,1]
	v_pk_fma_f32 v[28:29], v[124:125], v[28:29], v[76:77]
	v_pk_fma_f32 v[32:33], v[126:127], v[32:33], v[80:81]
	v_cvt_pk_fp8_f32 v40, v20, v21 op_sel:[0,0,1]
	v_cvt_pk_fp8_f32 v41, v24, v25 op_sel:[0,0,1]
	v_lshl_add_u64 v[34:35], v[62:63], 0, s[38:39]
	v_cvt_pk_fp8_f32 v42, v28, v29 op_sel:[0,0,1]
	v_cvt_pk_fp8_f32 v43, v32, v33 op_sel:[0,0,1]
	global_store_dwordx2 v[34:35], v[36:37], off
	global_store_dwordx2 v[34:35], v[38:39], off offset:512
	global_store_dwordx2 v[34:35], v[40:41], off offset:1024
	global_store_dwordx2 v[34:35], v[42:43], off offset:1536
	v_add_u32_e32 v34, s18, v1
	v_mov_b32_e32 v102, v93
	v_mov_b64_e32 v[74:75], v[64:65]
	v_mov_b32_e32 v69, v68
	v_mov_b32_e32 v38, v68
	v_mov_b32_e32 v39, v68
	v_mov_b32_e32 v40, v68
	v_mov_b32_e32 v41, v68
	v_mov_b32_e32 v42, v68
	v_mov_b32_e32 v43, v68
	v_mov_b32_e32 v44, v68
	v_mov_b32_e32 v45, v68
	v_mov_b32_e32 v46, v68
	v_mov_b32_e32 v47, v68
	v_mov_b32_e32 v48, v68
	v_mov_b32_e32 v49, v68
	v_mov_b32_e32 v50, v68
	v_mov_b32_e32 v51, v68
	v_mov_b32_e32 v52, v68
	v_mov_b32_e32 v53, v68
	v_mov_b32_e32 v70, v68
	v_mov_b32_e32 v71, v68
	v_mov_b32_e32 v72, v68
	v_mov_b32_e32 v73, v68
	v_mov_b32_e32 v76, v68
	v_mov_b32_e32 v77, v68
	v_mov_b32_e32 v78, v68
	v_mov_b32_e32 v79, v68
	v_mov_b32_e32 v80, v68
	v_mov_b32_e32 v81, v68
	v_mov_b32_e32 v82, v68
	v_mov_b32_e32 v83, v68
	v_mov_b32_e32 v84, v68
	v_mov_b32_e32 v85, v68
	ds_write_b128 v34, v[2:5]
	ds_write_b128 v34, v[6:9] offset:16
	ds_write_b128 v34, v[10:13] offset:2048
	ds_write_b128 v34, v[14:17] offset:2064
	ds_write_b128 v34, v[18:21] offset:4096
	ds_write_b128 v34, v[22:25] offset:4112
	ds_write_b128 v34, v[26:29] offset:6144
	ds_write_b128 v34, v[30:33] offset:6160
	s_waitcnt lgkmcnt(0)
	s_barrier

; #define LAS __attribute__((address_space(3)))
; __device__ __forceinline__ void hyprep_unit(Ctx& C, int l, int uidx) {
;     ...
;         for (int i = 0; i < 5; ++i) { const int idx0 = C.tid + 512 * i, idx = idx0 < 66 * 32 ? idx0 : 66 * 32 - 1, r = idx >> 5, ch = idx & 31, t = t0 - 1 + r; const bool ok = t >= 0 && t < L;
;             const int tc = t < 0 ? 0 : (t < L ? t : L - 1);
;             v[i] = *(const u32x4*)(Z + (size_t)(rowbase + tc) * INW + 1280 + 256 * cb + 8 * ch); if (!ok) v[i] = (u32x4){0u, 0u, 0u, 0u}; }
; #pragma unroll
;         for (int i = 0; i < 5; ++i) { const int idx0 = C.tid + 512 * i, idx = idx0 < 66 * 32 ? idx0 : 66 * 32 - 1, r = idx >> 5, ch = idx & 31;
;             if (i < 4 || idx0 < 66 * 32) *(LAS u32x4*)(C.lds + r * RS + ch * 16) = v[i]; } }
;     ...
;     const float w0 = INP(I_HCW)[(l * 3 + 0) * 1536 + ch], w1 = INP(I_HCW)[(l * 3 + 1) * 1536 + ch], w2 = INP(I_HCW)[(l * 3 + 2) * 1536 + ch], bias = INP(I_HCB)[l * 1536 + ch];
.LBB0_1716:
	s_or_b64 exec, exec, s[8:9]
	s_and_b64 vcc, exec, s[6:7]
	s_cbranch_vccnz .LBB0_1951
	v_mov_b32_e32 v172, v1
	s_mov_b64 s[6:7], s[20:21]
	s_mov_b32 s8, s3
	s_mov_b64 s[46:47], s[14:15]
	s_mov_b32 s9, s39
	s_mov_b64 s[48:49], s[16:17]
	s_cmpk_gt_i32 s56, 0xff
	v_and_b32_e32 v160, 63, v172
	v_readfirstlane_b32 s57, v172
	s_mov_b64 s[6:7], -1
	s_cbranch_scc0 .LBB0_1735
	s_cmpk_gt_u32 s56, 0x1ff
	s_cbranch_scc0 .LBB0_1732
	s_cmpk_gt_u32 s56, 0x3ff
	s_cbranch_scc0 .LBB0_1723
	s_add_i32 s6, s56, 0xfc00
	s_and_b32 s7, s6, 0xffff
	s_mul_i32 s7, s7, 0xaaab
	s_lshr_b32 s7, s7, 24
	s_mul_i32 s8, s7, 0x180
	s_sub_i32 s6, s6, s8
	s_lshl_b32 s18, s7, 12
	s_and_b32 s7, s6, 0xffff
	s_mul_i32 s7, s7, 0xaaab
	s_lshr_b32 s7, s7, 18
	s_mul_i32 s8, s7, 6
	s_lshl_b32 s19, s7, 6
	v_min_i32_e32 v2, 0x63f, v172
	s_sub_i32 s9, s6, s8
	s_load_dwordx2 s[10:11], s[48:49], 0x60
	v_and_b32_e32 v60, 0xff, v172
	v_lshl_or_b32 v60, s9, 8, v60
	v_and_b32_e32 v60, 0xffff, v60
	v_lshlrev_b32_e32 v60, 2, v60
	s_and_b32 s8, s19, 0xffc0
	v_add_u32_e32 v4, 0x200, v2
	s_add_i32 s8, s8, -1
	v_ashrrev_i32_e32 v26, 5, v4
	v_min_i32_e32 v8, 0x43f, v172
	v_add_u32_e32 v27, s8, v26
	v_add_u32_e32 v6, 0x400, v8
	v_med3_i32 v4, v27, 0, v166
	v_ashrrev_i32_e32 v28, 5, v6
	v_or_b32_e32 v4, s18, v4
	v_mov_b64_e32 v[16:17], s[46:47]
	v_add_u32_e32 v29, s8, v28
	v_mad_u64_u32 v[4:5], s[6:7], v4, s63, v[16:17]
	v_med3_i32 v6, v29, 0, v166
	s_lshl_b32 s6, s9, 9
	v_or_b32_e32 v6, s18, v6
	s_and_b32 s26, s6, 0x1fe00
	v_mad_u64_u32 v[6:7], s[6:7], v6, s63, v[16:17]
	v_lshlrev_b32_e32 v8, 4, v8
	v_add_u32_e32 v57, 0x4000, v60
	v_add_u32_e32 v58, 0x6000, v60
	v_add_u32_e32 v59, 0x7000, v60
	s_waitcnt lgkmcnt(0)
	global_load_dword v61, v57, s[10:11] offset:2048
	global_load_dword v62, v58, s[10:11]
	global_load_dword v63, v59, s[10:11] offset:2048
	v_min_i32_e32 v14, 0x23f, v172
	v_lshl_add_u64 v[6:7], v[6:7], 0, s[26:27]
	v_and_b32_e32 v20, 0x1f0, v8
	v_mov_b32_e32 v21, v3
	v_add_u32_e32 v12, 0x600, v14
	v_lshl_add_u64 v[6:7], v[6:7], 0, v[20:21]
	v_ashrrev_i32_e32 v21, 5, v12
	v_add_u32_e32 v30, s8, v21
	v_med3_i32 v12, v30, 0, v166
	v_or_b32_e32 v12, s18, v12
	v_lshlrev_b32_e32 v2, 4, v2
	v_mad_u64_u32 v[12:13], s[6:7], v12, s63, v[16:17]
	v_lshlrev_b32_e32 v14, 4, v14
	v_lshl_add_u64 v[4:5], v[4:5], 0, s[26:27]
	v_and_b32_e32 v2, 0x1f0, v2
	v_lshl_add_u64 v[12:13], v[12:13], 0, s[26:27]
	v_and_b32_e32 v22, 0x1f0, v14
	v_mov_b32_e32 v23, v3
	v_min_i32_e32 v18, 0x83f, v172
	v_lshl_add_u64 v[4:5], v[4:5], 0, v[2:3]
	v_lshl_add_u64 v[12:13], v[12:13], 0, v[22:23]
	v_ashrrev_i32_e32 v23, 5, v18
	v_add_co_u32_e32 v4, vcc, s64, v4
	v_add_u32_e32 v31, s8, v23
	s_nop 0
	v_addc_co_u32_e32 v5, vcc, 0, v5, vcc
	v_med3_i32 v19, v31, 0, v166
	v_add_co_u32_e32 v8, vcc, s64, v6
	v_or_b32_e32 v19, s18, v19
	s_nop 0
	v_addc_co_u32_e32 v9, vcc, 0, v7, vcc
	v_mad_u64_u32 v[16:17], s[6:7], v19, s63, v[16:17]
	s_load_dwordx2 s[6:7], s[48:49], 0x68
	v_lshlrev_b32_e32 v18, 4, v18
	v_add_co_u32_e32 v12, vcc, s64, v12
	v_lshl_add_u64 v[16:17], v[16:17], 0, s[26:27]
	v_and_b32_e32 v24, 0x1f0, v18
	v_mov_b32_e32 v25, v3
	v_addc_co_u32_e32 v13, vcc, 0, v13, vcc
	v_lshl_add_u64 v[16:17], v[16:17], 0, v[24:25]
	v_min_i32_e32 v52, 63, v172
	v_add_u32_e32 v53, 0x800, v52
	v_ashrrev_i32_e32 v53, 5, v53
	v_add_u32_e32 v56, s8, v53
	v_med3_i32 v53, v56, 0, v166
	v_or_b32_e32 v53, s18, v53
	v_mov_b64_e32 v[54:55], s[46:47]
	v_mad_u64_u32 v[54:55], vcc, v53, s63, v[54:55]
	v_lshlrev_b32_e32 v52, 4, v52
	v_lshl_add_u64 v[54:55], v[54:55], 0, s[26:27]
	v_and_b32_e32 v52, 0x1f0, v52
	v_mov_b32_e32 v53, v3
	v_lshl_add_u64 v[54:55], v[54:55], 0, v[52:53]
	v_add_co_u32_e32 v54, vcc, s64, v54
	s_nop 1
	v_addc_co_u32_e32 v55, vcc, 0, v55, vcc
	s_waitcnt lgkmcnt(0)
	v_add_u32_e32 v65, 0x1000, v60
	global_load_dword v64, v65, s[6:7] offset:2048
	s_barrier
	global_load_dwordx4 v[4:7], v[4:5], off offset:2560
	s_nop 0
	global_load_dwordx4 v[8:11], v[8:9], off offset:2560
	v_add_co_u32_e32 v16, vcc, s64, v16
	global_load_dwordx4 v[12:15], v[12:13], off offset:2560
	s_nop 0
	v_addc_co_u32_e32 v17, vcc, 0, v17, vcc
	global_load_dwordx4 v[16:19], v[16:17], off offset:2560
	global_load_dwordx4 v[66:69], v[54:55], off offset:2560
	v_cmp_gt_u32_e32 vcc, s62, v27
	v_mul_lo_u32 v23, v23, s66
	v_add3_u32 v23, 0, v23, v24
	s_lshl_b32 s34, s9, 8
	s_waitcnt vmcnt(4)
	v_cndmask_b32_e32 v7, 0, v7, vcc
	v_cndmask_b32_e32 v6, 0, v6, vcc
	v_cndmask_b32_e32 v5, 0, v5, vcc
	v_cndmask_b32_e32 v4, 0, v4, vcc
	v_cmp_gt_u32_e32 vcc, s62, v29
	s_waitcnt vmcnt(3)
	s_nop 0
	v_cndmask_b32_e32 v11, 0, v11, vcc
	v_cndmask_b32_e32 v10, 0, v10, vcc
	v_cndmask_b32_e32 v9, 0, v9, vcc
	v_cndmask_b32_e32 v8, 0, v8, vcc
	v_cmp_gt_u32_e32 vcc, s62, v30
	s_waitcnt vmcnt(2)
	s_nop 0
	v_cndmask_b32_e32 v15, 0, v15, vcc
	v_cndmask_b32_e32 v14, 0, v14, vcc
	v_cndmask_b32_e32 v13, 0, v13, vcc
	v_cndmask_b32_e32 v12, 0, v12, vcc
	v_cmp_gt_u32_e32 vcc, s62, v31
	s_waitcnt vmcnt(1)
	s_nop 0
	v_cndmask_b32_e32 v19, 0, v19, vcc
	v_cndmask_b32_e32 v18, 0, v18, vcc
	v_cndmask_b32_e32 v17, 0, v17, vcc
	v_cndmask_b32_e32 v16, 0, v16, vcc
	ds_write_b128 v23, v[16:19]
	v_mul_lo_u32 v16, v26, s66
	v_add3_u32 v2, 0, v16, v2
	ds_write_b128 v2, v[4:7]
	v_mul_lo_u32 v2, v28, s66
	v_add3_u32 v2, 0, v2, v20
	ds_write_b128 v2, v[8:11]
	v_mul_lo_u32 v2, v21, s66
	v_add3_u32 v2, 0, v2, v22
	v_cmp_gt_i32_e32 vcc, 64, v172
	ds_write_b128 v2, v[12:15]
	s_and_saveexec_b64 s[6:7], vcc
	s_cbranch_execz .LBB0_1722
	v_add_u32_e32 v2, 0x800, v172
	v_cmp_gt_u32_e32 vcc, s62, v56
	v_ashrrev_i32_e32 v2, 5, v2
	v_lshlrev_b32_e32 v8, 4, v172
	v_mul_lo_u32 v2, v2, s66
	v_and_b32_e32 v8, 0x1f0, v8
	v_add3_u32 v2, 0, v2, v8
	s_waitcnt vmcnt(0)
	v_cndmask_b32_e32 v69, 0, v69, vcc
	v_cndmask_b32_e32 v68, 0, v68, vcc
	v_cndmask_b32_e32 v67, 0, v67, vcc
	v_cndmask_b32_e32 v66, 0, v66, vcc
	ds_write_b128 v2, v[66:69]
; #define LAS __attribute__((address_space(3)))
; __device__ __forceinline__ unsigned pk2(float lo, float hi) { f32x2 v = {lo, hi}; bf16x2_t b = __builtin_convertvector(v, bf16x2_t); return __builtin_bit_cast(unsigned, b); }
; __device__ __forceinline__ float bf1(bf16 v) { return __uint_as_float(((unsigned)v) << 16); }
; __device__ __forceinline__ void hyprep_unit(Ctx& C, int l, int uidx) {
;     ...
;     __syncthreads();
;     const int c = C.tid & 255, hf = C.tid >> 8, ch = 256 * cb + c, comp = ch >> 9, cc = ch & 511;
;     const float w0 = INP(I_HCW)[(l * 3 + 0) * 1536 + ch], w1 = INP(I_HCW)[(l * 3 + 1) * 1536 + ch], w2 = INP(I_HCW)[(l * 3 + 2) * 1536 + ch], bias = INP(I_HCB)[l * 1536 + ch];
;     bf16* dst = T + ((size_t)(comp * 512 + cc) * 4 + seq) * L + t0 + 32 * hf;
;     float zm = bf1(*(const LAS bf16*)(C.lds + (32 * hf) * RS + c * 2)), zc = bf1(*(const LAS bf16*)(C.lds + (32 * hf + 1) * RS + c * 2));
; #pragma unroll
;     for (int k = 0; k < 4; ++k) { float o[8];
; #pragma unroll
;         for (int e = 0; e < 8; ++e) { const float zn = bf1(*(const LAS bf16*)(C.lds + (32 * hf + 8 * k + e + 2) * RS + c * 2)); o[e] = bias + w0 * zm + w1 * zc + w2 * zn; zm = zc; zc = zn; }
;         u32x4 w; w.x = pk2(o[0], o[1]); w.y = pk2(o[2], o[3]); w.z = pk2(o[4], o[5]); w.w = pk2(o[6], o[7]); *(u32x4*)(dst + 8 * k) = w; }
.LBB0_1722:
	s_or_b64 exec, exec, s[6:7]
	s_waitcnt vmcnt(0) lgkmcnt(0)
	s_barrier
	s_and_b32 s6, 0xffff, s34
	v_or_b32_sdwa v14, v172, s6 dst_sel:DWORD dst_unused:UNUSED_PAD src0_sel:BYTE_0 src1_sel:DWORD
	v_mov_b32_e32 v4, v61
	v_mov_b32_e32 v6, v64
	v_mov_b32_e32 v8, v62
	v_mov_b32_e32 v10, v63
	v_ashrrev_i32_e32 v5, 3, v172
	v_and_b32_e32 v12, 0xffffffe0, v5
	v_lshlrev_b32_sdwa v7, v167, v172 dst_sel:DWORD dst_unused:UNUSED_PAD src0_sel:DWORD src1_sel:BYTE_0
	v_mul_lo_u32 v9, v12, s66
	v_add3_u32 v9, 0, v9, v7
	ds_read_u16 v11, v9 offset:4752
	ds_read_u16 v40, v9 offset:7392
	ds_read_u16 v41, v9 offset:7920
	ds_read_u16 v42, v9 offset:6336
	ds_read_u16 v43, v9 offset:6864
	ds_read_u16 v44, v9 offset:5280
	ds_read_u16 v45, v9 offset:5808
	ds_read_u16 v19, v9 offset:4224
	ds_read_u16 v18, v9 offset:3168
	ds_read_u16 v20, v9 offset:3696
	ds_read_u16 v22, v9 offset:2112
	ds_read_u16 v21, v9 offset:2640
	ds_read_u16 v24, v9 offset:1056
	ds_read_u16 v23, v9 offset:1584
	ds_read_u16 v26, v9
	ds_read_u16 v25, v9 offset:528
	v_lshlrev_b32_e32 v2, 14, v14
	s_and_b32 s8, 0xffff, s19
	v_add_lshl_u32 v2, v2, s18, 1
	s_lshl_b32 s26, s8, 1
	v_lshl_add_u64 v[14:15], s[46:47], 0, v[2:3]
	v_ashrrev_i32_e32 v13, 31, v12
	v_lshl_add_u64 v[14:15], v[14:15], 0, s[26:27]
	v_lshl_add_u64 v[16:17], v[12:13], 1, v[14:15]
	s_waitcnt lgkmcnt(8)
	v_lshlrev_b32_e32 v14, 16, v19
	s_waitcnt lgkmcnt(6)
	v_lshlrev_b32_e32 v19, 16, v20
	s_waitcnt lgkmcnt(5)
	v_lshlrev_b32_e32 v20, 16, v22
	s_waitcnt lgkmcnt(2)
	v_lshlrev_b32_e32 v23, 16, v23
	v_lshlrev_b32_e32 v22, 16, v24
	s_waitcnt lgkmcnt(0)
	v_lshlrev_b32_e32 v25, 16, v25
	v_lshlrev_b32_e32 v24, 16, v26
	v_lshlrev_b32_e32 v18, 16, v18
	v_lshlrev_b32_e32 v21, 16, v21
	v_pk_mov_b32 v[28:29], v[24:25], v[22:23] op_sel:[1,0]
	v_mov_b32_e32 v26, v19
	v_mov_b32_e32 v27, v14
	v_pk_mov_b32 v[30:31], v[22:23], v[20:21] op_sel:[1,0]
	v_pk_mov_b32 v[32:33], v[20:21], v[18:19] op_sel:[1,0]
	v_lshlrev_b32_e32 v15, 16, v11
	s_mov_b64 s[6:7], 0x42400000
	v_lshl_add_u64 v[12:13], v[16:17], 0, s[6:7]
	s_mov_b32 s6, 0x42400000
	v_add_co_u32_e32 v16, vcc, s6, v16
	s_mov_b64 s[6:7], 0
	s_nop 0
	v_addc_co_u32_e32 v17, vcc, 0, v17, vcc
	s_waitcnt vmcnt(2)
	v_pk_fma_f32 v[24:25], v[4:5], v[24:25], v[6:7] op_sel_hi:[0,1,0]
	v_pk_fma_f32 v[34:35], v[4:5], v[22:23], v[6:7] op_sel_hi:[0,1,0]
	v_pk_fma_f32 v[36:37], v[4:5], v[20:21], v[6:7] op_sel_hi:[0,1,0]
	v_pk_fma_f32 v[38:39], v[4:5], v[18:19], v[6:7] op_sel_hi:[0,1,0]
	s_waitcnt vmcnt(1)
	v_pk_fma_f32 v[24:25], v[8:9], v[28:29], v[24:25] op_sel_hi:[0,1,1]
	v_pk_fma_f32 v[28:29], v[8:9], v[30:31], v[34:35] op_sel_hi:[0,1,1]
	v_pk_fma_f32 v[30:31], v[8:9], v[32:33], v[36:37] op_sel_hi:[0,1,1]
	v_pk_fma_f32 v[26:27], v[8:9], v[26:27], v[38:39] op_sel_hi:[0,1,1]
	s_waitcnt vmcnt(0)
	v_pk_fma_f32 v[22:23], v[10:11], v[22:23], v[24:25] op_sel_hi:[0,1,1]
	v_pk_fma_f32 v[20:21], v[10:11], v[20:21], v[28:29] op_sel_hi:[0,1,1]
	v_pk_fma_f32 v[24:25], v[10:11], v[18:19], v[30:31] op_sel_hi:[0,1,1]
	v_pk_fma_f32 v[26:27], v[10:11], v[14:15], v[26:27] op_sel_hi:[0,1,1]
	v_cvt_pk_bf16_f32 v18, v22, v23
	ds_read_u16 v2, v9 offset:8976
	ds_read_u16 v11, v9 offset:11616
	ds_read_u16 v28, v9 offset:12144
	ds_read_u16 v29, v9 offset:10560
	ds_read_u16 v30, v9 offset:11088
	ds_read_u16 v31, v9 offset:9504
	ds_read_u16 v32, v9 offset:10032
	ds_read_u16 v22, v9 offset:8448
	v_cvt_pk_bf16_f32 v19, v20, v21
	v_cvt_pk_bf16_f32 v20, v24, v25
	v_lshlrev_b32_e32 v25, 16, v45
	v_lshlrev_b32_e32 v24, 16, v44
	v_cvt_pk_bf16_f32 v21, v26, v27
	v_pk_fma_f32 v[26:27], v[4:5], v[14:15], v[6:7] op_sel_hi:[0,1,0]
	v_pk_mov_b32 v[14:15], v[14:15], v[24:25] op_sel:[1,0]
	global_store_dwordx4 v[16:17], v[18:21], off
	v_lshlrev_b32_e32 v23, 16, v43
	v_pk_fma_f32 v[14:15], v[8:9], v[14:15], v[26:27] op_sel_hi:[0,1,1]
	s_waitcnt lgkmcnt(0)
	v_lshlrev_b32_e32 v18, 16, v22
	v_lshlrev_b32_e32 v22, 16, v42
	v_pk_fma_f32 v[14:15], v[10:11], v[24:25], v[14:15] op_sel_hi:[0,1,1]
	v_pk_fma_f32 v[26:27], v[4:5], v[24:25], v[6:7] op_sel_hi:[0,1,0]
	v_pk_mov_b32 v[24:25], v[24:25], v[22:23] op_sel:[1,0]
	v_lshlrev_b32_e32 v16, 16, v40
	v_pk_fma_f32 v[24:25], v[8:9], v[24:25], v[26:27] op_sel_hi:[0,1,1]
	v_lshlrev_b32_e32 v17, 16, v41
	v_pk_fma_f32 v[24:25], v[10:11], v[22:23], v[24:25] op_sel_hi:[0,1,1]
	v_lshlrev_b32_e32 v19, 16, v2
	v_pk_fma_f32 v[26:27], v[4:5], v[22:23], v[6:7] op_sel_hi:[0,1,0]
	v_pk_mov_b32 v[22:23], v[22:23], v[16:17] op_sel:[1,0]
	v_cvt_pk_bf16_f32 v14, v14, v15
	v_cvt_pk_bf16_f32 v15, v24, v25
	ds_read_u16 v2, v9 offset:13200
	ds_read_u16 v33, v9 offset:15840
	ds_read_u16 v34, v9 offset:16368
	ds_read_u16 v35, v9 offset:14784
	ds_read_u16 v36, v9 offset:15312
	ds_read_u16 v37, v9 offset:13728
	ds_read_u16 v38, v9 offset:14256
	ds_read_u16 v24, v9 offset:12672
	v_pk_fma_f32 v[22:23], v[8:9], v[22:23], v[26:27] op_sel_hi:[0,1,1]
	v_mov_b32_e32 v20, v17
	v_mov_b32_e32 v21, v18
	v_pk_fma_f32 v[22:23], v[10:11], v[16:17], v[22:23] op_sel_hi:[0,1,1]
	v_pk_fma_f32 v[16:17], v[4:5], v[16:17], v[6:7] op_sel_hi:[0,1,0]
	v_pk_fma_f32 v[16:17], v[8:9], v[20:21], v[16:17] op_sel_hi:[0,1,1]
	v_pk_fma_f32 v[20:21], v[10:11], v[18:19], v[16:17] op_sel_hi:[0,1,1]
	v_cvt_pk_bf16_f32 v17, v20, v21
	s_waitcnt lgkmcnt(0)
; #define LAS __attribute__((address_space(3)))
; __device__ __forceinline__ unsigned pk2(float lo, float hi) { f32x2 v = {lo, hi}; bf16x2_t b = __builtin_convertvector(v, bf16x2_t); return __builtin_bit_cast(unsigned, b); }
; __device__ __forceinline__ float bf1(bf16 v) { return __uint_as_float(((unsigned)v) << 16); }
; __device__ __forceinline__ void hyprep_unit(Ctx& C, int l, int uidx) {
;     ...
;     float zm = bf1(*(const LAS bf16*)(C.lds + (32 * hf) * RS + c * 2)), zc = bf1(*(const LAS bf16*)(C.lds + (32 * hf + 1) * RS + c * 2));
; #pragma unroll
;     for (int k = 0; k < 4; ++k) { float o[8];
; #pragma unroll
;         for (int e = 0; e < 8; ++e) { const float zn = bf1(*(const LAS bf16*)(C.lds + (32 * hf + 8 * k + e + 2) * RS + c * 2)); o[e] = bias + w0 * zm + w1 * zc + w2 * zn; zm = zc; zc = zn; }
;         u32x4 w; w.x = pk2(o[0], o[1]); w.y = pk2(o[2], o[3]); w.z = pk2(o[4], o[5]); w.w = pk2(o[6], o[7]); *(u32x4*)(dst + 8 * k) = w; }
	v_lshlrev_b32_e32 v20, 16, v24
	v_lshlrev_b32_e32 v25, 16, v32
	v_lshlrev_b32_e32 v24, 16, v31
	v_pk_fma_f32 v[26:27], v[4:5], v[18:19], v[6:7] op_sel_hi:[0,1,0]
	v_pk_mov_b32 v[18:19], v[18:19], v[24:25] op_sel:[1,0]
	v_cvt_pk_bf16_f32 v16, v22, v23
	v_lshlrev_b32_e32 v23, 16, v30
	v_lshlrev_b32_e32 v22, 16, v29
	v_pk_fma_f32 v[18:19], v[8:9], v[18:19], v[26:27] op_sel_hi:[0,1,1]
	v_pk_fma_f32 v[18:19], v[10:11], v[24:25], v[18:19] op_sel_hi:[0,1,1]
	v_pk_fma_f32 v[26:27], v[4:5], v[24:25], v[6:7] op_sel_hi:[0,1,0]
	v_pk_mov_b32 v[24:25], v[24:25], v[22:23] op_sel:[1,0]
	global_store_dwordx4 v[12:13], v[14:17], off offset:16
	v_lshlrev_b32_e32 v21, 16, v2
	v_pk_fma_f32 v[24:25], v[8:9], v[24:25], v[26:27] op_sel_hi:[0,1,1]
	v_lshlrev_b32_e32 v14, 16, v11
	v_lshlrev_b32_e32 v15, 16, v28
	v_or_b32_e32 v2, 31, v5
	v_pk_fma_f32 v[24:25], v[10:11], v[22:23], v[24:25] op_sel_hi:[0,1,1]
	v_pk_fma_f32 v[26:27], v[4:5], v[22:23], v[6:7] op_sel_hi:[0,1,0]
	v_pk_mov_b32 v[22:23], v[22:23], v[14:15] op_sel:[1,0]
	v_mul_lo_u32 v2, v2, s66
	v_pk_fma_f32 v[22:23], v[8:9], v[22:23], v[26:27] op_sel_hi:[0,1,1]
	v_add3_u32 v2, 0, v2, v7
	v_mov_b32_e32 v16, v15
	v_pk_fma_f32 v[22:23], v[10:11], v[14:15], v[22:23] op_sel_hi:[0,1,1]
	v_pk_fma_f32 v[14:15], v[4:5], v[14:15], v[6:7] op_sel_hi:[0,1,0]
	ds_read_u16 v5, v9 offset:16896
	ds_read_u16 v2, v2 offset:1056
	v_mov_b32_e32 v17, v20
	v_pk_fma_f32 v[14:15], v[8:9], v[16:17], v[14:15] op_sel_hi:[0,1,1]
	v_pk_fma_f32 v[26:27], v[10:11], v[20:21], v[14:15] op_sel_hi:[0,1,1]
	v_cvt_pk_bf16_f32 v15, v24, v25
	v_lshlrev_b32_e32 v25, 16, v38
	v_lshlrev_b32_e32 v24, 16, v37
	v_cvt_pk_bf16_f32 v17, v26, v27
	s_waitcnt lgkmcnt(1)
	v_pk_fma_f32 v[26:27], v[4:5], v[20:21], v[6:7] op_sel_hi:[0,1,0]
	v_pk_mov_b32 v[20:21], v[20:21], v[24:25] op_sel:[1,0]
	v_cvt_pk_bf16_f32 v16, v22, v23
	v_lshlrev_b32_e32 v23, 16, v36
	v_lshlrev_b32_e32 v22, 16, v35
	v_pk_fma_f32 v[20:21], v[8:9], v[20:21], v[26:27] op_sel_hi:[0,1,1]
	v_cvt_pk_bf16_f32 v14, v18, v19
	v_pk_fma_f32 v[20:21], v[10:11], v[24:25], v[20:21] op_sel_hi:[0,1,1]
	v_pk_fma_f32 v[26:27], v[4:5], v[24:25], v[6:7] op_sel_hi:[0,1,0]
	v_pk_mov_b32 v[24:25], v[24:25], v[22:23] op_sel:[1,0]
	global_store_dwordx4 v[12:13], v[14:17], off offset:32
	v_pk_fma_f32 v[24:25], v[8:9], v[24:25], v[26:27] op_sel_hi:[0,1,1]
	v_lshlrev_b32_e32 v19, 16, v5
	v_lshlrev_b32_e32 v14, 16, v33
	v_lshlrev_b32_e32 v15, 16, v34
	v_mov_b32_e32 v18, v15
	v_pk_fma_f32 v[24:25], v[10:11], v[22:23], v[24:25] op_sel_hi:[0,1,1]
	v_pk_fma_f32 v[26:27], v[4:5], v[22:23], v[6:7] op_sel_hi:[0,1,0]
	v_pk_mov_b32 v[22:23], v[22:23], v[14:15] op_sel:[1,0]
	v_pk_fma_f32 v[4:5], v[4:5], v[14:15], v[6:7] op_sel_hi:[0,1,0]
	s_waitcnt lgkmcnt(0)
	v_lshlrev_b32_e32 v17, 16, v2
	v_pk_fma_f32 v[22:23], v[8:9], v[22:23], v[26:27] op_sel_hi:[0,1,1]
	v_mov_b32_e32 v16, v19
	v_pk_fma_f32 v[4:5], v[8:9], v[18:19], v[4:5] op_sel_hi:[0,1,1]
	v_pk_fma_f32 v[22:23], v[10:11], v[14:15], v[22:23] op_sel_hi:[0,1,1]
	v_pk_fma_f32 v[8:9], v[10:11], v[16:17], v[4:5] op_sel_hi:[0,1,1]
	v_cvt_pk_bf16_f32 v4, v20, v21
	v_cvt_pk_bf16_f32 v5, v24, v25
	v_cvt_pk_bf16_f32 v6, v22, v23
	v_cvt_pk_bf16_f32 v7, v8, v9
	global_store_dwordx4 v[12:13], v[4:7], off offset:48
; #define LAS __attribute__((address_space(3)))
; #define MFMA32(a, b, c) __builtin_amdgcn_mfma_f32_32x32x16_bf16((a), (b), (c), 0, 0, 0)
; __device__ __forceinline__ void pool_unit(Ctx& C, int l, int blk) {
;     ...
;     { u32x4 v[6];
; #pragma unroll
;         for (int i = 0; i < 6; ++i) { const int idx = C.tid + 512 * i, r = idx >> 6, ch = idx & 63, t = t0 - 8 + r; const bool ok = t >= 0 && t < L; const int tc = t < 0 ? 0 : (t < L ? t : L - 1);
;             v[i] = *(const u32x4*)(Z + (size_t)(s0 + tc) * INW + 8 * ch); if (!ok) v[i] = (u32x4){0u, 0u, 0u, 0u}; }
; #pragma unroll
;         for (int i = 0; i < 6; ++i) { const int idx = C.tid + 512 * i, r = idx >> 6, ch = idx & 63; *(LAS u32x4*)(C.lds + r * RS + ch * 16) = v[i]; } }
;     __syncthreads();
;     {
;         const int c8 = C.tid & 63, tg = C.tid >> 6, hw = 1 << (c8 >> 4);
;     ...
;     const bf16* wt = WSP(bf16, WS_POOLWT) + (size_t)((l * 4 + gi) * 128 + 64 * oh + r32) * 128 + 8 * h;
; #pragma unroll
;     for (int s = 0; s < 8; ++s) {
;         const bf16x8 Bf = *(const LAS bf16x8*)(C.lds + DT_OFF + r32 * RS + (128 * gi + 16 * s + 8 * h) * 2);
; #pragma unroll
;         for (int rb = 0; rb < 2; ++rb) { const bf16x8 Af = *(const bf16x8*)(wt + (size_t)(32 * rb) * 128 + 16 * s); acc[rb] = MFMA32(Af, Bf, acc[rb]); }
.LBB0_1723:
	s_and_b64 vcc, exec, s[6:7]
	s_cbranch_vccz .LBB0_1731
	s_lshl_b32 s6, s56, 5
	s_add_i32 s10, s6, 0xffffc000
	s_and_b32 s11, s10, 0xffffcfe0
	v_lshlrev_b32_e32 v2, 4, v172
	v_add_u32_e32 v6, 0x200, v172
	s_add_i32 s9, s11, -8
	v_and_b32_e32 v2, 0x3f0, v2
	v_ashrrev_i32_e32 v28, 6, v172
	v_ashrrev_i32_e32 v30, 6, v6
	s_and_b32 s8, s6, 0x3000
	v_lshl_add_u64 v[4:5], s[46:47], 0, v[2:3]
	s_mov_b64 s[6:7], 0x36000000
	v_add_u32_e32 v29, s9, v28
	v_add_u32_e32 v31, s9, v30
	v_lshl_add_u64 v[24:25], v[4:5], 0, s[6:7]
	v_med3_i32 v4, v29, 0, v166
	v_med3_i32 v6, v31, 0, v166
	v_or_b32_e32 v4, s8, v4
	v_or_b32_e32 v6, s8, v6
	v_add_u32_e32 v12, 0x400, v172
	v_add_u32_e32 v14, 0x600, v172
	v_mul_u32_u24_e32 v4, 0x1e00, v4
	v_mov_b32_e32 v5, v3
	v_mul_u32_u24_e32 v6, 0x1e00, v6
	v_mov_b32_e32 v7, v3
	v_ashrrev_i32_e32 v32, 6, v12
	v_ashrrev_i32_e32 v34, 6, v14
	v_lshl_add_u64 v[4:5], v[24:25], 0, v[4:5]
	v_lshl_add_u64 v[8:9], v[24:25], 0, v[6:7]
	v_add_u32_e32 v33, s9, v32
	v_add_u32_e32 v35, s9, v34
	s_waitcnt lgkmcnt(0)
	s_barrier
	global_load_dwordx4 v[4:7], v[4:5], off
	s_nop 0
	global_load_dwordx4 v[8:11], v[8:9], off
	v_med3_i32 v12, v33, 0, v166
	v_med3_i32 v14, v35, 0, v166
	v_add_u32_e32 v20, 0x800, v172
	v_or_b32_e32 v12, s8, v12
	v_or_b32_e32 v14, s8, v14
	v_ashrrev_i32_e32 v36, 6, v20
	v_mul_u32_u24_e32 v12, 0x1e00, v12
	v_mov_b32_e32 v13, v3
	v_mul_u32_u24_e32 v14, 0x1e00, v14
	v_mov_b32_e32 v15, v3
	v_add_u32_e32 v37, s9, v36
	v_add_u32_e32 v26, 0xa00, v172
	v_lshl_add_u64 v[12:13], v[24:25], 0, v[12:13]
	v_lshl_add_u64 v[16:17], v[24:25], 0, v[14:15]
	v_med3_i32 v20, v37, 0, v166
	v_ashrrev_i32_e32 v38, 6, v26
	global_load_dwordx4 v[12:15], v[12:13], off
	s_nop 0
	global_load_dwordx4 v[16:19], v[16:17], off
	v_or_b32_e32 v20, s8, v20
	v_add_u32_e32 v39, s9, v38
	v_mul_u32_u24_e32 v20, 0x1e00, v20
	v_mov_b32_e32 v21, v3
	v_med3_i32 v26, v39, 0, v166
	v_lshl_add_u64 v[20:21], v[24:25], 0, v[20:21]
	v_or_b32_e32 v26, s8, v26
	global_load_dwordx4 v[20:23], v[20:21], off
	v_mul_u32_u24_e32 v26, 0x1e00, v26
	v_mov_b32_e32 v27, v3
	v_lshl_add_u64 v[24:25], v[24:25], 0, v[26:27]
	global_load_dwordx4 v[24:27], v[24:25], off
	v_cmp_gt_u32_e32 vcc, s62, v29
	v_mul_lo_u32 v28, v28, s67
	v_add3_u32 v28, 0, v28, v2
	s_mul_i32 s6, s11, 0x410
	s_mov_b32 s18, 0
	s_waitcnt vmcnt(5)
	v_cndmask_b32_e32 v7, 0, v7, vcc
	v_cndmask_b32_e32 v6, 0, v6, vcc
	v_cndmask_b32_e32 v5, 0, v5, vcc
	v_cndmask_b32_e32 v4, 0, v4, vcc
	v_cmp_gt_u32_e32 vcc, s62, v31
	ds_write_b128 v28, v[4:7]
	v_mul_lo_u32 v4, v30, s67
	s_waitcnt vmcnt(4)
	v_cndmask_b32_e32 v11, 0, v11, vcc
	v_cndmask_b32_e32 v10, 0, v10, vcc
	v_cndmask_b32_e32 v9, 0, v9, vcc
	v_cndmask_b32_e32 v8, 0, v8, vcc
	v_add3_u32 v4, 0, v4, v2
	v_cmp_gt_u32_e32 vcc, s62, v33
	ds_write_b128 v4, v[8:11]
	v_mul_lo_u32 v4, v32, s67
	v_add3_u32 v4, 0, v4, v2
	s_waitcnt vmcnt(3)
	v_cndmask_b32_e32 v15, 0, v15, vcc
	v_cndmask_b32_e32 v14, 0, v14, vcc
	v_cndmask_b32_e32 v13, 0, v13, vcc
	v_cndmask_b32_e32 v12, 0, v12, vcc
	v_cmp_gt_u32_e32 vcc, s62, v35
	ds_write_b128 v4, v[12:15]
	v_mul_lo_u32 v4, v34, s67
	s_waitcnt vmcnt(2)
	v_cndmask_b32_e32 v19, 0, v19, vcc
	v_cndmask_b32_e32 v18, 0, v18, vcc
	v_cndmask_b32_e32 v17, 0, v17, vcc
	v_cndmask_b32_e32 v16, 0, v16, vcc
	v_add3_u32 v4, 0, v4, v2
	v_cmp_gt_u32_e32 vcc, s62, v37
	ds_write_b128 v4, v[16:19]
	v_mul_lo_u32 v4, v36, s67
	s_waitcnt vmcnt(1)
	v_cndmask_b32_e32 v23, 0, v23, vcc
	v_cndmask_b32_e32 v22, 0, v22, vcc
	v_cndmask_b32_e32 v21, 0, v21, vcc
	v_cndmask_b32_e32 v20, 0, v20, vcc
	v_add3_u32 v4, 0, v4, v2
	v_cmp_gt_u32_e32 vcc, s62, v39
	ds_write_b128 v4, v[20:23]
	v_mul_lo_u32 v4, v38, s67
	s_waitcnt vmcnt(0)
	v_cndmask_b32_e32 v27, 0, v27, vcc
	v_cndmask_b32_e32 v26, 0, v26, vcc
	v_cndmask_b32_e32 v25, 0, v25, vcc
	v_cndmask_b32_e32 v24, 0, v24, vcc
	v_add3_u32 v2, 0, v4, v2
	ds_write_b128 v2, v[24:27]
	v_lshrrev_b32_e32 v2, 4, v160
	v_lshlrev_b32_e64 v5, v2, 1
	v_ashrrev_i32_e32 v2, 4, v172
	v_and_b32_e32 v16, -4, v2
	v_lshlrev_b32_e32 v4, 4, v160
	v_add_u32_e32 v2, 0, v4
	v_subrev_u32_e32 v4, s6, v4
	v_add_u32_e32 v6, s11, v16
	v_add_u32_e32 v4, s68, v4
	v_sub_u32_e32 v17, v6, v5
	s_waitcnt lgkmcnt(0)
	s_barrier
	v_and_b32_e32 v128, 0xffffffdf, v172
	v_add_u32_e32 v128, 0x200, v128
	v_lshlrev_b32_e32 v128, 8, v128
	v_lshrrev_b32_e32 v129, 5, v160
	v_lshl_add_u32 v128, v129, 4, v128
	v_mov_b32_e32 v129, v3
	v_lshl_add_u64 v[128:129], s[46:47], 0, v[128:129]
	v_add_co_u32_e32 v130, vcc, 0x300000, v128
	s_nop 1
	v_addc_co_u32_e32 v131, vcc, 0, v129, vcc
	v_add_co_u32_e32 v132, vcc, 0x302000, v128
	s_nop 1
	v_addc_co_u32_e32 v133, vcc, 0, v129, vcc
	global_load_dwordx4 v[64:67], v[130:131], off
	global_load_dwordx4 v[68:71], v[132:133], off
	global_load_dwordx4 v[72:75], v[130:131], off offset:32
	global_load_dwordx4 v[76:79], v[132:133], off offset:32
	global_load_dwordx4 v[80:83], v[130:131], off offset:64
	global_load_dwordx4 v[84:87], v[132:133], off offset:64
	global_load_dwordx4 v[88:91], v[130:131], off offset:96
	global_load_dwordx4 v[92:95], v[132:133], off offset:96
	global_load_dwordx4 v[96:99], v[130:131], off offset:128
	global_load_dwordx4 v[100:103], v[132:133], off offset:128
	global_load_dwordx4 v[104:107], v[130:131], off offset:160
	global_load_dwordx4 v[108:111], v[132:133], off offset:160
	global_load_dwordx4 v[112:115], v[130:131], off offset:192
	global_load_dwordx4 v[116:119], v[132:133], off offset:192
	global_load_dwordx4 v[120:123], v[130:131], off offset:224
	global_load_dwordx4 v[124:127], v[132:133], off offset:224
	s_branch .LBB0_1726

; #define LAS __attribute__((address_space(3)))
; __device__ __forceinline__ unsigned pk2(float lo, float hi) { f32x2 v = {lo, hi}; bf16x2_t b = __builtin_convertvector(v, bf16x2_t); return __builtin_bit_cast(unsigned, b); }
; #define MFMA32(a, b, c) __builtin_amdgcn_mfma_f32_32x32x16_bf16((a), (b), (c), 0, 0, 0)
; __device__ __forceinline__ void pool_unit(Ctx& C, int l, int blk) {
;     ...
;     const int gi = C.wave >> 1, oh = C.wave & 1, r32 = C.lane & 31, h = C.lane >> 5;
;     f32x16 acc[2];
; #pragma unroll
;     for (int a = 0; a < 2; ++a)
; #pragma unroll
;         for (int i = 0; i < 16; ++i) acc[a][i] = 0.f;
;     const bf16* wt = WSP(bf16, WS_POOLWT) + (size_t)((l * 4 + gi) * 128 + 64 * oh + r32) * 128 + 8 * h;
; #pragma unroll
;     for (int s = 0; s < 8; ++s) {
;         const bf16x8 Bf = *(const LAS bf16x8*)(C.lds + DT_OFF + r32 * RS + (128 * gi + 16 * s + 8 * h) * 2);
; #pragma unroll
;         for (int rb = 0; rb < 2; ++rb) { const bf16x8 Af = *(const bf16x8*)(wt + (size_t)(32 * rb) * 128 + 16 * s); acc[rb] = MFMA32(Af, Bf, acc[rb]); }
;     }
;     bf16* yp = WSP(bf16, WS_YCAT) + (size_t)(row0 + r32) * DM + 128 * gi + 64 * oh;
; #pragma unroll
;     for (int rb = 0; rb < 2; ++rb)
; #pragma unroll
;         for (int rg = 0; rg < 4; ++rg) { u32x2 w; w.x = pk2(acc[rb][4 * rg], acc[rb][4 * rg + 1]); w.y = pk2(acc[rb][4 * rg + 2], acc[rb][4 * rg + 3]); *(u32x2*)(yp + 32 * rb + 8 * rg + 4 * h) = w; }
.LBB0_1730:
	s_and_b32 s6, s57, 0xffffff80
	s_and_b32 s8, s57, 64
	s_or_b32 s7, s6, s8
	v_and_b32_e32 v60, 31, v172
	s_addk_i32 s7, 0x200
	v_or_b32_e32 v4, s7, v60
	v_ashrrev_i32_e32 v5, 31, v4
	v_lshrrev_b32_e32 v2, 5, v160
	v_lshlrev_b64 v[4:5], 8, v[4:5]
	v_lshl_add_u64 v[4:5], s[46:47], 0, v[4:5]
	v_lshlrev_b32_e32 v6, 4, v2
	v_mov_b32_e32 v7, v3
	v_lshl_add_u64 v[12:13], v[4:5], 0, v[6:7]
	s_mov_b32 s7, 0x300000
	v_add_co_u32_e32 v4, vcc, s7, v12
	s_waitcnt lgkmcnt(0)
	s_nop 0
	v_addc_co_u32_e32 v5, vcc, 0, v13, vcc
	s_barrier
	s_waitcnt vmcnt(0)
	s_mov_b32 s7, 0x302000
	v_add_co_u32_e32 v56, vcc, s7, v12
	s_mov_b64 s[18:19], 0x300000
	s_nop 0
	v_addc_co_u32_e32 v57, vcc, 0, v13, vcc
	v_lshl_add_u64 v[58:59], v[12:13], 0, s[18:19]
	v_lshlrev_b32_e32 v2, 3, v2
	v_or_b32_e32 v15, s6, v2
	v_mul_u32_u24_e32 v14, 0x410, v60
	v_lshlrev_b32_e32 v15, 1, v15
	v_add3_u32 v61, 0, v14, v15
	ds_read_b128 v[12:15], v61 offset:49920
	ds_read_b128 v[40:43], v61 offset:49952
	s_ashr_i32 s7, s6, 31
	s_lshl_b32 s26, s8, 1
	s_mov_b64 s[18:19], 0x3e000000
	s_waitcnt lgkmcnt(1)
	v_mfma_f32_32x32x16_bf16 v[20:35], v[64:67], v[12:15], 0
	v_mfma_f32_32x32x16_bf16 v[4:19], v[68:71], v[12:15], 0
	s_waitcnt lgkmcnt(0)
	v_mfma_f32_32x32x16_bf16 v[20:35], v[72:75], v[40:43], v[20:35]
	v_mfma_f32_32x32x16_bf16 v[4:19], v[76:79], v[40:43], v[4:19]
	ds_read_b128 v[44:47], v61 offset:49984
	ds_read_b128 v[52:55], v61 offset:50016
	s_waitcnt lgkmcnt(1)
	v_mfma_f32_32x32x16_bf16 v[20:35], v[80:83], v[44:47], v[20:35]
	v_mfma_f32_32x32x16_bf16 v[4:19], v[84:87], v[44:47], v[4:19]
	s_waitcnt lgkmcnt(0)
	v_mfma_f32_32x32x16_bf16 v[20:35], v[88:91], v[52:55], v[20:35]
	v_mfma_f32_32x32x16_bf16 v[4:19], v[92:95], v[52:55], v[4:19]
	ds_read_b128 v[48:51], v61 offset:50048
	ds_read_b128 v[52:55], v61 offset:50080
	s_waitcnt lgkmcnt(1)
	v_mfma_f32_32x32x16_bf16 v[20:35], v[96:99], v[48:51], v[20:35]
	v_mfma_f32_32x32x16_bf16 v[4:19], v[100:103], v[48:51], v[4:19]
	s_waitcnt lgkmcnt(0)
	v_mfma_f32_32x32x16_bf16 v[20:35], v[104:107], v[52:55], v[20:35]
	v_mfma_f32_32x32x16_bf16 v[4:19], v[108:111], v[52:55], v[4:19]
	ds_read_b128 v[48:51], v61 offset:50112
	ds_read_b128 v[52:55], v61 offset:50144
	s_waitcnt lgkmcnt(1)
	v_mfma_f32_32x32x16_bf16 v[20:35], v[112:115], v[48:51], v[20:35]
	v_mov_b32_e32 v57, v3
	v_mfma_f32_32x32x16_bf16 v[4:19], v[116:119], v[48:51], v[4:19]
	v_or_b32_e32 v44, s10, v60
	v_lshlrev_b32_e32 v56, 12, v44
	v_lshl_add_u64 v[44:45], s[46:47], 0, v[56:57]
	v_lshl_add_u64 v[44:45], s[6:7], 1, v[44:45]
	s_waitcnt lgkmcnt(0)
	v_mfma_f32_32x32x16_bf16 v[20:35], v[120:123], v[52:55], v[20:35]
	v_lshl_add_u64 v[36:37], v[44:45], 0, s[26:27]
	v_lshl_add_u64 v[36:37], v[36:37], 0, v[2:3]
	v_lshl_add_u64 v[38:39], v[36:37], 0, s[18:19]
	v_add_co_u32_e32 v36, vcc, s69, v36
	s_nop 7
	v_cvt_pk_bf16_f32 v20, v20, v21
	v_mfma_f32_32x32x16_bf16 v[4:19], v[124:127], v[52:55], v[4:19]
	v_addc_co_u32_e32 v37, vcc, 0, v37, vcc
	v_cvt_pk_bf16_f32 v21, v22, v23
	v_cvt_pk_bf16_f32 v22, v24, v25
	v_cvt_pk_bf16_f32 v23, v26, v27
	v_cvt_pk_bf16_f32 v24, v28, v29
	v_cvt_pk_bf16_f32 v25, v30, v31
	v_cvt_pk_bf16_f32 v26, v32, v33
	v_cvt_pk_bf16_f32 v27, v34, v35
	s_nop 3
	v_cvt_pk_bf16_f32 v4, v4, v5
	v_cvt_pk_bf16_f32 v5, v6, v7
	v_cvt_pk_bf16_f32 v6, v8, v9
	v_cvt_pk_bf16_f32 v7, v10, v11
	v_cvt_pk_bf16_f32 v8, v12, v13
	v_cvt_pk_bf16_f32 v9, v14, v15
	v_cvt_pk_bf16_f32 v10, v16, v17
	v_cvt_pk_bf16_f32 v11, v18, v19
	global_store_dwordx2 v[36:37], v[20:21], off
	global_store_dwordx2 v[38:39], v[22:23], off offset:16
	global_store_dwordx2 v[38:39], v[24:25], off offset:32
	global_store_dwordx2 v[38:39], v[26:27], off offset:48
	global_store_dwordx2 v[38:39], v[4:5], off offset:64
	global_store_dwordx2 v[38:39], v[6:7], off offset:80
	global_store_dwordx2 v[38:39], v[8:9], off offset:96
	global_store_dwordx2 v[38:39], v[10:11], off offset:112

; #define LAS __attribute__((address_space(3)))
;     ...
;         if (o == 0) { const bf16* src = T + (size_t)(2 * 512 + c) * 4 * L;
;             { constexpr int N1 = (4 * L / 8) / NT; u32x4 t1[N1];
; #pragma unroll
;               for (int i = 0; i < N1; ++i) t1[i] = *(const u32x4*)(src + 8 * (C.tid + NT * i));
; #pragma unroll
;               for (int i = 0; i < N1; ++i) { const int idx = C.tid + NT * i, b = idx / (L / 8), tc = idx % (L / 8); *(LAS u32x4*)(C.lds + b * SB + tc * 16) = t1[i]; } }
;             if (C.tid < 4) *(LAS u32x4*)(C.lds + Z_OFF + 16 * C.tid) = (u32x4){0u, 0u, 0u, 0u}; }
;         { const bf16* fsrc = (L == SL) ? WSP(bf16, WS_FILT) + (size_t)((l * 2 + o) * 512 + c) * (2 * L) : WSP(bf16, WS_FILTC) + (size_t)(o * 512 + c) * (2 * L);
;           constexpr int N2 = (L / 4) / NT; u32x4 t2[N2];
; #pragma unroll
;           for (int i = 0; i < N2; ++i) t2[i] = *(const u32x4*)(fsrc + 8 * (C.tid + NT * i));
; #pragma unroll
;           for (int i = 0; i < N2; ++i) *(LAS u32x4*)(C.lds + R_OFF + 16 * (C.tid + NT * i)) = t2[i]; }
;         __syncthreads();
;         for (int idx = C.tid; idx < 3 * (L / 2); idx += NT) { const int p = 1 + idx / (L / 2), w = idx % (L / 2); unsigned short e[4];
; #pragma unroll
;             for (int k = 0; k < 4; ++k) { const int n = 4 * w + p + k; e[k] = n < 2 * L ? *(const LAS bf16*)(C.lds + R_OFF + 2 * n) : (bf16)0; }
;             *(LAS u32x2*)(C.lds + R_OFF + p * CSZ + 8 + 64 * p + 8 * w) = (u32x2){(unsigned)e[0] | ((unsigned)e[1] << 16), (unsigned)e[2] | ((unsigned)e[3] << 16)}; }
.LBB0_2068:
	s_xor_b64 s[48:49], s[10:11], -1
	s_and_b64 vcc, exec, s[48:49]
	s_waitcnt vmcnt(0) lgkmcnt(0)
	s_barrier
	s_cbranch_vccnz .LBB0_2072
	global_load_dwordx4 v[2:5], v[168:169], off
	global_load_dwordx4 v[6:9], v[170:171], off
	global_load_dwordx4 v[10:13], v[172:173], off
	global_load_dwordx4 v[14:17], v[174:175], off
	s_add_i32 s12, s35, s46
	s_ashr_i32 s13, s12, 31
	s_lshl_b64 s[12:13], s[12:13], 14
	s_add_u32 s12, s18, s12
	s_addc_u32 s13, s19, s13
	v_lshl_add_u64 v[244:245], v[164:165], 1, s[12:13]
	v_lshl_add_u64 v[248:249], v[166:167], 1, s[12:13]
	global_load_dwordx4 v[244:247], v[244:245], off
	s_nop 0
	global_load_dwordx4 v[248:251], v[248:249], off
	s_waitcnt vmcnt(5)
	ds_write_b128 v225, v[2:5]
	s_waitcnt vmcnt(4)
	ds_write_b128 v226, v[6:9]
	s_waitcnt vmcnt(3)
	ds_write_b128 v227, v[10:13]
	s_waitcnt vmcnt(2)
	ds_write_b128 v228, v[14:17]
	s_and_saveexec_b64 s[10:11], s[8:9]
	v_add_u32_e32 v2, 0, v213
	ds_write_b128 v2, v[238:241] offset:32832
	s_or_b64 exec, exec, s[10:11]
	s_branch .Lhyf_l1_have
.LBB0_2072:
	s_add_i32 s12, s35, s46
	s_ashr_i32 s13, s12, 31
	s_lshl_b64 s[12:13], s[12:13], 14
	s_add_u32 s12, s18, s12
	s_addc_u32 s13, s19, s13
	v_lshl_add_u64 v[244:245], v[164:165], 1, s[12:13]
	v_lshl_add_u64 v[248:249], v[166:167], 1, s[12:13]
	global_load_dwordx4 v[244:247], v[244:245], off
	s_nop 0
	global_load_dwordx4 v[248:251], v[248:249], off
.Lhyf_l1_have:
	s_add_i32 s10, s35, s46
	s_ashr_i32 s11, s10, 31
	v_add_u32_e32 v10, 0, v213
	s_waitcnt vmcnt(1)
	ds_write_b128 v10, v[244:247] offset:32896
	s_waitcnt vmcnt(0)
	ds_write_b128 v10, v[248:251] offset:41088
	s_waitcnt lgkmcnt(0)
	s_barrier
	s_and_saveexec_b64 s[12:13], s[6:7]
	s_cbranch_execz .LBB0_2081
	v_lshlrev_b32_e32 v2, 3, v212
	v_add_u32_e32 v3, 0x8000, v2
	ds_read_b64 v[4:5], v2 offset:32896
	ds_read_b64 v[6:7], v2 offset:32904
	ds_read_b64 v[8:9], v2 offset:36992
	ds_read_b64 v[10:11], v2 offset:37000
	ds_read_b64 v[12:13], v2 offset:41088
	ds_read_b64 v[14:15], v2 offset:41096
	ds_read_b64 v[16:17], v2 offset:45184
	ds_read_b64 v[18:19], v2 offset:45192
	v_cmp_ne_u32_e32 vcc, 0x1ff, v212
	s_waitcnt lgkmcnt(0)
	v_cndmask_b32_e32 v18, 0, v18, vcc
	v_cndmask_b32_e32 v19, 0, v19, vcc
	v_alignbit_b32 v20, v5, v4, 16
	v_alignbit_b32 v21, v6, v5, 16
	v_mov_b32_e32 v22, v5
	v_mov_b32_e32 v23, v6
	v_mov_b32_e32 v24, v21
	v_alignbit_b32 v25, v7, v6, 16
	ds_write_b64 v2, v[20:21] offset:49352
	ds_write_b64 v3, v[22:23] offset:33032
	ds_write_b64 v3, v[24:25] offset:49480
	s_nop 0
	v_alignbit_b32 v20, v9, v8, 16
	v_alignbit_b32 v21, v10, v9, 16
	v_mov_b32_e32 v22, v9
	v_mov_b32_e32 v23, v10
	v_mov_b32_e32 v24, v21
	v_alignbit_b32 v25, v11, v10, 16
	ds_write_b64 v2, v[20:21] offset:53448
	ds_write_b64 v3, v[22:23] offset:37128
	ds_write_b64 v3, v[24:25] offset:53576
	s_nop 0
	v_alignbit_b32 v20, v13, v12, 16
	v_alignbit_b32 v21, v14, v13, 16
	v_mov_b32_e32 v22, v13
	v_mov_b32_e32 v23, v14
	v_mov_b32_e32 v24, v21
	v_alignbit_b32 v25, v15, v14, 16
	ds_write_b64 v2, v[20:21] offset:57544
	ds_write_b64 v3, v[22:23] offset:41224
	ds_write_b64 v3, v[24:25] offset:57672
	s_nop 0
	v_alignbit_b32 v20, v17, v16, 16
	v_alignbit_b32 v21, v18, v17, 16
	v_mov_b32_e32 v22, v17
	v_mov_b32_e32 v23, v18
	v_mov_b32_e32 v24, v21
	v_alignbit_b32 v25, v19, v18, 16
	ds_write_b64 v2, v[20:21] offset:61640
	ds_write_b64 v3, v[22:23] offset:45320
	ds_write_b64 v3, v[24:25] offset:61768
	s_nop 0

; __device__ __forceinline__ float wave_sum(float v) { return xor32_sum(xor16_sum(row16_sum(v))); }
; __device__ __forceinline__ void cvt8(const u32x4 r, float (&f)[8]) { f[0] = bflo(r.x); f[1] = bfhi(r.x); f[2] = bflo(r.y); f[3] = bfhi(r.y); f[4] = bflo(r.z); f[5] = bfhi(r.z); f[6] = bflo(r.w); f[7] = bfhi(r.w); }
; __device__ __forceinline__ void row_ln(float (&v)[32]) {
;     float s = 0.f;
; #pragma unroll
;     for (int i = 0; i < 32; ++i) s += v[i];
;     const float mean = wave_sum(s) * (1.0f / DM); float q = 0.f;
; __device__ __forceinline__ void ph_post1(Ctx& C, int l, int nrows, bool dry = false) {
;     ...
;               for (int j = 0; j < 4; ++j) { float t8[8]; cvt8(*(const u32x4*)(yo + 512 * j + 8 * C.lane), t8);
; #pragma unroll
;                   for (int e = 0; e < 8; ++e) y[8 * j + e] = t8[e]; } }
; #pragma unroll
;             for (int i = 0; i < 32; ++i) v[i] = ALPHA * v[i] + g1[i] * y[i];
.Lp1b_nopf:
	s_waitcnt lgkmcnt(14)
	v_pk_add_f32 v[78:79], v[86:87], 0 op_sel_hi:[1,0]
	v_pk_add_f32 v[80:81], v[84:85], 0 op_sel_hi:[1,0]
	v_pk_add_f32 v[84:85], v[88:89], 0 op_sel_hi:[1,0]
	s_waitcnt lgkmcnt(12)
	v_pk_add_f32 v[86:87], v[146:147], 0 op_sel_hi:[1,0]
	v_pk_add_f32 v[88:89], v[144:145], 0 op_sel_hi:[1,0]
	s_lshl_b64 s[26:27], s[8:9], 11
	v_pk_add_f32 v[82:83], v[82:83], 0 op_sel_hi:[1,0]
	s_waitcnt lgkmcnt(8)
	v_pk_add_f32 v[2:3], v[2:3], 0 op_sel_hi:[1,0]
	v_pk_add_f32 v[46:47], v[46:47], 0 op_sel_hi:[1,0]
	v_pk_add_f32 v[44:45], v[44:45], 0 op_sel_hi:[1,0]
	v_pk_add_f32 v[42:43], v[42:43], 0 op_sel_hi:[1,0]
	v_pk_add_f32 v[48:49], v[48:49], 0 op_sel_hi:[1,0]
	v_pk_add_f32 v[40:41], v[40:41], 0 op_sel_hi:[1,0]
	v_pk_add_f32 v[38:39], v[38:39], 0 op_sel_hi:[1,0]
	v_mov_b32_e32 v74, 0
	v_lshlrev_b32_e32 v146, 16, v113
	v_lshlrev_b32_e32 v144, 16, v93
	v_and_b32_e32 v145, 0xffff0000, v93
	v_and_b32_e32 v147, 0xffff0000, v113
	v_lshlrev_b32_e32 v166, 16, v92
	v_and_b32_e32 v167, 0xffff0000, v92
	v_lshlrev_b32_e32 v92, 16, v112
	v_and_b32_e32 v93, 0xffff0000, v112
	v_lshlrev_b32_e32 v112, 16, v91
	v_and_b32_e32 v113, 0xffff0000, v91
	v_lshlrev_b32_e32 v168, 16, v111
	v_and_b32_e32 v169, 0xffff0000, v111
	v_lshlrev_b32_e32 v170, 16, v90
	v_and_b32_e32 v171, 0xffff0000, v90
	v_lshlrev_b32_e32 v90, 16, v110
	v_and_b32_e32 v91, 0xffff0000, v110
	v_pk_mul_f32 v[124:125], v[124:125], v[168:169]
	v_pk_mul_f32 v[90:91], v[122:123], v[90:91]
	v_pk_fma_f32 v[112:113], v[112:113], s[14:15], v[124:125] op_sel_hi:[1,0,1]
	v_pk_fma_f32 v[124:125], v[170:171], s[14:15], v[90:91] op_sel_hi:[1,0,1]
	v_lshlrev_b32_e32 v176, 16, v119
	v_and_b32_e32 v177, 0xffff0000, v119
	v_pk_mul_f32 v[92:93], v[126:127], v[92:93]
	v_pk_mul_f32 v[126:127], v[132:133], v[176:177]
	v_pk_fma_f32 v[132:133], v[166:167], s[14:15], v[92:93] op_sel_hi:[1,0,1]
	v_pk_add_f32 v[248:249], v[124:125], v[112:113]
	v_pk_mul_f32 v[128:129], v[128:129], v[146:147]
	v_pk_fma_f32 v[128:129], v[144:145], s[14:15], v[128:129] op_sel_hi:[1,0,1]
	v_pk_add_f32 v[248:249], v[248:249], v[132:133]
	v_lshlrev_b32_e32 v92, 16, v118
	v_and_b32_e32 v93, 0xffff0000, v118
	v_lshlrev_b32_e32 v90, 16, v114
	v_and_b32_e32 v91, 0xffff0000, v114
	v_pk_mul_f32 v[92:93], v[130:131], v[92:93]
	v_lshlrev_b32_e32 v110, 16, v117
	v_and_b32_e32 v111, 0xffff0000, v117
	v_lshlrev_b32_e32 v172, 16, v121
	v_and_b32_e32 v173, 0xffff0000, v121
	v_lshlrev_b32_e32 v174, 16, v116
	v_and_b32_e32 v175, 0xffff0000, v116
	v_lshlrev_b32_e32 v116, 16, v120
	v_and_b32_e32 v117, 0xffff0000, v120
	v_lshlrev_b32_e32 v120, 16, v115
	v_and_b32_e32 v121, 0xffff0000, v115
	v_pk_add_f32 v[248:249], v[248:249], v[128:129]
	v_pk_fma_f32 v[114:115], v[90:91], s[14:15], v[92:93] op_sel_hi:[1,0,1]
	v_pk_mul_f32 v[122:123], v[136:137], v[172:173]
	v_pk_fma_f32 v[120:121], v[120:121], s[14:15], v[126:127] op_sel_hi:[1,0,1]
	v_pk_add_f32 v[248:249], v[248:249], v[114:115]
	v_pk_mul_f32 v[116:117], v[134:135], v[116:117]
	v_pk_fma_f32 v[110:111], v[110:111], s[14:15], v[122:123] op_sel_hi:[1,0,1]
	v_lshlrev_b32_e32 v122, 16, v157
	v_and_b32_e32 v123, 0xffff0000, v157
	v_pk_fma_f32 v[116:117], v[174:175], s[14:15], v[116:117] op_sel_hi:[1,0,1]
	v_pk_add_f32 v[248:249], v[248:249], v[120:121]
	v_lshlrev_b32_e32 v118, 16, v153
	v_and_b32_e32 v119, 0xffff0000, v153
	v_pk_mul_f32 v[122:123], v[140:141], v[122:123]
	v_lshlrev_b32_e32 v126, 16, v156
	v_and_b32_e32 v127, 0xffff0000, v156
	v_pk_fma_f32 v[118:119], v[118:119], s[14:15], v[122:123] op_sel_hi:[1,0,1]
	v_lshlrev_b32_e32 v122, 16, v152
	v_and_b32_e32 v123, 0xffff0000, v152
	v_pk_mul_f32 v[126:127], v[138:139], v[126:127]
	v_lshlrev_b32_e32 v130, 16, v155
	v_and_b32_e32 v131, 0xffff0000, v155
	v_pk_add_f32 v[248:249], v[248:249], v[116:117]
	v_pk_fma_f32 v[122:123], v[122:123], s[14:15], v[126:127] op_sel_hi:[1,0,1]
	v_lshlrev_b32_e32 v126, 16, v151
	v_and_b32_e32 v127, 0xffff0000, v151
	v_pk_mul_f32 v[60:61], v[60:61], v[130:131]
	v_lshlrev_b32_e32 v130, 16, v154
	v_and_b32_e32 v131, 0xffff0000, v154
	v_pk_fma_f32 v[60:61], v[126:127], s[14:15], v[60:61] op_sel_hi:[1,0,1]
	v_lshlrev_b32_e32 v126, 16, v150
	v_and_b32_e32 v127, 0xffff0000, v150
	v_pk_mul_f32 v[58:59], v[58:59], v[130:131]
	v_pk_add_f32 v[248:249], v[248:249], v[110:111]
	v_pk_fma_f32 v[58:59], v[126:127], s[14:15], v[58:59] op_sel_hi:[1,0,1]
	v_lshlrev_b32_e32 v130, 16, v165
	v_pk_add_f32 v[248:249], v[248:249], v[58:59]
	v_and_b32_e32 v131, 0xffff0000, v165
	v_pk_add_f32 v[248:249], v[248:249], v[60:61]
	v_lshlrev_b32_e32 v126, 16, v161
	v_and_b32_e32 v127, 0xffff0000, v161
	v_pk_mul_f32 v[56:57], v[56:57], v[130:131]
	v_lshlrev_b32_e32 v130, 16, v164
	v_and_b32_e32 v131, 0xffff0000, v164
	v_pk_fma_f32 v[56:57], v[126:127], s[14:15], v[56:57] op_sel_hi:[1,0,1]
	v_lshlrev_b32_e32 v126, 16, v160
	v_and_b32_e32 v127, 0xffff0000, v160
	v_pk_mul_f32 v[54:55], v[54:55], v[130:131]
	v_lshlrev_b32_e32 v130, 16, v163
	v_and_b32_e32 v131, 0xffff0000, v163
	v_pk_add_f32 v[248:249], v[248:249], v[122:123]
	v_pk_fma_f32 v[54:55], v[126:127], s[14:15], v[54:55] op_sel_hi:[1,0,1]
	v_lshlrev_b32_e32 v126, 16, v159
	v_and_b32_e32 v127, 0xffff0000, v159
	v_pk_mul_f32 v[52:53], v[52:53], v[130:131]
	v_lshlrev_b32_e32 v130, 16, v162
	v_and_b32_e32 v131, 0xffff0000, v162
	v_pk_fma_f32 v[52:53], v[126:127], s[14:15], v[52:53] op_sel_hi:[1,0,1]
	v_lshlrev_b32_e32 v126, 16, v158
	v_and_b32_e32 v127, 0xffff0000, v158
	v_pk_mul_f32 v[50:51], v[50:51], v[130:131]
	v_pk_add_f32 v[248:249], v[248:249], v[118:119]
	v_pk_fma_f32 v[50:51], v[126:127], s[14:15], v[50:51] op_sel_hi:[1,0,1]
	v_pk_add_f32 v[90:91], v[142:143], 0 op_sel_hi:[1,0]
; __device__ __forceinline__ float wave_sum(float v) { return xor32_sum(xor16_sum(row16_sum(v))); }
; __device__ __forceinline__ void row_ln(float (&v)[32]) {
;     float s = 0.f;
; #pragma unroll
;     for (int i = 0; i < 32; ++i) s += v[i];
;     const float mean = wave_sum(s) * (1.0f / DM); float q = 0.f;
; #pragma unroll
;     for (int i = 0; i < 32; ++i) { v[i] -= mean; q += v[i] * v[i]; }
;     const float rstd = 1.0f / sqrtf(wave_sum(q) * (1.0f / DM) + LN_EPS);
; #pragma unroll
;     for (int i = 0; i < 32; ++i) v[i] *= rstd;
; }
	v_pk_add_f32 v[248:249], v[248:249], v[50:51]
	v_pk_add_f32 v[248:249], v[248:249], v[52:53]
	v_pk_add_f32 v[248:249], v[248:249], v[54:55]
	v_pk_add_f32 v[248:249], v[248:249], v[56:57]
	v_add_f32_e32 v75, v248, v249
	v_pk_add_f32 v[92:93], v[148:149], 0 op_sel_hi:[1,0]
	s_nop 0
	v_add_f32_dpp v75, v75, v75 quad_perm:[1,0,3,2] row_mask:0xf bank_mask:0xf bound_ctrl:1
	s_nop 1
	v_add_f32_dpp v75, v75, v75 quad_perm:[2,3,0,1] row_mask:0xf bank_mask:0xf bound_ctrl:1
	s_nop 1
	v_add_f32_dpp v75, v75, v75 row_half_mirror row_mask:0xf bank_mask:0xf bound_ctrl:1
	s_nop 1
	v_add_f32_dpp v75, v75, v75 row_mirror row_mask:0xf bank_mask:0xf bound_ctrl:1
	v_mov_b32_e32 v126, v75
	s_nop 1
	v_permlane16_swap_b32_e32 v75, v126
	v_add_f32_e32 v75, v75, v126
	v_mov_b32_e32 v126, v75
	s_nop 1
	v_permlane32_swap_b32_e32 v75, v126
	v_add_f32_e32 v75, v75, v126
	v_mul_f32_e32 v126, 0x3a000000, v75
	v_pk_add_f32 v[124:125], v[124:125], v[126:127] op_sel_hi:[1,0] neg_lo:[0,1] neg_hi:[0,1]
	v_pk_add_f32 v[112:113], v[112:113], v[126:127] op_sel_hi:[1,0] neg_lo:[0,1] neg_hi:[0,1]
	v_pk_mul_f32 v[248:249], v[124:125], v[124:125]
	v_pk_fma_f32 v[248:249], v[112:113], v[112:113], v[248:249]
	v_pk_add_f32 v[132:133], v[132:133], v[126:127] op_sel_hi:[1,0] neg_lo:[0,1] neg_hi:[0,1]
	v_pk_fma_f32 v[248:249], v[132:133], v[132:133], v[248:249]
	v_pk_add_f32 v[128:129], v[128:129], v[126:127] op_sel_hi:[1,0] neg_lo:[0,1] neg_hi:[0,1]
	v_pk_fma_f32 v[248:249], v[128:129], v[128:129], v[248:249]
	v_pk_add_f32 v[114:115], v[114:115], v[126:127] op_sel_hi:[1,0] neg_lo:[0,1] neg_hi:[0,1]
	v_pk_fma_f32 v[248:249], v[114:115], v[114:115], v[248:249]
	v_pk_add_f32 v[120:121], v[120:121], v[126:127] op_sel_hi:[1,0] neg_lo:[0,1] neg_hi:[0,1]
	v_pk_fma_f32 v[248:249], v[120:121], v[120:121], v[248:249]
	v_pk_add_f32 v[116:117], v[116:117], v[126:127] op_sel_hi:[1,0] neg_lo:[0,1] neg_hi:[0,1]
	v_pk_fma_f32 v[248:249], v[116:117], v[116:117], v[248:249]
	v_pk_add_f32 v[110:111], v[110:111], v[126:127] op_sel_hi:[1,0] neg_lo:[0,1] neg_hi:[0,1]
	v_pk_fma_f32 v[248:249], v[110:111], v[110:111], v[248:249]
	v_pk_add_f32 v[58:59], v[58:59], v[126:127] op_sel_hi:[1,0] neg_lo:[0,1] neg_hi:[0,1]
	v_pk_fma_f32 v[248:249], v[58:59], v[58:59], v[248:249]
	v_pk_add_f32 v[60:61], v[60:61], v[126:127] op_sel_hi:[1,0] neg_lo:[0,1] neg_hi:[0,1]
	v_pk_fma_f32 v[248:249], v[60:61], v[60:61], v[248:249]
	v_pk_add_f32 v[122:123], v[122:123], v[126:127] op_sel_hi:[1,0] neg_lo:[0,1] neg_hi:[0,1]
	v_pk_fma_f32 v[248:249], v[122:123], v[122:123], v[248:249]
	v_pk_add_f32 v[118:119], v[118:119], v[126:127] op_sel_hi:[1,0] neg_lo:[0,1] neg_hi:[0,1]
	v_pk_fma_f32 v[248:249], v[118:119], v[118:119], v[248:249]
	v_pk_add_f32 v[50:51], v[50:51], v[126:127] op_sel_hi:[1,0] neg_lo:[0,1] neg_hi:[0,1]
	v_pk_fma_f32 v[248:249], v[50:51], v[50:51], v[248:249]
	v_pk_add_f32 v[52:53], v[52:53], v[126:127] op_sel_hi:[1,0] neg_lo:[0,1] neg_hi:[0,1]
	v_pk_fma_f32 v[248:249], v[52:53], v[52:53], v[248:249]
	v_pk_add_f32 v[54:55], v[54:55], v[126:127] op_sel_hi:[1,0] neg_lo:[0,1] neg_hi:[0,1]
	v_pk_fma_f32 v[248:249], v[54:55], v[54:55], v[248:249]
	v_pk_add_f32 v[56:57], v[56:57], v[126:127] op_sel_hi:[1,0] neg_lo:[0,1] neg_hi:[0,1]
	v_pk_fma_f32 v[248:249], v[56:57], v[56:57], v[248:249]
	v_add_f32_e32 v75, v248, v249
	s_nop 1
	v_add_f32_dpp v75, v75, v75 quad_perm:[1,0,3,2] row_mask:0xf bank_mask:0xf bound_ctrl:1
	s_nop 1
	v_add_f32_dpp v75, v75, v75 quad_perm:[2,3,0,1] row_mask:0xf bank_mask:0xf bound_ctrl:1
	s_nop 1
	v_add_f32_dpp v75, v75, v75 row_half_mirror row_mask:0xf bank_mask:0xf bound_ctrl:1
	s_nop 1
	v_add_f32_dpp v75, v75, v75 row_mirror row_mask:0xf bank_mask:0xf bound_ctrl:1
	v_mov_b32_e32 v126, v75
	s_nop 1
	v_permlane16_swap_b32_e32 v75, v126
	v_add_f32_e32 v75, v75, v126
	v_mov_b32_e32 v126, v75
	s_nop 1
	v_permlane32_swap_b32_e32 v75, v126
	v_add_f32_e32 v75, v75, v126
	v_fmamk_f32 v75, v75, 0x3a000000, v105
	v_mul_f32_e32 v126, 0x4f800000, v75
	v_cmp_gt_f32_e32 vcc, s23, v75
	s_nop 1
	v_cndmask_b32_e32 v75, v75, v126, vcc
	v_sqrt_f32_e32 v126, v75
	s_nop 0
	v_add_u32_e32 v127, -1, v126
	v_fma_f32 v130, -v127, v126, v75
	v_cmp_ge_f32_e64 s[8:9], 0, v130
	v_add_u32_e32 v130, 1, v126
	s_nop 0
	v_cndmask_b32_e64 v127, v126, v127, s[8:9]
	v_fma_f32 v126, -v130, v126, v75
	v_cmp_lt_f32_e64 s[8:9], 0, v126
	s_nop 1
	v_cndmask_b32_e64 v126, v127, v130, s[8:9]
	v_mul_f32_e32 v127, 0x37800000, v126
	v_cndmask_b32_e32 v126, v126, v127, vcc
	v_cmp_class_f32_e32 vcc, v75, v106
	s_nop 1
	v_cndmask_b32_e32 v75, v126, v75, vcc
	v_div_scale_f32 v126, s[8:9], v75, v75, 1.0
	v_rcp_f32_e32 v127, v126
	s_nop 0
	v_fma_f32 v130, -v126, v127, 1.0
	v_fmac_f32_e32 v127, v130, v127
	v_div_scale_f32 v130, vcc, 1.0, v75, 1.0
	v_mul_f32_e32 v131, v130, v127
	v_fma_f32 v134, -v126, v131, v130
	v_fmac_f32_e32 v131, v134, v127
	v_fma_f32 v126, -v126, v131, v130
	v_div_fmas_f32 v126, v126, v127, v131
	v_div_fixup_f32 v126, v126, v75, 1.0
	v_pk_mul_f32 v[124:125], v[124:125], v[126:127] op_sel_hi:[1,0]
	v_pk_mul_f32 v[112:113], v[112:113], v[126:127] op_sel_hi:[1,0]
	v_pk_mul_f32 v[130:131], v[132:133], v[126:127] op_sel_hi:[1,0]
	v_pk_mul_f32 v[128:129], v[128:129], v[126:127] op_sel_hi:[1,0]
	v_pk_mul_f32 v[54:55], v[54:55], v[126:127] op_sel_hi:[1,0]
	v_pk_mul_f32 v[114:115], v[114:115], v[126:127] op_sel_hi:[1,0]
	v_pk_mul_f32 v[120:121], v[120:121], v[126:127] op_sel_hi:[1,0]
	v_pk_mul_f32 v[116:117], v[116:117], v[126:127] op_sel_hi:[1,0]
	v_pk_mul_f32 v[110:111], v[110:111], v[126:127] op_sel_hi:[1,0]
	v_pk_mul_f32 v[56:57], v[56:57], v[126:127] op_sel_hi:[1,0]
	s_waitcnt lgkmcnt(7)
; __device__ __forceinline__ unsigned pk2(float lo, float hi) { f32x2 v = {lo, hi}; bf16x2_t b = __builtin_convertvector(v, bf16x2_t); return __builtin_bit_cast(unsigned, b); }
; __device__ __forceinline__ unsigned pk4_fp8(float a, float b, float c, float d) { int p = 0; p = __builtin_amdgcn_cvt_pk_fp8_f32(a, b, p, false); p = __builtin_amdgcn_cvt_pk_fp8_f32(c, d, p, true); return (unsigned)p; }
; __device__ __forceinline__ float wave_sum(float v) { return xor32_sum(xor16_sum(row16_sum(v))); }
; __device__ __forceinline__ void row_store(float* p, int lane, const float (&v)[32]) {
; #pragma unroll
;     for (int j = 0; j < 4; ++j) { *(f32x4*)(p + 512 * j + 8 * lane) = (f32x4){v[8 * j], v[8 * j + 1], v[8 * j + 2], v[8 * j + 3]}; *(f32x4*)(p + 512 * j + 8 * lane + 4) = (f32x4){v[8 * j + 4], v[8 * j + 5], v[8 * j + 6], v[8 * j + 7]}; }
; }
; __device__ __forceinline__ void row_store_bf16(bf16* p, int lane, const float (&v)[32]) {
; #pragma unroll
;     for (int j = 0; j < 4; ++j) { u32x4 w; w.x = pk2(v[8 * j], v[8 * j + 1]); w.y = pk2(v[8 * j + 2], v[8 * j + 3]); w.z = pk2(v[8 * j + 4], v[8 * j + 5]); w.w = pk2(v[8 * j + 6], v[8 * j + 7]); *(u32x4*)(p + 512 * j + 8 * lane) = w; }
; }
; __device__ __forceinline__ void row_store_fp8(unsigned char* p, int lane, const float (&v)[32]) {
; #pragma unroll
;     for (int j = 0; j < 4; ++j) { u32x2 w; w.x = pk4_fp8(v[8 * j], v[8 * j + 1], v[8 * j + 2], v[8 * j + 3]); w.y = pk4_fp8(v[8 * j + 4], v[8 * j + 5], v[8 * j + 6], v[8 * j + 7]); *(u32x2*)(p + 512 * j + 8 * lane) = w; }
; }
; __device__ __forceinline__ void row_ln(float (&v)[32]) {
;     float s = 0.f;
; #pragma unroll
;     for (int i = 0; i < 32; ++i) s += v[i];
;     const float mean = wave_sum(s) * (1.0f / DM); float q = 0.f;
; #pragma unroll
;     for (int i = 0; i < 32; ++i) { v[i] -= mean; q += v[i] * v[i]; }
;     const float rstd = 1.0f / sqrtf(wave_sum(q) * (1.0f / DM) + LN_EPS);
; #pragma unroll
;     for (int i = 0; i < 32; ++i) v[i] *= rstd;
; }
; __device__ __forceinline__ void ph_post1(Ctx& C, int l, int nrows, bool dry = false) {
;     ...
;             row_ln(v); row_affine_lds(v, PAR + 2048, PAR + 4096, C.lane, 0.f);
;             row_store_bf16(WSP(bf16, WS_X) + (size_t)row * DM, C.lane, v);
;             row_ln(v); row_affine_lds(v, PAR + 6144, PAR + 8192, C.lane, 1.0f);
	v_pk_fma_f32 v[82:83], v[82:83], v[124:125], v[34:35]
	v_pk_fma_f32 v[80:81], v[80:81], v[112:113], v[36:37]
	s_waitcnt lgkmcnt(6)
	v_pk_fma_f32 v[112:113], v[78:79], v[130:131], v[30:31]
	v_pk_fma_f32 v[84:85], v[84:85], v[128:129], v[32:33]
	s_waitcnt lgkmcnt(0)
	v_pk_fma_f32 v[124:125], v[54:55], v[2:3], v[6:7]
	v_pk_add_f32 v[2:3], v[4:5], 0 op_sel_hi:[1,0]
	v_pk_mul_f32 v[58:59], v[58:59], v[126:127] op_sel_hi:[1,0]
	v_pk_mul_f32 v[60:61], v[60:61], v[126:127] op_sel_hi:[1,0]
	v_pk_mul_f32 v[122:123], v[122:123], v[126:127] op_sel_hi:[1,0]
	v_pk_mul_f32 v[118:119], v[118:119], v[126:127] op_sel_hi:[1,0]
	v_pk_mul_f32 v[50:51], v[50:51], v[126:127] op_sel_hi:[1,0]
	v_pk_mul_f32 v[52:53], v[52:53], v[126:127] op_sel_hi:[1,0]
	v_pk_fma_f32 v[90:91], v[90:91], v[114:115], v[26:27]
	v_pk_fma_f32 v[88:89], v[88:89], v[120:121], v[28:29]
	v_pk_fma_f32 v[86:87], v[86:87], v[116:117], v[18:19]
	v_pk_fma_f32 v[92:93], v[92:93], v[110:111], v[20:21]
	v_pk_fma_f32 v[126:127], v[56:57], v[2:3], v[8:9]
	v_cvt_pk_bf16_f32 v2, v82, v83
	v_cvt_pk_bf16_f32 v3, v80, v81
	v_cvt_pk_bf16_f32 v4, v112, v113
	v_cvt_pk_bf16_f32 v5, v84, v85
	v_pk_fma_f32 v[110:111], v[42:43], v[58:59], v[22:23]
	v_pk_fma_f32 v[114:115], v[44:45], v[60:61], v[24:25]
	v_pk_fma_f32 v[116:117], v[46:47], v[122:123], v[14:15]
	v_pk_fma_f32 v[118:119], v[48:49], v[118:119], v[16:17]
	global_store_dwordx4 v[76:77], v[2:5], off
	v_pk_fma_f32 v[120:121], v[50:51], v[38:39], v[10:11]
	v_pk_fma_f32 v[122:123], v[52:53], v[40:41], v[12:13]
	v_cvt_pk_bf16_f32 v2, v90, v91
	v_cvt_pk_bf16_f32 v3, v88, v89
	v_cvt_pk_bf16_f32 v4, v86, v87
	v_cvt_pk_bf16_f32 v5, v92, v93
	global_store_dwordx4 v[76:77], v[2:5], off offset:1024
	s_nop 1
	v_cvt_pk_bf16_f32 v2, v110, v111
	v_cvt_pk_bf16_f32 v3, v114, v115
	v_cvt_pk_bf16_f32 v4, v116, v117
	v_cvt_pk_bf16_f32 v5, v118, v119
	global_store_dwordx4 v[76:77], v[2:5], off offset:2048
	s_nop 1
	v_cvt_pk_bf16_f32 v2, v120, v121
	v_cvt_pk_bf16_f32 v3, v122, v123
	v_cvt_pk_bf16_f32 v4, v124, v125
	v_cvt_pk_bf16_f32 v5, v126, v127
	global_store_dwordx4 v[76:77], v[2:5], off offset:3072
	s_nop 1
	v_pk_add_f32 v[248:249], v[82:83], v[80:81]
	v_pk_add_f32 v[248:249], v[248:249], v[112:113]
	v_pk_add_f32 v[248:249], v[248:249], v[84:85]
	v_pk_add_f32 v[248:249], v[248:249], v[90:91]
	v_pk_add_f32 v[248:249], v[248:249], v[88:89]
	v_pk_add_f32 v[248:249], v[248:249], v[86:87]
	v_pk_add_f32 v[248:249], v[248:249], v[92:93]
	v_pk_add_f32 v[248:249], v[248:249], v[110:111]
	v_pk_add_f32 v[248:249], v[248:249], v[114:115]
	v_pk_add_f32 v[248:249], v[248:249], v[116:117]
	v_pk_add_f32 v[248:249], v[248:249], v[118:119]
	v_pk_add_f32 v[248:249], v[248:249], v[120:121]
	v_pk_add_f32 v[248:249], v[248:249], v[122:123]
	v_pk_add_f32 v[248:249], v[248:249], v[124:125]
	v_pk_add_f32 v[248:249], v[248:249], v[126:127]
	v_add_f32_e32 v2, v248, v249
	s_nop 1
	v_add_f32_dpp v2, v2, v2 quad_perm:[1,0,3,2] row_mask:0xf bank_mask:0xf bound_ctrl:1
	s_nop 1
	v_add_f32_dpp v2, v2, v2 quad_perm:[2,3,0,1] row_mask:0xf bank_mask:0xf bound_ctrl:1
	s_nop 1
	v_add_f32_dpp v2, v2, v2 row_half_mirror row_mask:0xf bank_mask:0xf bound_ctrl:1
	s_nop 1
	v_add_f32_dpp v2, v2, v2 row_mirror row_mask:0xf bank_mask:0xf bound_ctrl:1
	v_mov_b32_e32 v3, v2
	s_nop 1
	v_permlane16_swap_b32_e32 v2, v3
	v_add_f32_e32 v2, v2, v3
	v_mov_b32_e32 v3, v2
	s_nop 1
	v_permlane32_swap_b32_e32 v2, v3
	v_add_f32_e32 v2, v2, v3
	v_mul_f32_e32 v128, 0x3a000000, v2
	v_pk_add_f32 v[82:83], v[82:83], v[128:129] op_sel_hi:[1,0] neg_lo:[0,1] neg_hi:[0,1]
	v_pk_add_f32 v[80:81], v[80:81], v[128:129] op_sel_hi:[1,0] neg_lo:[0,1] neg_hi:[0,1]
	v_pk_mul_f32 v[248:249], v[82:83], v[82:83]
	v_pk_fma_f32 v[248:249], v[80:81], v[80:81], v[248:249]
	v_pk_add_f32 v[112:113], v[112:113], v[128:129] op_sel_hi:[1,0] neg_lo:[0,1] neg_hi:[0,1]
	v_pk_fma_f32 v[248:249], v[112:113], v[112:113], v[248:249]
	v_pk_add_f32 v[84:85], v[84:85], v[128:129] op_sel_hi:[1,0] neg_lo:[0,1] neg_hi:[0,1]
	v_pk_fma_f32 v[248:249], v[84:85], v[84:85], v[248:249]
	v_pk_add_f32 v[90:91], v[90:91], v[128:129] op_sel_hi:[1,0] neg_lo:[0,1] neg_hi:[0,1]
	v_pk_fma_f32 v[248:249], v[90:91], v[90:91], v[248:249]
	v_pk_add_f32 v[88:89], v[88:89], v[128:129] op_sel_hi:[1,0] neg_lo:[0,1] neg_hi:[0,1]
	v_pk_fma_f32 v[248:249], v[88:89], v[88:89], v[248:249]
	v_pk_add_f32 v[86:87], v[86:87], v[128:129] op_sel_hi:[1,0] neg_lo:[0,1] neg_hi:[0,1]
	v_pk_fma_f32 v[248:249], v[86:87], v[86:87], v[248:249]
	v_pk_add_f32 v[92:93], v[92:93], v[128:129] op_sel_hi:[1,0] neg_lo:[0,1] neg_hi:[0,1]
	v_pk_fma_f32 v[248:249], v[92:93], v[92:93], v[248:249]
	v_pk_add_f32 v[110:111], v[110:111], v[128:129] op_sel_hi:[1,0] neg_lo:[0,1] neg_hi:[0,1]
	v_pk_fma_f32 v[248:249], v[110:111], v[110:111], v[248:249]
	v_pk_add_f32 v[114:115], v[114:115], v[128:129] op_sel_hi:[1,0] neg_lo:[0,1] neg_hi:[0,1]
	v_pk_fma_f32 v[248:249], v[114:115], v[114:115], v[248:249]
	v_pk_add_f32 v[116:117], v[116:117], v[128:129] op_sel_hi:[1,0] neg_lo:[0,1] neg_hi:[0,1]
	v_pk_fma_f32 v[248:249], v[116:117], v[116:117], v[248:249]
	v_pk_add_f32 v[118:119], v[118:119], v[128:129] op_sel_hi:[1,0] neg_lo:[0,1] neg_hi:[0,1]
	v_pk_fma_f32 v[248:249], v[118:119], v[118:119], v[248:249]
	v_pk_add_f32 v[120:121], v[120:121], v[128:129] op_sel_hi:[1,0] neg_lo:[0,1] neg_hi:[0,1]
	v_pk_fma_f32 v[248:249], v[120:121], v[120:121], v[248:249]
	v_pk_add_f32 v[122:123], v[122:123], v[128:129] op_sel_hi:[1,0] neg_lo:[0,1] neg_hi:[0,1]
	v_pk_fma_f32 v[248:249], v[122:123], v[122:123], v[248:249]
	v_pk_add_f32 v[124:125], v[124:125], v[128:129] op_sel_hi:[1,0] neg_lo:[0,1] neg_hi:[0,1]
	v_pk_fma_f32 v[248:249], v[124:125], v[124:125], v[248:249]
	v_pk_add_f32 v[126:127], v[126:127], v[128:129] op_sel_hi:[1,0] neg_lo:[0,1] neg_hi:[0,1]
	v_pk_fma_f32 v[248:249], v[126:127], v[126:127], v[248:249]
	v_add_f32_e32 v75, v248, v249
	ds_read_b128 v[2:5], v107
	ds_read_b128 v[6:9], v107 offset:16
	ds_read_b128 v[10:13], v107 offset:2048
	ds_read_b128 v[14:17], v107 offset:2064
	ds_read_b128 v[18:21], v107 offset:4096
	ds_read_b128 v[22:25], v107 offset:4112
	ds_read_b128 v[26:29], v107 offset:6144
	ds_read_b128 v[30:33], v107 offset:6160
	ds_read_b128 v[34:37], v108
	ds_read_b128 v[38:41], v108 offset:16
	ds_read_b128 v[42:45], v108 offset:2048
	ds_read_b128 v[46:49], v108 offset:2064
	ds_read_b128 v[50:53], v108 offset:4096
	ds_read_b128 v[54:57], v108 offset:4112
	ds_read_b128 v[58:61], v108 offset:6144
	ds_read_b128 v[76:79], v108 offset:6160
	v_add_f32_dpp v75, v75, v75 quad_perm:[1,0,3,2] row_mask:0xf bank_mask:0xf bound_ctrl:1
	s_waitcnt lgkmcnt(14)
; #define LAS __attribute__((address_space(3)))
; __device__ __forceinline__ void ph_post1(Ctx& C, int l, int nrows, bool dry = false) {
;     ...
;             row_ln(v); row_affine_lds(v, PAR + 6144, PAR + 8192, C.lane, 1.0f);
;             row_store_fp8(WSP(unsigned char, WS_HB8) + (size_t)row * DM, C.lane, v);
; #pragma unroll
;             for (int j = 0; j < 4; ++j) { *(LAS f32x4*)(H2 + C.wave * DM + 512 * j + 8 * C.lane) = (f32x4){v[8 * j], v[8 * j + 1], v[8 * j + 2], v[8 * j + 3]};
;                 *(LAS f32x4*)(H2 + C.wave * DM + 512 * j + 8 * C.lane + 4) = (f32x4){v[8 * j + 4], v[8 * j + 5], v[8 * j + 6], v[8 * j + 7]}; }
;         }
;         __syncthreads();
	v_pk_add_f32 v[2:3], v[2:3], 1.0 op_sel_hi:[1,0]
	v_pk_add_f32 v[4:5], v[4:5], 1.0 op_sel_hi:[1,0]
	v_add_f32_dpp v75, v75, v75 quad_perm:[2,3,0,1] row_mask:0xf bank_mask:0xf bound_ctrl:1
	v_pk_add_f32 v[6:7], v[6:7], 1.0 op_sel_hi:[1,0]
	s_waitcnt lgkmcnt(13)
	v_pk_add_f32 v[10:11], v[10:11], 1.0 op_sel_hi:[1,0]
	v_add_f32_dpp v75, v75, v75 row_half_mirror row_mask:0xf bank_mask:0xf bound_ctrl:1
	s_waitcnt lgkmcnt(12)
	v_pk_add_f32 v[14:15], v[14:15], 1.0 op_sel_hi:[1,0]
	v_pk_add_f32 v[8:9], v[8:9], 1.0 op_sel_hi:[1,0]
	v_add_f32_dpp v75, v75, v75 row_mirror row_mask:0xf bank_mask:0xf bound_ctrl:1
	v_mov_b32_e32 v128, v75
	s_nop 1
	v_permlane16_swap_b32_e32 v75, v128
	v_add_f32_e32 v75, v75, v128
	v_mov_b32_e32 v128, v75
	s_nop 1
	v_permlane32_swap_b32_e32 v75, v128
	v_add_f32_e32 v75, v75, v128
	v_fmamk_f32 v75, v75, 0x3a000000, v105
	v_mul_f32_e32 v128, 0x4f800000, v75
	v_cmp_gt_f32_e32 vcc, s23, v75
	s_waitcnt lgkmcnt(11)
	v_pk_add_f32 v[18:19], v[18:19], 1.0 op_sel_hi:[1,0]
	s_waitcnt lgkmcnt(10)
	v_pk_add_f32 v[22:23], v[22:23], 1.0 op_sel_hi:[1,0]
	v_cndmask_b32_e32 v75, v75, v128, vcc
	v_sqrt_f32_e32 v128, v75
	s_waitcnt lgkmcnt(9)
	v_pk_add_f32 v[26:27], v[26:27], 1.0 op_sel_hi:[1,0]
	s_waitcnt lgkmcnt(8)
	v_pk_add_f32 v[30:31], v[30:31], 1.0 op_sel_hi:[1,0]
	v_pk_add_f32 v[12:13], v[12:13], 1.0 op_sel_hi:[1,0]
	v_add_u32_e32 v129, -1, v128
	v_fma_f32 v130, -v129, v128, v75
	v_cmp_ge_f32_e64 s[8:9], 0, v130
	v_add_u32_e32 v130, 1, v128
	v_pk_add_f32 v[16:17], v[16:17], 1.0 op_sel_hi:[1,0]
	v_cndmask_b32_e64 v129, v128, v129, s[8:9]
	v_fma_f32 v128, -v130, v128, v75
	v_cmp_lt_f32_e64 s[8:9], 0, v128
	v_pk_add_f32 v[20:21], v[20:21], 1.0 op_sel_hi:[1,0]
	v_pk_add_f32 v[24:25], v[24:25], 1.0 op_sel_hi:[1,0]
	v_cndmask_b32_e64 v128, v129, v130, s[8:9]
	v_mul_f32_e32 v129, 0x37800000, v128
	v_cndmask_b32_e32 v128, v128, v129, vcc
	v_cmp_class_f32_e32 vcc, v75, v106
	v_pk_add_f32 v[28:29], v[28:29], 1.0 op_sel_hi:[1,0]
	v_pk_add_f32 v[32:33], v[32:33], 1.0 op_sel_hi:[1,0]
	v_cndmask_b32_e32 v75, v128, v75, vcc
	v_div_scale_f32 v128, s[8:9], v75, v75, 1.0
	v_rcp_f32_e32 v129, v128
	s_mov_b32 s8, -4
	v_fma_f32 v130, -v128, v129, 1.0
	v_fmac_f32_e32 v129, v130, v129
	v_div_scale_f32 v130, vcc, 1.0, v75, 1.0
	v_mul_f32_e32 v131, v130, v129
	v_fma_f32 v132, -v128, v131, v130
	v_fmac_f32_e32 v131, v132, v129
	v_fma_f32 v128, -v128, v131, v130
	v_div_fmas_f32 v128, v128, v129, v131
	v_div_fixup_f32 v128, v128, v75, 1.0
	v_pk_mul_f32 v[82:83], v[82:83], v[128:129] op_sel_hi:[1,0]
	v_pk_mul_f32 v[80:81], v[80:81], v[128:129] op_sel_hi:[1,0]
	v_pk_mul_f32 v[112:113], v[112:113], v[128:129] op_sel_hi:[1,0]
	v_pk_mul_f32 v[90:91], v[90:91], v[128:129] op_sel_hi:[1,0]
	v_pk_mul_f32 v[86:87], v[86:87], v[128:129] op_sel_hi:[1,0]
	s_waitcnt lgkmcnt(7)
	v_pk_fma_f32 v[2:3], v[2:3], v[82:83], v[34:35]
	v_pk_fma_f32 v[4:5], v[4:5], v[80:81], v[36:37]
	s_waitcnt lgkmcnt(6)
	v_pk_fma_f32 v[6:7], v[6:7], v[112:113], v[38:39]
	v_mov_b32_e32 v36, 0
	v_mov_b32_e32 v37, 0
	v_pk_mul_f32 v[84:85], v[84:85], v[128:129] op_sel_hi:[1,0]
	v_pk_mul_f32 v[110:111], v[110:111], v[128:129] op_sel_hi:[1,0]
	v_pk_mul_f32 v[116:117], v[116:117], v[128:129] op_sel_hi:[1,0]
	s_waitcnt lgkmcnt(5)
	v_pk_fma_f32 v[10:11], v[10:11], v[90:91], v[42:43]
	s_waitcnt lgkmcnt(4)
	v_pk_fma_f32 v[14:15], v[14:15], v[86:87], v[46:47]
	v_cvt_pk_fp8_f32 v36, v2, v3
	v_cvt_pk_fp8_f32 v37, v6, v7
	v_mov_b32_e32 v38, 0
	v_mov_b32_e32 v39, 0
	v_pk_mul_f32 v[120:121], v[120:121], v[128:129] op_sel_hi:[1,0]
	v_pk_mul_f32 v[124:125], v[124:125], v[128:129] op_sel_hi:[1,0]
	v_pk_fma_f32 v[8:9], v[8:9], v[84:85], v[40:41]
	s_waitcnt lgkmcnt(3)
	v_pk_fma_f32 v[18:19], v[18:19], v[110:111], v[50:51]
	s_waitcnt lgkmcnt(2)
	v_pk_fma_f32 v[22:23], v[116:117], v[22:23], v[54:55]
	v_cvt_pk_fp8_f32 v38, v10, v11
	v_cvt_pk_fp8_f32 v39, v14, v15
	v_mov_b32_e32 v40, 0
	v_mov_b32_e32 v41, 0
	s_waitcnt lgkmcnt(1)
	v_pk_fma_f32 v[26:27], v[120:121], v[26:27], v[58:59]
	s_waitcnt lgkmcnt(0)
	v_pk_fma_f32 v[30:31], v[124:125], v[30:31], v[76:77]
	v_cvt_pk_fp8_f32 v40, v18, v19
	v_cvt_pk_fp8_f32 v41, v22, v23
	v_mov_b32_e32 v42, 0
	v_mov_b32_e32 v43, 0
	v_pk_mul_f32 v[88:89], v[88:89], v[128:129] op_sel_hi:[1,0]
	v_pk_mul_f32 v[92:93], v[92:93], v[128:129] op_sel_hi:[1,0]
	v_cvt_pk_fp8_f32 v42, v26, v27
	v_cvt_pk_fp8_f32 v43, v30, v31
	v_pk_mul_f32 v[114:115], v[114:115], v[128:129] op_sel_hi:[1,0]
	v_pk_mul_f32 v[118:119], v[118:119], v[128:129] op_sel_hi:[1,0]
	v_pk_fma_f32 v[12:13], v[12:13], v[88:89], v[44:45]
	v_pk_fma_f32 v[16:17], v[16:17], v[92:93], v[48:49]
	v_cvt_pk_fp8_f32 v36, v4, v5 op_sel:[0,0,1]
	v_cvt_pk_fp8_f32 v37, v8, v9 op_sel:[0,0,1]
	v_pk_mul_f32 v[122:123], v[122:123], v[128:129] op_sel_hi:[1,0]
	v_pk_mul_f32 v[126:127], v[126:127], v[128:129] op_sel_hi:[1,0]
	v_pk_fma_f32 v[20:21], v[20:21], v[114:115], v[52:53]
	v_pk_fma_f32 v[24:25], v[118:119], v[24:25], v[56:57]
	v_cvt_pk_fp8_f32 v38, v12, v13 op_sel:[0,0,1]
	v_cvt_pk_fp8_f32 v39, v16, v17 op_sel:[0,0,1]
	v_pk_fma_f32 v[28:29], v[122:123], v[28:29], v[60:61]
	v_pk_fma_f32 v[32:33], v[126:127], v[32:33], v[78:79]
	v_cvt_pk_fp8_f32 v40, v20, v21 op_sel:[0,0,1]
	v_cvt_pk_fp8_f32 v41, v24, v25 op_sel:[0,0,1]
	v_lshl_add_u64 v[34:35], v[68:69], 0, s[26:27]
	v_cvt_pk_fp8_f32 v42, v28, v29 op_sel:[0,0,1]
	v_cvt_pk_fp8_f32 v43, v32, v33 op_sel:[0,0,1]
	global_store_dwordx2 v[34:35], v[36:37], off
	global_store_dwordx2 v[34:35], v[38:39], off offset:512
	global_store_dwordx2 v[34:35], v[40:41], off offset:1024
	global_store_dwordx2 v[34:35], v[42:43], off offset:1536
	v_add_u32_e32 v34, s15, v1
	v_mov_b32_e32 v84, v101
	v_mov_b64_e32 v[58:59], v[70:71]
	v_mov_b32_e32 v75, v74
	v_mov_b32_e32 v38, v74
	v_mov_b32_e32 v39, v74
	v_mov_b32_e32 v40, v74
	v_mov_b32_e32 v41, v74
	v_mov_b32_e32 v42, v74
	v_mov_b32_e32 v43, v74
	v_mov_b32_e32 v44, v74
	v_mov_b32_e32 v45, v74
	v_mov_b32_e32 v46, v74
	v_mov_b32_e32 v47, v74
	v_mov_b32_e32 v48, v74
	v_mov_b32_e32 v49, v74
	v_mov_b32_e32 v50, v74
	v_mov_b32_e32 v51, v74
	v_mov_b32_e32 v52, v74
	v_mov_b32_e32 v53, v74
	v_mov_b32_e32 v54, v74
	v_mov_b32_e32 v55, v74
	v_mov_b32_e32 v56, v74
	v_mov_b32_e32 v57, v74
	v_mov_b32_e32 v60, v74
	v_mov_b32_e32 v61, v74
	v_mov_b32_e32 v76, v74
	v_mov_b32_e32 v77, v74
	v_mov_b32_e32 v78, v74
	v_mov_b32_e32 v79, v74
	v_mov_b32_e32 v80, v74
	v_mov_b32_e32 v81, v74
	v_mov_b32_e32 v82, v74
	v_mov_b32_e32 v83, v74
	ds_write_b128 v34, v[2:5]
	ds_write_b128 v34, v[6:9] offset:16
	ds_write_b128 v34, v[10:13] offset:2048
	ds_write_b128 v34, v[14:17] offset:2064
	ds_write_b128 v34, v[18:21] offset:4096
	ds_write_b128 v34, v[22:25] offset:4112
	ds_write_b128 v34, v[26:29] offset:6144
	ds_write_b128 v34, v[30:33] offset:6160
	s_waitcnt lgkmcnt(0)
	s_barrier

; __global__ void __launch_bounds__(512, 2) fwd_kernel(Args args) {
	.amdhsa_kernel _Z10fwd_kernel4Args
		.amdhsa_group_segment_fixed_size 0
		.amdhsa_private_segment_fixed_size 0
		.amdhsa_kernarg_size 560
		.amdhsa_user_sgpr_count 2
		.amdhsa_user_sgpr_dispatch_ptr 0
		.amdhsa_user_sgpr_queue_ptr 0
		.amdhsa_user_sgpr_kernarg_segment_ptr 1
		.amdhsa_user_sgpr_dispatch_id 0
		.amdhsa_user_sgpr_kernarg_preload_length 0
		.amdhsa_user_sgpr_kernarg_preload_offset 0
		.amdhsa_user_sgpr_private_segment_size 0
		.amdhsa_uses_dynamic_stack 0
		.amdhsa_enable_private_segment 0
		.amdhsa_system_sgpr_workgroup_id_x 1
		.amdhsa_system_sgpr_workgroup_id_y 0
		.amdhsa_system_sgpr_workgroup_id_z 0
		.amdhsa_system_sgpr_workgroup_info 0
		.amdhsa_system_vgpr_workitem_id 0
		.amdhsa_next_free_vgpr 252
		.amdhsa_next_free_sgpr 98
		.amdhsa_accum_offset 252
		.amdhsa_reserve_vcc 1
		.amdhsa_float_round_mode_32 0
		.amdhsa_float_round_mode_16_64 0
		.amdhsa_float_denorm_mode_32 3
		.amdhsa_float_denorm_mode_16_64 3
		.amdhsa_dx10_clamp 1
		.amdhsa_ieee_mode 1
		.amdhsa_fp16_overflow 0
		.amdhsa_tg_split 0
		.amdhsa_exception_fp_ieee_invalid_op 0
		.amdhsa_exception_fp_denorm_src 0
		.amdhsa_exception_fp_ieee_div_zero 0
		.amdhsa_exception_fp_ieee_overflow 0
		.amdhsa_exception_fp_ieee_underflow 0
		.amdhsa_exception_fp_ieee_inexact 0
		.amdhsa_exception_int_div_zero 0
	.end_amdhsa_kernel

; __global__ void __launch_bounds__(512, 2) fwd_kernel(Args args) {
amdhsa.kernels:
  - .agpr_count:     0
    .args:
      - .offset:         0
        .size:           304
        .value_kind:     by_value
      - .offset:         304
        .size:           4
        .value_kind:     hidden_block_count_x
      - .offset:         308
        .size:           4
        .value_kind:     hidden_block_count_y
      - .offset:         312
        .size:           4
        .value_kind:     hidden_block_count_z
      - .offset:         316
        .size:           2
        .value_kind:     hidden_group_size_x
      - .offset:         318
        .size:           2
        .value_kind:     hidden_group_size_y
      - .offset:         320
        .size:           2
        .value_kind:     hidden_group_size_z
      - .offset:         322
        .size:           2
        .value_kind:     hidden_remainder_x
      - .offset:         324
        .size:           2
        .value_kind:     hidden_remainder_y
      - .offset:         326
        .size:           2
        .value_kind:     hidden_remainder_z
      - .offset:         344
        .size:           8
        .value_kind:     hidden_global_offset_x
      - .offset:         352
        .size:           8
        .value_kind:     hidden_global_offset_y
      - .offset:         360
        .size:           8
        .value_kind:     hidden_global_offset_z
      - .offset:         368
        .size:           2
        .value_kind:     hidden_grid_dims
      - .offset:         424
        .size:           4
        .value_kind:     hidden_dynamic_lds_size
    .group_segment_fixed_size: 0
    .kernarg_segment_align: 8
    .kernarg_segment_size: 560
    .language:       OpenCL C
    .language_version:
      - 2
      - 0
    .max_flat_workgroup_size: 512
    .name:           _Z10fwd_kernel4Args
    .private_segment_fixed_size: 0
    .sgpr_count:     104
    .sgpr_spill_count: 12
    .symbol:         _Z10fwd_kernel4Args.kd
    .uniform_work_group_size: 1
    .uses_dynamic_stack: false
    .vgpr_count:     252
    .vgpr_spill_count: 0
    .wavefront_size: 64
